# v30 + every global store write-through (sc1) and the grid barrier's L2 write-back (buffer_wbl2) dropped
# speedup vs baseline: 1.0139x; 1.0125x over previous
; __device__ __forceinline__ void prologue(const Ctx& C, const In& I, unsigned char* ws, bf16* hs0) {
;     ...
;     float* lut = (float*)(ws + WS_LUT);
;     for (int e = C.gw * 64 + C.lane; e < 16 * 132; e += C.ngw * 64) { const int h = e / 132, rel = e % 132; lut[e] = I.rel_bias[t5_bucket(rel > 128 ? 128 : rel) * 16 + h] * LOG2E; }
.LBB0_74:
	s_or_b64 exec, exec, s[12:13]
	v_lshl_add_u32 v4, v4, 4, v3
	v_readlane_b32 s36, v253, 0
	v_ashrrev_i32_e32 v5, 31, v4
	v_readlane_b32 s46, v253, 10
	v_readlane_b32 s47, v253, 11
	v_ashrrev_i32_e32 v3, 31, v2
	v_readlane_b32 s37, v253, 1
	v_lshl_add_u64 v[4:5], v[4:5], 2, s[46:47]
	global_load_dword v6, v[4:5], off
	v_lshl_add_u64 v[4:5], v[2:3], 2, s[8:9]
	v_add_u32_e32 v2, s14, v2
	v_cmp_lt_i32_e32 vcc, s26, v2
	s_or_b64 s[10:11], vcc, s[10:11]
	v_readlane_b32 s38, v253, 2
	v_readlane_b32 s39, v253, 3
	v_readlane_b32 s40, v253, 4
	v_readlane_b32 s41, v253, 5
	v_readlane_b32 s42, v253, 6
	v_readlane_b32 s43, v253, 7
	v_readlane_b32 s44, v253, 8
	v_readlane_b32 s45, v253, 9
	v_readlane_b32 s48, v253, 12
	v_readlane_b32 s49, v253, 13
	v_readlane_b32 s50, v253, 14
	v_readlane_b32 s51, v253, 15
	s_waitcnt vmcnt(0)
	v_mul_f32_e32 v3, 0x3fb8aa3b, v6
	flat_store_dword v[4:5], v3 sc1
	s_andn2_b64 exec, exec, s[10:11]
	s_cbranch_execz .LBB0_77

; __device__ __forceinline__ void prologue(const Ctx& C, const In& I, unsigned char* ws, bf16* hs0) {
;     ...
;     for (int w = C.ngw - 1 - C.gw; w < 256; w += C.ngw) {
;         const int e0 = 4 * w, jk = e0 >> 8, col = (e0 & 255) + (C.lane & 3), ks = C.lane >> 2;
;         const float* pe = I.nsa_pe + (size_t)jk * 2048 + 128 * ks; const float* w1 = I.nsa_w1 + (size_t)jk * 2048 * 256 + (size_t)(128 * ks) * 256 + col; float sacc = 0.f;
; #pragma unroll 8
;         for (int i = 0; i < 128; ++i) sacc += pe[i] * w1[(size_t)i * 256];
;         sacc += __shfl_xor(sacc, 4); sacc += __shfl_xor(sacc, 8); sacc += __shfl_xor(sacc, 16); sacc += __shfl_xor(sacc, 32);
;         if (C.lane < 4) b1f[e0 + C.lane] = sacc + I.nsa_b1[e0 + C.lane];
;     }
.LBB0_81:
	v_lshl_add_u64 v[20:21], v[6:7], 0, s[12:13]
	global_load_dwordx4 v[16:19], v[20:21], off offset:16
	s_nop 0
	global_load_dwordx4 v[20:23], v[20:21], off
	v_add_co_u32_e32 v24, vcc, 0xfffff000, v8
	s_add_u32 s12, s12, 32
	s_nop 0
	v_addc_co_u32_e32 v25, vcc, -1, v9, vcc
	global_load_dword v26, v[24:25], off offset:-3072
	global_load_dword v27, v[24:25], off offset:-2048
	s_nop 0
	global_load_dword v24, v[24:25], off offset:-1024
	s_nop 0
	global_load_dword v25, v[8:9], off offset:-4096
	global_load_dword v28, v[8:9], off offset:-3072
	global_load_dword v29, v[8:9], off offset:-2048
	global_load_dword v30, v[8:9], off offset:-1024
	global_load_dword v31, v[8:9], off
	s_addc_u32 s13, s13, 0
	v_lshl_add_u64 v[8:9], v[8:9], 0, s[10:11]
	s_cmpk_eq_i32 s12, 0x200
	s_waitcnt vmcnt(0)
	v_fmac_f32_e32 v15, v20, v26
	v_fmac_f32_e32 v15, v21, v27
	v_fmac_f32_e32 v15, v22, v24
	v_fmac_f32_e32 v15, v23, v25
	v_fmac_f32_e32 v15, v16, v28
	v_fmac_f32_e32 v15, v17, v29
	v_fmac_f32_e32 v15, v18, v30
	v_fmac_f32_e32 v15, v19, v31
	s_cbranch_scc0 .LBB0_81
	ds_bpermute_b32 v6, v11, v15
	s_waitcnt lgkmcnt(0)
	v_add_f32_e32 v6, v15, v6
	ds_bpermute_b32 v7, v12, v6
	s_waitcnt lgkmcnt(0)
	v_add_f32_e32 v6, v6, v7
	ds_bpermute_b32 v7, v13, v6
	s_waitcnt lgkmcnt(0)
	v_add_f32_e32 v6, v6, v7
	ds_bpermute_b32 v7, v14, v6
	s_and_saveexec_b64 s[12:13], s[0:1]
	s_cbranch_execz .LBB0_79
	v_lshl_or_b32 v8, s14, 2, v1
	v_ashrrev_i32_e32 v9, 31, v8
	v_readlane_b32 s36, v253, 16
	v_lshlrev_b64 v[8:9], 2, v[8:9]
	v_readlane_b32 s38, v253, 18
	v_readlane_b32 s39, v253, 19
	s_waitcnt lgkmcnt(0)
	v_add_f32_e32 v6, v6, v7
	v_readlane_b32 s37, v253, 17
	v_lshl_add_u64 v[16:17], s[38:39], 0, v[8:9]
	global_load_dword v15, v[16:17], off
	v_lshl_add_u64 v[8:9], s[8:9], 0, v[8:9]
	v_readlane_b32 s40, v253, 20
	v_readlane_b32 s41, v253, 21
	v_readlane_b32 s42, v253, 22
	v_readlane_b32 s43, v253, 23
	v_readlane_b32 s44, v253, 24
	v_readlane_b32 s45, v253, 25
	v_readlane_b32 s46, v253, 26
	v_readlane_b32 s47, v253, 27
	v_readlane_b32 s48, v253, 28
	v_readlane_b32 s49, v253, 29
	v_readlane_b32 s50, v253, 30
	v_readlane_b32 s51, v253, 31
	s_waitcnt vmcnt(0)
	v_add_f32_e32 v6, v6, v15
	flat_store_dword v[8:9], v6 sc1
	s_branch .LBB0_79

; __device__ __forceinline__ unsigned pk2(float lo, float hi) { unsigned r; asm("v_cvt_pk_bf16_f32 %0, %1, %2" : "=v"(r) : "v"(lo), "v"(hi)); return r; }
; __device__ __forceinline__ void first_norm_row(const float* xrow, const float* g, bf16* urow, bf16* hrow, int lane) {
;     const f32x4* xp = (const f32x4*)xrow; const f32x4* gp = (const f32x4*)g;
;     f32x4 v[4] = {xp[2 * lane], xp[2 * lane + 1], xp[128 + 2 * lane], xp[128 + 2 * lane + 1]};
;     float ss = 0.f;
; #pragma unroll
;     for (int i = 0; i < 4; ++i) ss += (v[i][0] * v[i][0] + v[i][1] * v[i][1]) + (v[i][2] * v[i][2] + v[i][3] * v[i][3]);
;     const float r = 1.0f / sqrtf(wave_sum(ss) * (1.0f / D) + RMS_EPS);
;     { v4u h0, h1; h0.x = pk2(v[0][0], v[0][1]); h0.y = pk2(v[0][2], v[0][3]); h0.z = pk2(v[1][0], v[1][1]); h0.w = pk2(v[1][2], v[1][3]);
;       h1.x = pk2(v[2][0], v[2][1]); h1.y = pk2(v[2][2], v[2][3]); h1.z = pk2(v[3][0], v[3][1]); h1.w = pk2(v[3][2], v[3][3]);
;       ((v4u*)hrow)[lane] = h0; ((v4u*)hrow)[64 + lane] = h1; }
;     const f32x4 g4[4] = {gp[2 * lane], gp[2 * lane + 1], gp[128 + 2 * lane], gp[128 + 2 * lane + 1]};
; #pragma unroll
;     for (int i = 0; i < 4; ++i) v[i] = v[i] * r * g4[i];
;     v4u o0, o1; o0.x = pk2(v[0][0], v[0][1]); o0.y = pk2(v[0][2], v[0][3]); o0.z = pk2(v[1][0], v[1][1]); o0.w = pk2(v[1][2], v[1][3]);
;     o1.x = pk2(v[2][0], v[2][1]); o1.y = pk2(v[2][2], v[2][3]); o1.z = pk2(v[3][0], v[3][1]); o1.w = pk2(v[3][2], v[3][3]);
;     ((v4u*)urow)[lane] = o0; ((v4u*)urow)[64 + lane] = o1;
; }
; __device__ __forceinline__ void prologue(const Ctx& C, const In& I, unsigned char* ws, bf16* hs0) {
;     ...
;     else for (int m = C.gw; m < M; m += C.ngw) first_norm_row(I.x + (size_t)m * D, I.norm_g, U + (size_t)m * D, hs0 + (size_t)m * D, C.lane);
.LBB0_87:
	s_waitcnt lgkmcnt(0)
	global_load_dwordx4 v[6:9], v[22:23], off
	global_load_dwordx4 v[2:5], v[22:23], off offset:16
	global_load_dwordx4 v[10:13], v[22:23], off offset:2064
	global_load_dwordx4 v[14:17], v[22:23], off offset:2048
	v_lshl_add_u64 v[26:27], s[10:11], 0, v[20:21]
	v_add_co_u32_e32 v34, vcc, s14, v26
	s_add_i32 s20, s20, s4
	s_nop 0
	v_addc_co_u32_e32 v35, vcc, 0, v27, vcc
	v_lshl_add_u64 v[42:43], s[6:7], 0, v[20:21]
	s_add_u32 s6, s6, s8
	s_addc_u32 s7, s7, s9
	s_add_u32 s10, s10, s8
	s_addc_u32 s11, s11, s9
	v_lshl_add_u64 v[22:23], v[22:23], 0, s[12:13]
	s_cmpk_lt_i32 s20, 0x4000
	s_waitcnt vmcnt(0)
	v_cvt_pk_bf16_f32 v26, v6, v7
	v_cvt_pk_bf16_f32 v27, v8, v9
	v_cvt_pk_bf16_f32 v28, v2, v3
	v_cvt_pk_bf16_f32 v29, v4, v5
	v_pk_mul_f32 v[36:37], v[8:9], v[8:9]
	v_pk_mul_f32 v[44:45], v[6:7], v[6:7]
	v_pk_mul_f32 v[38:39], v[4:5], v[4:5]
	v_pk_mul_f32 v[46:47], v[2:3], v[2:3]
	v_mul_f32_e32 v40, v15, v15
	v_cvt_pk_bf16_f32 v30, v14, v15
	v_cvt_pk_bf16_f32 v31, v16, v17
	v_cvt_pk_bf16_f32 v32, v10, v11
	v_cvt_pk_bf16_f32 v33, v12, v13
	global_store_dwordx4 v[34:35], v[26:29], off sc1
	global_store_dwordx4 v[34:35], v[30:33], off offset:1024 sc1
	v_pk_mov_b32 v[50:51], v[44:45], v[36:37] op_sel:[1,0]
	v_mov_b32_e32 v45, v37
	v_pk_mov_b32 v[52:53], v[46:47], v[38:39] op_sel:[1,0]
	v_mov_b32_e32 v47, v39
	v_pk_fma_f32 v[54:55], v[14:15], v[14:15], v[40:41] op_sel_hi:[1,1,0]
	global_load_dwordx4 v[26:29], v[18:19], off
	global_load_dwordx4 v[30:33], v[18:19], off offset:16
	global_load_dwordx4 v[34:37], v[18:19], off offset:2048
	global_load_dwordx4 v[38:41], v[18:19], off offset:2064
	v_mul_f32_e32 v48, v17, v17
	v_pk_add_f32 v[44:45], v[50:51], v[44:45]
	v_pk_add_f32 v[46:47], v[52:53], v[46:47]
	v_mul_f32_e32 v56, v10, v10
	v_mul_f32_e32 v57, v11, v11
	v_mul_f32_e32 v58, v12, v12
	v_mul_f32_e32 v59, v13, v13
	v_pk_fma_f32 v[48:49], v[16:17], v[16:17], v[48:49] op_sel_hi:[1,1,0]
	v_pk_add_f32 v[44:45], v[44:45], v[44:45] op_sel:[0,1] op_sel_hi:[1,0]
	v_pk_add_f32 v[46:47], v[46:47], v[46:47] op_sel:[0,1] op_sel_hi:[1,0]
	v_mov_b32_e32 v55, v58
	v_mov_b32_e32 v49, v59
	v_mov_b32_e32 v45, v56
	v_mov_b32_e32 v47, v57
	v_pk_add_f32 v[48:49], v[54:55], v[48:49]
	v_pk_add_f32 v[44:45], v[44:45], v[46:47]
	s_nop 0
	v_pk_add_f32 v[44:45], v[44:45], v[48:49]
	s_nop 0
	v_add_f32_e32 v44, v44, v45
	s_nop 1
	v_add_f32_dpp v44, v44, v44 quad_perm:[1,0,3,2] row_mask:0xf bank_mask:0xf bound_ctrl:1
	s_nop 1
	v_add_f32_dpp v44, v44, v44 quad_perm:[2,3,0,1] row_mask:0xf bank_mask:0xf bound_ctrl:1
	s_nop 1
	v_add_f32_dpp v44, v44, v44 row_half_mirror row_mask:0xf bank_mask:0xf bound_ctrl:1
	s_nop 1
	v_add_f32_dpp v44, v44, v44 row_mirror row_mask:0xf bank_mask:0xf bound_ctrl:1
	s_nop 0
	v_readlane_b32 s16, v44, 16
	v_readlane_b32 s17, v44, 48
	v_readlane_b32 s0, v44, 0
	v_readlane_b32 s1, v44, 32
	v_mov_b32_e32 v44, s16
	v_mov_b32_e32 v45, s17
	v_pk_add_f32 v[44:45], s[0:1], v[44:45]
	s_nop 0
	v_add_f32_e32 v44, v44, v45
	v_fmamk_f32 v44, v44, 0x3a800000, v24
	v_mul_f32_e32 v45, 0x4f800000, v44
	v_cmp_gt_f32_e32 vcc, s5, v44
	s_nop 1
	v_cndmask_b32_e32 v44, v44, v45, vcc
	v_sqrt_f32_e32 v45, v44
	s_nop 0
	v_add_u32_e32 v46, -1, v45
	v_add_u32_e32 v47, 1, v45
	v_fma_f32 v48, -v46, v45, v44
	v_fma_f32 v49, -v47, v45, v44
	v_cmp_ge_f32_e64 s[0:1], 0, v48
	s_nop 1
	v_cndmask_b32_e64 v45, v45, v46, s[0:1]
	v_cmp_lt_f32_e64 s[0:1], 0, v49
	s_nop 1
	v_cndmask_b32_e64 v45, v45, v47, s[0:1]
	v_mul_f32_e32 v46, 0x37800000, v45
	v_cndmask_b32_e32 v45, v45, v46, vcc
	v_cmp_class_f32_e32 vcc, v44, v25
	s_nop 1
	v_cndmask_b32_e32 v44, v45, v44, vcc
	v_div_scale_f32 v45, s[0:1], v44, v44, 1.0
	v_rcp_f32_e32 v47, v45
	v_div_scale_f32 v46, vcc, 1.0, v44, 1.0
	v_fma_f32 v48, -v45, v47, 1.0
	v_fmac_f32_e32 v47, v48, v47
	v_mul_f32_e32 v48, v46, v47
	v_fma_f32 v49, -v45, v48, v46
	v_fmac_f32_e32 v48, v49, v47
	v_fma_f32 v45, -v45, v48, v46
	v_div_fmas_f32 v45, v45, v47, v48
	v_div_fixup_f32 v44, v45, v44, 1.0
	v_pk_mul_f32 v[6:7], v[6:7], v[44:45] op_sel_hi:[1,0]
	v_pk_mul_f32 v[2:3], v[2:3], v[44:45] op_sel_hi:[1,0]
	v_pk_mul_f32 v[4:5], v[4:5], v[44:45] op_sel_hi:[1,0]
	v_add_co_u32_e32 v42, vcc, s15, v42
	v_pk_mul_f32 v[8:9], v[8:9], v[44:45] op_sel_hi:[1,0]
	s_waitcnt vmcnt(3)
	v_pk_mul_f32 v[6:7], v[6:7], v[26:27]
	s_waitcnt vmcnt(2)
	v_pk_mul_f32 v[26:27], v[4:5], v[32:33]
	v_pk_mul_f32 v[4:5], v[2:3], v[30:31]
	v_addc_co_u32_e32 v43, vcc, 0, v43, vcc
	v_pk_mul_f32 v[14:15], v[14:15], v[44:45] op_sel_hi:[1,0]
	v_pk_mul_f32 v[16:17], v[16:17], v[44:45] op_sel_hi:[1,0]
	v_pk_mul_f32 v[10:11], v[10:11], v[44:45] op_sel_hi:[1,0]
	v_pk_mul_f32 v[12:13], v[12:13], v[44:45] op_sel_hi:[1,0]
	v_pk_mul_f32 v[8:9], v[8:9], v[28:29]
	v_cvt_pk_bf16_f32 v2, v6, v7
	v_cvt_pk_bf16_f32 v4, v4, v5
	v_cvt_pk_bf16_f32 v5, v26, v27
	s_waitcnt vmcnt(1)
	v_pk_mul_f32 v[16:17], v[16:17], v[36:37]
	v_cvt_pk_bf16_f32 v3, v8, v9
	v_pk_mul_f32 v[14:15], v[14:15], v[34:35]
	s_waitcnt vmcnt(0)
	v_pk_mul_f32 v[12:13], v[12:13], v[40:41]
	v_pk_mul_f32 v[10:11], v[10:11], v[38:39]
	v_cvt_pk_bf16_f32 v6, v14, v15
	v_cvt_pk_bf16_f32 v7, v16, v17
	v_cvt_pk_bf16_f32 v9, v12, v13
	s_nop 0
	v_cvt_pk_bf16_f32 v8, v10, v11
	flat_store_dwordx4 v[42:43], v[2:5] sc1
	flat_store_dwordx4 v[42:43], v[6:9] offset:1024 sc1
	s_cbranch_scc1 .LBB0_87

; __device__ __forceinline__ unsigned pk2(float lo, float hi) { unsigned r; asm("v_cvt_pk_bf16_f32 %0, %1, %2" : "=v"(r) : "v"(lo), "v"(hi)); return r; }
; __device__ __forceinline__ void first_norm_row(const float* xrow, const float* g, bf16* urow, bf16* hrow, int lane) {
;     const f32x4* xp = (const f32x4*)xrow; const f32x4* gp = (const f32x4*)g;
;     f32x4 v[4] = {xp[2 * lane], xp[2 * lane + 1], xp[128 + 2 * lane], xp[128 + 2 * lane + 1]};
;     float ss = 0.f;
; #pragma unroll
;     for (int i = 0; i < 4; ++i) ss += (v[i][0] * v[i][0] + v[i][1] * v[i][1]) + (v[i][2] * v[i][2] + v[i][3] * v[i][3]);
;     const float r = 1.0f / sqrtf(wave_sum(ss) * (1.0f / D) + RMS_EPS);
;     { v4u h0, h1; h0.x = pk2(v[0][0], v[0][1]); h0.y = pk2(v[0][2], v[0][3]); h0.z = pk2(v[1][0], v[1][1]); h0.w = pk2(v[1][2], v[1][3]);
;       h1.x = pk2(v[2][0], v[2][1]); h1.y = pk2(v[2][2], v[2][3]); h1.z = pk2(v[3][0], v[3][1]); h1.w = pk2(v[3][2], v[3][3]);
;       ((v4u*)hrow)[lane] = h0; ((v4u*)hrow)[64 + lane] = h1; }
;     const f32x4 g4[4] = {gp[2 * lane], gp[2 * lane + 1], gp[128 + 2 * lane], gp[128 + 2 * lane + 1]};
; #pragma unroll
;     for (int i = 0; i < 4; ++i) v[i] = v[i] * r * g4[i];
;     v4u o0, o1; o0.x = pk2(v[0][0], v[0][1]); o0.y = pk2(v[0][2], v[0][3]); o0.z = pk2(v[1][0], v[1][1]); o0.w = pk2(v[1][2], v[1][3]);
;     o1.x = pk2(v[2][0], v[2][1]); o1.y = pk2(v[2][2], v[2][3]); o1.z = pk2(v[3][0], v[3][1]); o1.w = pk2(v[3][2], v[3][3]);
;     ((v4u*)urow)[lane] = o0; ((v4u*)urow)[64 + lane] = o1;
; }
; __device__ __forceinline__ void prologue(const Ctx& C, const In& I, unsigned char* ws, bf16* hs0) {
;     ...
;     if (C.G == 256) { const int mb = 2048 * (C.bx & 7) + 64 * (C.bx >> 3) + 8 * C.wave;
;         for (int m = mb; m < mb + 8; ++m) first_norm_row(I.x + (size_t)m * D, I.norm_g, U + (size_t)m * D, hs0 + (size_t)m * D, C.lane); }
.LBB0_91:
	s_waitcnt lgkmcnt(0)
	global_load_dwordx4 v[6:9], v[22:23], off
	global_load_dwordx4 v[2:5], v[22:23], off offset:16
	global_load_dwordx4 v[10:13], v[22:23], off offset:2064
	global_load_dwordx4 v[14:17], v[22:23], off offset:2048
	v_lshl_add_u64 v[26:27], s[4:5], 0, v[20:21]
	v_add_co_u32_e32 v34, vcc, s11, v26
	s_add_i32 s9, s9, 1
	s_nop 0
	v_addc_co_u32_e32 v35, vcc, 0, v27, vcc
	v_lshl_add_u64 v[42:43], s[2:3], 0, v[20:21]
	s_add_u32 s2, s2, 0x800
	s_addc_u32 s3, s3, 0
	s_add_u32 s4, s4, 0x800
	s_addc_u32 s5, s5, 0
	v_lshl_add_u64 v[22:23], v[22:23], 0, s[6:7]
	s_cmp_ge_i32 s9, s8
	s_waitcnt vmcnt(0)
	v_cvt_pk_bf16_f32 v26, v6, v7
	v_cvt_pk_bf16_f32 v27, v8, v9
	v_cvt_pk_bf16_f32 v28, v2, v3
	v_cvt_pk_bf16_f32 v29, v4, v5
	v_pk_mul_f32 v[36:37], v[8:9], v[8:9]
	v_pk_mul_f32 v[44:45], v[6:7], v[6:7]
	v_pk_mul_f32 v[38:39], v[4:5], v[4:5]
	v_pk_mul_f32 v[46:47], v[2:3], v[2:3]
	v_mul_f32_e32 v40, v15, v15
	v_cvt_pk_bf16_f32 v30, v14, v15
	v_cvt_pk_bf16_f32 v31, v16, v17
	v_cvt_pk_bf16_f32 v32, v10, v11
	v_cvt_pk_bf16_f32 v33, v12, v13
	global_store_dwordx4 v[34:35], v[26:29], off sc1
	global_store_dwordx4 v[34:35], v[30:33], off offset:1024 sc1
	v_pk_mov_b32 v[50:51], v[44:45], v[36:37] op_sel:[1,0]
	v_mov_b32_e32 v45, v37
	v_pk_mov_b32 v[52:53], v[46:47], v[38:39] op_sel:[1,0]
	v_mov_b32_e32 v47, v39
	v_pk_fma_f32 v[54:55], v[14:15], v[14:15], v[40:41] op_sel_hi:[1,1,0]
	global_load_dwordx4 v[26:29], v[18:19], off
	global_load_dwordx4 v[30:33], v[18:19], off offset:16
	global_load_dwordx4 v[34:37], v[18:19], off offset:2048
	global_load_dwordx4 v[38:41], v[18:19], off offset:2064
	v_mul_f32_e32 v48, v17, v17
	v_pk_add_f32 v[44:45], v[50:51], v[44:45]
	v_pk_add_f32 v[46:47], v[52:53], v[46:47]
	v_mul_f32_e32 v25, v10, v10
	v_mul_f32_e32 v56, v11, v11
	v_mul_f32_e32 v57, v12, v12
	v_mul_f32_e32 v58, v13, v13
	v_pk_fma_f32 v[48:49], v[16:17], v[16:17], v[48:49] op_sel_hi:[1,1,0]
	v_pk_add_f32 v[44:45], v[44:45], v[44:45] op_sel:[0,1] op_sel_hi:[1,0]
	v_pk_add_f32 v[46:47], v[46:47], v[46:47] op_sel:[0,1] op_sel_hi:[1,0]
	v_mov_b32_e32 v55, v57
	v_mov_b32_e32 v49, v58
	v_mov_b32_e32 v45, v25
	v_mov_b32_e32 v47, v56
	v_pk_add_f32 v[48:49], v[54:55], v[48:49]
	v_pk_add_f32 v[44:45], v[44:45], v[46:47]
	s_nop 0
	v_pk_add_f32 v[44:45], v[44:45], v[48:49]
	s_nop 0
	v_add_f32_e32 v25, v44, v45
	s_nop 1
	v_add_f32_dpp v25, v25, v25 quad_perm:[1,0,3,2] row_mask:0xf bank_mask:0xf bound_ctrl:1
	s_nop 1
	v_add_f32_dpp v25, v25, v25 quad_perm:[2,3,0,1] row_mask:0xf bank_mask:0xf bound_ctrl:1
	s_nop 1
	v_add_f32_dpp v25, v25, v25 row_half_mirror row_mask:0xf bank_mask:0xf bound_ctrl:1
	s_nop 1
	v_add_f32_dpp v25, v25, v25 row_mirror row_mask:0xf bank_mask:0xf bound_ctrl:1
	s_nop 0
	v_readlane_b32 s13, v25, 16
	v_readlane_b32 s14, v25, 48
	v_readlane_b32 s0, v25, 0
	v_readlane_b32 s1, v25, 32
	v_mov_b32_e32 v44, s13
	v_mov_b32_e32 v45, s14
	v_pk_add_f32 v[44:45], s[0:1], v[44:45]
	s_nop 0
	v_add_f32_e32 v25, v44, v45
	v_fmamk_f32 v25, v25, 0x3a800000, v1
	v_mul_f32_e32 v44, 0x4f800000, v25
	v_cmp_gt_f32_e32 vcc, s10, v25
	s_nop 1
	v_cndmask_b32_e32 v25, v25, v44, vcc
	v_sqrt_f32_e32 v44, v25
	s_nop 0
	v_add_u32_e32 v45, -1, v44
	v_add_u32_e32 v46, 1, v44
	v_fma_f32 v47, -v45, v44, v25
	v_fma_f32 v48, -v46, v44, v25
	v_cmp_ge_f32_e64 s[0:1], 0, v47
	s_nop 1
	v_cndmask_b32_e64 v44, v44, v45, s[0:1]
	v_cmp_lt_f32_e64 s[0:1], 0, v48
	s_nop 1
	v_cndmask_b32_e64 v44, v44, v46, s[0:1]
	v_mul_f32_e32 v45, 0x37800000, v44
	v_cndmask_b32_e32 v44, v44, v45, vcc
	v_cmp_class_f32_e32 vcc, v25, v24
	s_nop 1
	v_cndmask_b32_e32 v25, v44, v25, vcc
	v_div_scale_f32 v44, s[0:1], v25, v25, 1.0
	v_rcp_f32_e32 v46, v44
	v_div_scale_f32 v45, vcc, 1.0, v25, 1.0
	v_fma_f32 v47, -v44, v46, 1.0
	v_fmac_f32_e32 v46, v47, v46
	v_mul_f32_e32 v47, v45, v46
	v_fma_f32 v48, -v44, v47, v45
	v_fmac_f32_e32 v47, v48, v46
	v_fma_f32 v44, -v44, v47, v45
	v_div_fmas_f32 v44, v44, v46, v47
	v_div_fixup_f32 v44, v44, v25, 1.0
	v_pk_mul_f32 v[6:7], v[6:7], v[44:45] op_sel_hi:[1,0]
	v_pk_mul_f32 v[2:3], v[2:3], v[44:45] op_sel_hi:[1,0]
	v_pk_mul_f32 v[4:5], v[4:5], v[44:45] op_sel_hi:[1,0]
	v_add_co_u32_e32 v42, vcc, s12, v42
	v_pk_mul_f32 v[8:9], v[8:9], v[44:45] op_sel_hi:[1,0]
	s_waitcnt vmcnt(3)
	v_pk_mul_f32 v[6:7], v[6:7], v[26:27]
	s_waitcnt vmcnt(2)
	v_pk_mul_f32 v[26:27], v[4:5], v[32:33]
	v_pk_mul_f32 v[4:5], v[2:3], v[30:31]
	v_addc_co_u32_e32 v43, vcc, 0, v43, vcc
	v_pk_mul_f32 v[14:15], v[14:15], v[44:45] op_sel_hi:[1,0]
	v_pk_mul_f32 v[16:17], v[16:17], v[44:45] op_sel_hi:[1,0]
	v_pk_mul_f32 v[10:11], v[10:11], v[44:45] op_sel_hi:[1,0]
	v_pk_mul_f32 v[12:13], v[12:13], v[44:45] op_sel_hi:[1,0]
	v_pk_mul_f32 v[8:9], v[8:9], v[28:29]
	v_cvt_pk_bf16_f32 v2, v6, v7
	v_cvt_pk_bf16_f32 v4, v4, v5
	v_cvt_pk_bf16_f32 v5, v26, v27
	s_waitcnt vmcnt(1)
	v_pk_mul_f32 v[16:17], v[16:17], v[36:37]
	v_cvt_pk_bf16_f32 v3, v8, v9
	v_pk_mul_f32 v[14:15], v[14:15], v[34:35]
	s_waitcnt vmcnt(0)
	v_pk_mul_f32 v[12:13], v[12:13], v[40:41]
	v_pk_mul_f32 v[10:11], v[10:11], v[38:39]
	v_cvt_pk_bf16_f32 v6, v14, v15
	v_cvt_pk_bf16_f32 v7, v16, v17
	v_cvt_pk_bf16_f32 v9, v12, v13
	s_nop 0
	v_cvt_pk_bf16_f32 v8, v10, v11
	flat_store_dwordx4 v[42:43], v[2:5] sc1
	flat_store_dwordx4 v[42:43], v[6:9] offset:1024 sc1
	s_cbranch_scc0 .LBB0_91

; __device__ __forceinline__ unsigned xb_ld(unsigned* p)              { return __hip_atomic_load(p, __ATOMIC_RELAXED, __HIP_MEMORY_SCOPE_AGENT); }
; __device__ __forceinline__ unsigned xb_add(unsigned* p, unsigned v) { return __hip_atomic_fetch_add(p, v, __ATOMIC_RELAXED, __HIP_MEMORY_SCOPE_AGENT); }
; #define XB_SPIN(cond, bar) do { unsigned _sp = 0; while (cond) { __builtin_amdgcn_s_sleep(1); \
;     if ((++_sp & 255u) == 0u) { if (xb_ld(&(bar)[XB_TMO])) break; if (_sp > XB_SPIN_CAP) { atomicAdd(&(bar)[XB_TMO], 1u); break; } } } } while (0)
; __device__ __forceinline__ void xcd_barrier(const XcdBarrier& b) {
;     ...
;         const unsigned old = xb_add(&bar[XB_XSUB(b.x)], 1u);
;         const unsigned gen = old / nloc;
;         if (old + 1u == (gen + 1u) * nloc) {
;             __builtin_amdgcn_fence(__ATOMIC_RELEASE, "agent");
;             asm volatile("s_waitcnt vmcnt(0)" ::: "memory");
;             const unsigned og = xb_add(&bar[XB_TOP], 1u);
;             const unsigned tg = og / nx;
;             if (og + 1u == (tg + 1u) * nx) xb_add(&bar[XB_TOPGEN], 1u);
;             else XB_SPIN(xb_ld(&bar[XB_TOPGEN]) == tg, bar);
.LBB0_121:
	s_andn2_saveexec_b64 s[0:1], s[0:1]
	s_cbranch_execz .LBB0_137
	v_mov_b32_e32 v1, s30
	v_add_co_u32_e32 v4, vcc, 0x3000, v1
	v_mov_b32_e32 v1, s31
	s_waitcnt vmcnt(0)
	v_addc_co_u32_e32 v5, vcc, 0, v1, vcc
	v_mov_b32_e32 v1, 1
	flat_atomic_add v1, v[4:5], v1 offset:1024 sc0
	v_cvt_f32_u32_e32 v3, v2
	v_sub_u32_e32 v4, 0, v2
	s_add_u32 s0, s30, 0x3500
	s_addc_u32 s1, s31, 0
	v_rcp_iflag_f32_e32 v3, v3
	s_mov_b64 s[4:5], -1
	v_mul_f32_e32 v3, 0x4f7ffffe, v3
	v_cvt_u32_f32_e32 v3, v3
	v_mul_lo_u32 v4, v4, v3
	v_mul_hi_u32 v4, v3, v4
	v_add_u32_e32 v3, v3, v4
	s_waitcnt vmcnt(0) lgkmcnt(0)
	v_mul_hi_u32 v3, v1, v3
	v_mul_lo_u32 v5, v3, v2
	v_add_u32_e32 v4, 1, v1
	v_sub_u32_e32 v1, v1, v5
	v_add_u32_e32 v6, 1, v3
	v_cmp_ge_u32_e32 vcc, v1, v2
	v_sub_u32_e32 v5, v1, v2
	s_nop 0
	v_cndmask_b32_e32 v3, v3, v6, vcc
	v_cndmask_b32_e32 v1, v1, v5, vcc
	v_add_u32_e32 v5, 1, v3
	v_cmp_ge_u32_e32 vcc, v1, v2
	s_nop 1
	v_cndmask_b32_e32 v1, v3, v5, vcc
	v_mad_u64_u32 v[2:3], s[2:3], v2, v1, v[2:3]
	v_cmp_ne_u32_e32 vcc, v4, v2
	v_mov_b64_e32 v[2:3], s[0:1]
	s_and_saveexec_b64 s[2:3], vcc
	s_cbranch_execz .LBB0_134
	v_mov_b64_e32 v[2:3], s[0:1]
	flat_load_dword v2, v[2:3] sc1
	s_mov_b64 s[8:9], 0
	s_waitcnt vmcnt(0) lgkmcnt(0)
	v_cmp_eq_u32_e32 vcc, v2, v1
	s_and_saveexec_b64 s[6:7], vcc
	s_cbranch_execz .LBB0_133
	s_add_u32 s4, s30, 0x200
	s_addc_u32 s5, s31, 0
	s_mov_b32 s21, 1
	s_branch .LBB0_126

; __device__ __forceinline__ unsigned xb_ld(unsigned* p)              { return __hip_atomic_load(p, __ATOMIC_RELAXED, __HIP_MEMORY_SCOPE_AGENT); }
; __device__ __forceinline__ unsigned xb_add(unsigned* p, unsigned v) { return __hip_atomic_fetch_add(p, v, __ATOMIC_RELAXED, __HIP_MEMORY_SCOPE_AGENT); }
; #define XB_SPIN(cond, bar) do { unsigned _sp = 0; while (cond) { __builtin_amdgcn_s_sleep(1); \
;     if ((++_sp & 255u) == 0u) { if (xb_ld(&(bar)[XB_TMO])) break; if (_sp > XB_SPIN_CAP) { atomicAdd(&(bar)[XB_TMO], 1u); break; } } } } while (0)
; __device__ __forceinline__ void xcd_barrier(const XcdBarrier& b) {
;     ...
;         const unsigned old = xb_add(&bar[XB_XSUB(b.x)], 1u);
;         const unsigned gen = old / nloc;
;         if (old + 1u == (gen + 1u) * nloc) {
;             __builtin_amdgcn_fence(__ATOMIC_RELEASE, "agent");
;             asm volatile("s_waitcnt vmcnt(0)" ::: "memory");
;             const unsigned og = xb_add(&bar[XB_TOP], 1u);
;             const unsigned tg = og / nx;
;             if (og + 1u == (tg + 1u) * nx) xb_add(&bar[XB_TOPGEN], 1u);
;             else XB_SPIN(xb_ld(&bar[XB_TOPGEN]) == tg, bar);
.LBB0_628:
	s_andn2_saveexec_b64 s[2:3], s[2:3]
	s_cbranch_execz .LBB0_644
	v_mov_b32_e32 v4, s34
	v_add_co_u32_e32 v4, vcc, 0x3000, v4
	v_mov_b32_e32 v5, s35
	s_waitcnt vmcnt(0)
	v_addc_co_u32_e32 v5, vcc, 0, v5, vcc
	flat_atomic_add v4, v[4:5], v1 offset:1024 sc0
	v_cvt_f32_u32_e32 v5, v2
	v_sub_u32_e32 v6, 0, v2
	s_mov_b64 s[6:7], -1
	v_rcp_iflag_f32_e32 v5, v5
	s_nop 0
	v_mul_f32_e32 v5, 0x4f7ffffe, v5
	v_cvt_u32_f32_e32 v5, v5
	v_mul_lo_u32 v6, v6, v5
	v_mul_hi_u32 v6, v5, v6
	v_add_u32_e32 v5, v5, v6
	s_waitcnt vmcnt(0) lgkmcnt(0)
	v_mul_hi_u32 v5, v4, v5
	v_mul_lo_u32 v6, v5, v2
	v_sub_u32_e32 v6, v4, v6
	v_cmp_ge_u32_e32 vcc, v6, v2
	v_add_u32_e32 v7, 1, v5
	s_nop 0
	v_cndmask_b32_e32 v5, v5, v7, vcc
	v_sub_u32_e32 v7, v6, v2
	v_cndmask_b32_e32 v6, v6, v7, vcc
	v_cmp_ge_u32_e32 vcc, v6, v2
	v_add_u32_e32 v6, 1, v5
	v_add_u32_e32 v7, 1, v4
	v_cndmask_b32_e32 v6, v5, v6, vcc
	v_mad_u64_u32 v[4:5], s[2:3], v2, v6, v[2:3]
	s_add_u32 s2, s34, 0x3500
	s_addc_u32 s3, s35, 0
	v_cmp_ne_u32_e32 vcc, v7, v4
	v_mov_b64_e32 v[4:5], s[2:3]
	s_and_saveexec_b64 s[4:5], vcc
	s_cbranch_execz .LBB0_641
	v_mov_b64_e32 v[4:5], s[2:3]
	flat_load_dword v2, v[4:5] sc1
	s_mov_b64 s[10:11], 0
	s_waitcnt vmcnt(0) lgkmcnt(0)
	v_cmp_eq_u32_e32 vcc, v2, v6
	s_and_saveexec_b64 s[8:9], vcc
	s_cbranch_execz .LBB0_640
	s_add_u32 s6, s34, 0x200
	s_addc_u32 s7, s35, 0
	s_mov_b32 s22, 1
	s_branch .LBB0_633

; __device__ __forceinline__ void thin_pass(const Ctx& C, const bf16* hin, bf16* hout, bf16* u, float* out, const bf16* y, const float* gpost, float cmul, const float* gpre, bool last) {
;     ...
;     for (int m0 = mstart; m0 < mend; m0 += mstep) {
;         v4u yr[RB][2], hr[RB][2];
; #pragma unroll
;         for (int b = 0; b < RB; ++b) { const v4u* yp = (const v4u*)(y + (size_t)(m0 + b) * D); const v4u* hp = (const v4u*)(hin + (size_t)(m0 + b) * D);
;             yr[b][0] = yp[lane]; yr[b][1] = yp[64 + lane]; hr[b][0] = hp[lane]; hr[b][1] = hp[64 + lane]; }
; #pragma unroll
;         for (int b = 0; b < RB; ++b) {
;             const int m = m0 + b; const v4u y0 = yr[b][0], y1 = yr[b][1], h0 = hr[b][0], h1 = hr[b][1];
;             f32x4 yv[4], h[4];
;             yv[0] = (f32x4){bf_lo(y0.x), bf_hi(y0.x), bf_lo(y0.y), bf_hi(y0.y)}; yv[1] = (f32x4){bf_lo(y0.z), bf_hi(y0.z), bf_lo(y0.w), bf_hi(y0.w)};
;             yv[2] = (f32x4){bf_lo(y1.x), bf_hi(y1.x), bf_lo(y1.y), bf_hi(y1.y)}; yv[3] = (f32x4){bf_lo(y1.z), bf_hi(y1.z), bf_lo(y1.w), bf_hi(y1.w)};
;             h[0] = (f32x4){bf_lo(h0.x), bf_hi(h0.x), bf_lo(h0.y), bf_hi(h0.y)}; h[1] = (f32x4){bf_lo(h0.z), bf_hi(h0.z), bf_lo(h0.w), bf_hi(h0.w)};
;             h[2] = (f32x4){bf_lo(h1.x), bf_hi(h1.x), bf_lo(h1.y), bf_hi(h1.y)}; h[3] = (f32x4){bf_lo(h1.z), bf_hi(h1.z), bf_lo(h1.w), bf_hi(h1.w)};
;             float ss = 0.f;
; #pragma unroll
;             for (int i = 0; i < 4; ++i) ss += (yv[i][0] * yv[i][0] + yv[i][1] * yv[i][1]) + (yv[i][2] * yv[i][2] + yv[i][3] * yv[i][3]);
;             const float ry = cmul / sqrtf(wave_sum(ss) * (1.0f / D) + RMS_EPS);
; #pragma unroll
;             for (int i = 0; i < 4; ++i) h[i] = h[i] + yv[i] * ry * g4[i];
.LBB0_734:
	v_lshl_add_u64 v[114:115], s[14:15], 0, v[100:101]
	v_add_co_u32_e32 v38, vcc, 0xd000000, v114
	v_lshl_add_u64 v[36:37], s[20:21], 0, v[100:101]
	s_nop 0
	v_addc_co_u32_e32 v39, vcc, 0, v115, vcc
	flat_load_dwordx4 v[84:87], v[36:37]
	flat_load_dwordx4 v[88:91], v[36:37] offset:1024
	flat_load_dwordx4 v[92:95], v[38:39] offset:1024
	flat_load_dwordx4 v[96:99], v[38:39]
	s_add_i32 s22, s10, 3
	flat_load_dwordx4 v[80:83], v[36:37] offset:2048
	flat_load_dwordx4 v[68:71], v[36:37] offset:3072
	v_add_co_u32_e32 v36, vcc, s84, v36
	s_ashr_i32 s23, s22, 31
	s_nop 0
	v_addc_co_u32_e32 v37, vcc, 0, v37, vcc
	v_add_co_u32_e32 v56, vcc, s91, v114
	s_lshl_b64 s[2:3], s[22:23], 11
	flat_load_dwordx4 v[64:67], v[36:37]
	flat_load_dwordx4 v[52:55], v[36:37] offset:1024
	v_lshl_add_u64 v[36:37], v[102:103], 0, s[2:3]
	v_lshl_add_u64 v[58:59], v[104:105], 0, s[2:3]
	v_addc_co_u32_e32 v57, vcc, 0, v115, vcc
	flat_load_dwordx4 v[76:79], v[38:39] offset:2048
	flat_load_dwordx4 v[72:75], v[38:39] offset:3072
	flat_load_dwordx4 v[44:47], v[36:37]
	flat_load_dwordx4 v[40:43], v[36:37] offset:1024
	flat_load_dwordx4 v[48:51], v[58:59]
	s_nop 0
	flat_load_dwordx4 v[36:39], v[58:59] offset:1024
	flat_load_dwordx4 v[60:63], v[56:57]
	s_nop 0
	flat_load_dwordx4 v[56:59], v[56:57] offset:1024
	s_waitcnt vmcnt(0) lgkmcnt(0)
	v_lshlrev_b32_e32 v118, 16, v86
	v_and_b32_e32 v119, 0xffff0000, v86
	v_lshlrev_b32_e32 v124, 16, v94
	v_and_b32_e32 v142, 0xffff0000, v94
	v_lshlrev_b32_e32 v86, 16, v96
	v_lshlrev_b32_e32 v94, 16, v97
	v_lshlrev_b32_e32 v120, 16, v87
	v_and_b32_e32 v121, 0xffff0000, v87
	v_lshlrev_b32_e32 v122, 16, v88
	v_and_b32_e32 v123, 0xffff0000, v88
	v_lshlrev_b32_e32 v126, 16, v95
	v_and_b32_e32 v127, 0xffff0000, v95
	v_and_b32_e32 v87, 0xffff0000, v96
	v_and_b32_e32 v95, 0xffff0000, v97
	v_lshlrev_b32_e32 v97, 16, v99
	v_lshlrev_b32_e32 v96, 16, v98
	v_and_b32_e32 v99, 0xffff0000, v99
	v_and_b32_e32 v98, 0xffff0000, v98
	v_mul_f32_e32 v2, v86, v86
	v_mul_f32_e32 v88, v94, v94
	v_lshlrev_b32_e32 v128, 16, v92
	v_and_b32_e32 v129, 0xffff0000, v92
	v_lshlrev_b32_e32 v92, 16, v93
	v_pk_mul_f32 v[130:131], v[98:99], v[98:99]
	v_pk_fma_f32 v[138:139], v[86:87], v[86:87], v[2:3] op_sel_hi:[1,1,0]
	v_pk_fma_f32 v[140:141], v[94:95], v[94:95], v[88:89] op_sel_hi:[1,1,0]
	v_and_b32_e32 v93, 0xffff0000, v93
	v_mul_f32_e32 v132, v128, v128
	v_mul_f32_e32 v134, v92, v92
	v_mov_b32_e32 v136, v124
	v_pk_fma_f32 v[130:131], v[96:97], v[96:97], v[130:131]
	v_mov_b32_e32 v125, v139
	v_mov_b32_e32 v137, v141
	v_pk_fma_f32 v[132:133], v[128:129], v[128:129], v[132:133] op_sel_hi:[1,1,0]
	v_pk_fma_f32 v[134:135], v[92:93], v[92:93], v[134:135] op_sel_hi:[1,1,0]
	v_pk_add_f32 v[130:131], v[130:131], v[130:131] op_sel_hi:[0,1]
	v_pk_add_f32 v[138:139], v[138:139], v[140:141]
	v_pk_mul_f32 v[136:137], v[124:125], v[136:137]
	v_mul_f32_e32 v132, v126, v126
	v_mul_f32_e32 v134, v127, v127
	v_mul_f32_e32 v130, v142, v142
	v_mov_b32_e32 v137, v139
	v_pk_add_f32 v[132:133], v[132:133], v[134:135]
	v_pk_add_f32 v[130:131], v[136:137], v[130:131]
	v_lshlrev_b32_e32 v134, 16, v91
	v_pk_add_f32 v[130:131], v[130:131], v[132:133]
	v_lshlrev_b32_e32 v132, 16, v90
	v_add_f32_e32 v2, v130, v131
	v_and_b32_e32 v135, 0xffff0000, v91
	v_lshlrev_b32_e32 v116, 16, v84
	v_add_f32_dpp v2, v2, v2 quad_perm:[1,0,3,2] row_mask:0xf bank_mask:0xf bound_ctrl:1
	v_and_b32_e32 v117, 0xffff0000, v84
	v_lshlrev_b32_e32 v84, 16, v85
	v_add_f32_dpp v2, v2, v2 quad_perm:[2,3,0,1] row_mask:0xf bank_mask:0xf bound_ctrl:1
	v_and_b32_e32 v85, 0xffff0000, v85
	s_nop 0
	v_add_f32_dpp v2, v2, v2 row_half_mirror row_mask:0xf bank_mask:0xf bound_ctrl:1
	s_nop 1
	v_add_f32_dpp v2, v2, v2 row_mirror row_mask:0xf bank_mask:0xf bound_ctrl:1
	s_nop 0
	v_readlane_b32 s1, v2, 16
	v_readlane_b32 s4, v2, 48
	v_readlane_b32 s2, v2, 0
	v_readlane_b32 s3, v2, 32
	v_mov_b32_e32 v130, s1
	v_mov_b32_e32 v131, s4
	v_pk_add_f32 v[130:131], s[2:3], v[130:131]
	s_mov_b64 s[4:5], -1
	v_add_f32_e32 v2, v130, v131
	v_fmamk_f32 v2, v2, 0x3a800000, v214
	v_lshlrev_b32_e32 v130, 16, v89
	v_and_b32_e32 v131, 0xffff0000, v89
	v_and_b32_e32 v133, 0xffff0000, v90
	v_rsq_f32_e32 v2, v2
	s_nop 0
	v_mul_f32_e32 v2, 0.5, v2
	v_pk_mul_f32 v[88:89], v[2:3], v[86:87] op_sel_hi:[0,1]
	v_pk_mul_f32 v[86:87], v[2:3], v[94:95] op_sel_hi:[0,1]
	v_pk_fma_f32 v[86:87], v[10:11], v[86:87], v[84:85]
	v_pk_fma_f32 v[84:85], v[8:9], v[88:89], v[116:117]
	v_mov_b32_e32 v88, v96
	v_mov_b32_e32 v89, v98
	v_mov_b32_e32 v98, v97
	v_pk_mul_f32 v[96:97], v[2:3], v[128:129] op_sel_hi:[0,1]
	v_pk_mul_f32 v[92:93], v[2:3], v[92:93] op_sel_hi:[0,1]
	v_mov_b32_e32 v125, v142
	v_pk_mul_f32 v[88:89], v[2:3], v[88:89] op_sel_hi:[0,1]
	v_pk_mul_f32 v[90:91], v[2:3], v[98:99] op_sel_hi:[0,1]
	v_pk_fma_f32 v[94:95], v[18:19], v[92:93], v[130:131]
	v_pk_fma_f32 v[92:93], v[16:17], v[96:97], v[122:123]
	v_pk_mul_f32 v[96:97], v[124:125], v[2:3] op_sel_hi:[1,0]
	v_pk_mul_f32 v[98:99], v[126:127], v[2:3] op_sel_hi:[1,0]
	v_cndmask_b32_e64 v2, 0, 1, s[6:7]
	v_pk_fma_f32 v[90:91], v[6:7], v[90:91], v[120:121]
	v_pk_fma_f32 v[88:89], v[4:5], v[88:89], v[118:119]
	v_pk_fma_f32 v[98:99], v[14:15], v[98:99], v[134:135]
	v_pk_fma_f32 v[96:97], v[12:13], v[96:97], v[132:133]
	v_cmp_ne_u32_e64 s[2:3], 1, v2
	s_andn2_b64 vcc, exec, s[6:7]
	v_lshl_add_u64 v[116:117], s[18:19], 0, v[100:101]
	s_cbranch_vccnz .LBB0_736
; __device__ __forceinline__ void thin_pass(const Ctx& C, const bf16* hin, bf16* hout, bf16* u, float* out, const bf16* y, const float* gpost, float cmul, const float* gpre, bool last) {
;     ...
;         for (int b = 0; b < RB; ++b) {
;             const int m = m0 + b; const v4u y0 = yr[b][0], y1 = yr[b][1], h0 = hr[b][0], h1 = hr[b][1];
;             f32x4 yv[4], h[4];
;             yv[0] = (f32x4){bf_lo(y0.x), bf_hi(y0.x), bf_lo(y0.y), bf_hi(y0.y)}; yv[1] = (f32x4){bf_lo(y0.z), bf_hi(y0.z), bf_lo(y0.w), bf_hi(y0.w)};
;             yv[2] = (f32x4){bf_lo(y1.x), bf_hi(y1.x), bf_lo(y1.y), bf_hi(y1.y)}; yv[3] = (f32x4){bf_lo(y1.z), bf_hi(y1.z), bf_lo(y1.w), bf_hi(y1.w)};
;             h[0] = (f32x4){bf_lo(h0.x), bf_hi(h0.x), bf_lo(h0.y), bf_hi(h0.y)}; h[1] = (f32x4){bf_lo(h0.z), bf_hi(h0.z), bf_lo(h0.w), bf_hi(h0.w)};
;             h[2] = (f32x4){bf_lo(h1.x), bf_hi(h1.x), bf_lo(h1.y), bf_hi(h1.y)}; h[3] = (f32x4){bf_lo(h1.z), bf_hi(h1.z), bf_lo(h1.w), bf_hi(h1.w)};
;             float ss = 0.f;
; #pragma unroll
;     ...
;             if (last) { f32x4* op = (f32x4*)(out + (size_t)m * D); op[2 * lane] = h[0]; op[2 * lane + 1] = h[1]; op[128 + 2 * lane] = h[2]; op[128 + 2 * lane + 1] = h[3]; }
;             else {
;                 float s2 = 0.f;
; #pragma unroll
;                 for (int i = 0; i < 4; ++i) s2 += (h[i][0] * h[i][0] + h[i][1] * h[i][1]) + (h[i][2] * h[i][2] + h[i][3] * h[i][3]);
;                 const float rh = 1.0f / sqrtf(wave_sum(s2) * (1.0f / D) + RMS_EPS);
;                 v4u o0, o1; o0.x = pk2(h[0][0], h[0][1]); o0.y = pk2(h[0][2], h[0][3]); o0.z = pk2(h[1][0], h[1][1]); o0.w = pk2(h[1][2], h[1][3]);
;                 o1.x = pk2(h[2][0], h[2][1]); o1.y = pk2(h[2][2], h[2][3]); o1.z = pk2(h[3][0], h[3][1]); o1.w = pk2(h[3][2], h[3][3]);
;                 v4u* hp = (v4u*)(hout + (size_t)m * D); hp[lane] = o0; hp[64 + lane] = o1;
; #pragma unroll
;                 for (int i = 0; i < 4; ++i) h[i] = h[i] * rh * q4[i];
;                 o0.x = pk2(h[0][0], h[0][1]); o0.y = pk2(h[0][2], h[0][3]); o0.z = pk2(h[1][0], h[1][1]); o0.w = pk2(h[1][2], h[1][3]);
;                 o1.x = pk2(h[2][0], h[2][1]); o1.y = pk2(h[2][2], h[2][3]); o1.z = pk2(h[3][0], h[3][1]); o1.w = pk2(h[3][2], h[3][3]);
;                 v4u* up = (v4u*)(u + (size_t)m * D); up[lane] = o0; up[64 + lane] = o1;
	v_pk_mul_f32 v[118:119], v[86:87], v[86:87]
	v_pk_mul_f32 v[120:121], v[84:85], v[84:85]
	v_mul_f32_e32 v2, v92, v92
	v_pk_mov_b32 v[122:123], v[120:121], v[118:119] op_sel:[1,0]
	v_mov_b32_e32 v121, v119
	v_pk_add_f32 v[118:119], v[122:123], v[120:121]
	v_pk_mul_f32 v[120:121], v[90:91], v[90:91]
	v_pk_mul_f32 v[122:123], v[88:89], v[88:89]
	v_pk_add_f32 v[118:119], v[118:119], v[118:119] op_sel_hi:[0,1]
	v_pk_mov_b32 v[124:125], v[122:123], v[120:121] op_sel:[1,0]
	v_mov_b32_e32 v123, v121
	v_pk_add_f32 v[120:121], v[124:125], v[122:123]
	v_pk_fma_f32 v[122:123], v[92:93], v[92:93], v[2:3] op_sel_hi:[1,1,0]
	v_mul_f32_e32 v2, v94, v94
	v_pk_add_f32 v[120:121], v[120:121], v[120:121] op_sel_hi:[0,1]
	v_pk_fma_f32 v[124:125], v[94:95], v[94:95], v[2:3] op_sel_hi:[1,1,0]
	v_mul_f32_e32 v122, v96, v96
	v_mul_f32_e32 v124, v97, v97
	v_mul_f32_e32 v118, v98, v98
	v_mul_f32_e32 v120, v99, v99
	v_pk_add_f32 v[122:123], v[122:123], v[124:125]
	v_pk_add_f32 v[118:119], v[118:119], v[120:121]
	v_cvt_pk_bf16_f32 v124, v96, v97
	v_cvt_pk_bf16_f32 v125, v98, v99
	s_nop 0
	v_pk_add_f32 v[118:119], v[122:123], v[118:119]
	v_cvt_pk_bf16_f32 v123, v94, v95
	s_nop 0
	v_add_f32_e32 v2, v118, v119
	s_nop 1
	v_add_f32_dpp v2, v2, v2 quad_perm:[1,0,3,2] row_mask:0xf bank_mask:0xf bound_ctrl:1
	s_nop 1
	v_add_f32_dpp v2, v2, v2 quad_perm:[2,3,0,1] row_mask:0xf bank_mask:0xf bound_ctrl:1
	s_nop 1
	v_add_f32_dpp v2, v2, v2 row_half_mirror row_mask:0xf bank_mask:0xf bound_ctrl:1
	s_nop 1
	v_add_f32_dpp v2, v2, v2 row_mirror row_mask:0xf bank_mask:0xf bound_ctrl:1
	s_nop 0
	v_readlane_b32 s1, v2, 16
	v_readlane_b32 s9, v2, 48
	v_readlane_b32 s4, v2, 0
	v_readlane_b32 s5, v2, 32
	v_mov_b32_e32 v118, s1
	v_mov_b32_e32 v119, s9
	v_pk_add_f32 v[118:119], s[4:5], v[118:119]
	s_brev_b32 s1, 64
	v_add_f32_e32 v2, v118, v119
	v_fmamk_f32 v2, v2, 0x3a800000, v214
	s_mov_b64 s[4:5], 0
	v_add_co_u32_e32 v126, vcc, s1, v116
	v_rsq_f32_e32 v2, v2
	s_nop 0
	v_cvt_pk_bf16_f32 v118, v84, v85
	v_cvt_pk_bf16_f32 v119, v86, v87
	v_cvt_pk_bf16_f32 v120, v88, v89
	v_cvt_pk_bf16_f32 v121, v90, v91
	v_cvt_pk_bf16_f32 v122, v92, v93
	s_nop 0
	v_addc_co_u32_e32 v127, vcc, 0, v117, vcc
	global_store_dwordx4 v[126:127], v[118:121], off sc1
	global_store_dwordx4 v[126:127], v[122:125], off offset:1024 sc1
	v_pk_mul_f32 v[126:127], v[92:93], v[2:3] op_sel_hi:[1,0]
	v_pk_mul_f32 v[118:119], v[84:85], v[2:3] op_sel_hi:[1,0]
	v_pk_mul_f32 v[120:121], v[86:87], v[2:3] op_sel_hi:[1,0]
	v_pk_mul_f32 v[122:123], v[88:89], v[2:3] op_sel_hi:[1,0]
	v_pk_mul_f32 v[120:121], v[26:27], v[120:121]
	v_pk_mul_f32 v[118:119], v[24:25], v[118:119]
	v_pk_mul_f32 v[122:123], v[20:21], v[122:123]
	v_pk_mul_f32 v[126:127], v[32:33], v[126:127]
	v_pk_mul_f32 v[124:125], v[90:91], v[2:3] op_sel_hi:[1,0]
	v_cvt_pk_bf16_f32 v118, v118, v119
	v_cvt_pk_bf16_f32 v119, v120, v121
	v_cvt_pk_bf16_f32 v120, v122, v123
	v_cvt_pk_bf16_f32 v122, v126, v127
	v_add_co_u32_e32 v126, vcc, 0xb000000, v114
	v_pk_mul_f32 v[124:125], v[22:23], v[124:125]
	v_pk_mul_f32 v[128:129], v[94:95], v[2:3] op_sel_hi:[1,0]
	v_pk_mul_f32 v[130:131], v[96:97], v[2:3] op_sel_hi:[1,0]
	v_pk_mul_f32 v[132:133], v[98:99], v[2:3] op_sel_hi:[1,0]
	v_cvt_pk_bf16_f32 v121, v124, v125
	v_addc_co_u32_e32 v127, vcc, 0, v115, vcc
	v_pk_mul_f32 v[128:129], v[34:35], v[128:129]
	v_pk_mul_f32 v[132:133], v[30:31], v[132:133]
	v_pk_mul_f32 v[130:131], v[28:29], v[130:131]
	v_cvt_pk_bf16_f32 v123, v128, v129
	v_cvt_pk_bf16_f32 v125, v132, v133
	s_nop 0
	v_cvt_pk_bf16_f32 v124, v130, v131
	flat_store_dwordx4 v[126:127], v[118:121] sc1
	flat_store_dwordx4 v[126:127], v[122:125] offset:1024 sc1
.LBB0_736:
	s_andn2_b64 vcc, exec, s[4:5]
	s_cbranch_vccnz .LBB0_738
	v_add_co_u32_e32 v118, vcc, 0xffffe000, v112
	s_nop 1
	v_addc_co_u32_e32 v119, vcc, -1, v113, vcc
	global_store_dwordx4 v[118:119], v[84:87], off offset:-2064 sc1
	global_store_dwordx4 v[118:119], v[88:91], off offset:-2048 sc1
	global_store_dwordx4 v[118:119], v[92:95], off offset:-16 sc1
	global_store_dwordx4 v[118:119], v[96:99], off sc1
.LBB0_738:
	s_nop 0
	v_lshlrev_b32_e32 v92, 16, v76
	v_and_b32_e32 v93, 0xffff0000, v76
	v_mul_f32_e32 v2, v92, v92
	v_lshlrev_b32_e32 v76, 16, v77
	v_pk_fma_f32 v[94:95], v[92:93], v[92:93], v[2:3] op_sel_hi:[1,1,0]
	v_and_b32_e32 v77, 0xffff0000, v77
	v_mul_f32_e32 v2, v76, v76
	v_lshlrev_b32_e32 v99, 16, v79
	v_lshlrev_b32_e32 v98, 16, v78
	v_and_b32_e32 v79, 0xffff0000, v79
	v_and_b32_e32 v78, 0xffff0000, v78
	v_lshlrev_b32_e32 v120, 16, v72
	v_lshlrev_b32_e32 v84, 16, v74
	v_pk_fma_f32 v[96:97], v[76:77], v[76:77], v[2:3] op_sel_hi:[1,1,0]
	v_pk_mul_f32 v[118:119], v[78:79], v[78:79]
	v_and_b32_e32 v121, 0xffff0000, v72
	v_mul_f32_e32 v2, v120, v120
	v_lshlrev_b32_e32 v124, 16, v73
	v_pk_fma_f32 v[118:119], v[98:99], v[98:99], v[118:119]
	v_pk_fma_f32 v[122:123], v[120:121], v[120:121], v[2:3] op_sel_hi:[1,1,0]
	v_and_b32_e32 v125, 0xffff0000, v73
	v_mul_f32_e32 v2, v124, v124
	v_mov_b32_e32 v85, v95
	v_mov_b32_e32 v126, v84
	v_mov_b32_e32 v127, v97
	v_and_b32_e32 v128, 0xffff0000, v74
	v_lshlrev_b32_e32 v86, 16, v75
	v_and_b32_e32 v87, 0xffff0000, v75
	v_pk_add_f32 v[118:119], v[118:119], v[118:119] op_sel_hi:[0,1]
	v_pk_fma_f32 v[72:73], v[124:125], v[124:125], v[2:3] op_sel_hi:[1,1,0]
	v_pk_mul_f32 v[126:127], v[84:85], v[126:127]
	v_pk_add_f32 v[94:95], v[94:95], v[96:97]
	v_mul_f32_e32 v118, v128, v128
	v_mul_f32_e32 v122, v86, v86
	v_mul_f32_e32 v72, v87, v87
	v_mov_b32_e32 v127, v95
	v_pk_add_f32 v[94:95], v[126:127], v[118:119]
	v_pk_add_f32 v[72:73], v[122:123], v[72:73]
	v_lshlrev_b32_e32 v90, 16, v68
	v_pk_add_f32 v[72:73], v[94:95], v[72:73]
; __device__ __forceinline__ void thin_pass(const Ctx& C, const bf16* hin, bf16* hout, bf16* u, float* out, const bf16* y, const float* gpost, float cmul, const float* gpre, bool last) {
;     ...
;         for (int b = 0; b < RB; ++b) {
;             const int m = m0 + b; const v4u y0 = yr[b][0], y1 = yr[b][1], h0 = hr[b][0], h1 = hr[b][1];
;             f32x4 yv[4], h[4];
;             yv[0] = (f32x4){bf_lo(y0.x), bf_hi(y0.x), bf_lo(y0.y), bf_hi(y0.y)}; yv[1] = (f32x4){bf_lo(y0.z), bf_hi(y0.z), bf_lo(y0.w), bf_hi(y0.w)};
;             yv[2] = (f32x4){bf_lo(y1.x), bf_hi(y1.x), bf_lo(y1.y), bf_hi(y1.y)}; yv[3] = (f32x4){bf_lo(y1.z), bf_hi(y1.z), bf_lo(y1.w), bf_hi(y1.w)};
;             h[0] = (f32x4){bf_lo(h0.x), bf_hi(h0.x), bf_lo(h0.y), bf_hi(h0.y)}; h[1] = (f32x4){bf_lo(h0.z), bf_hi(h0.z), bf_lo(h0.w), bf_hi(h0.w)};
;             h[2] = (f32x4){bf_lo(h1.x), bf_hi(h1.x), bf_lo(h1.y), bf_hi(h1.y)}; h[3] = (f32x4){bf_lo(h1.z), bf_hi(h1.z), bf_lo(h1.w), bf_hi(h1.w)};
;             float ss = 0.f;
; #pragma unroll
;             for (int i = 0; i < 4; ++i) ss += (yv[i][0] * yv[i][0] + yv[i][1] * yv[i][1]) + (yv[i][2] * yv[i][2] + yv[i][3] * yv[i][3]);
;             const float ry = cmul / sqrtf(wave_sum(ss) * (1.0f / D) + RMS_EPS);
; #pragma unroll
;             for (int i = 0; i < 4; ++i) h[i] = h[i] + yv[i] * ry * g4[i];
;             if (last) { f32x4* op = (f32x4*)(out + (size_t)m * D); op[2 * lane] = h[0]; op[2 * lane + 1] = h[1]; op[128 + 2 * lane] = h[2]; op[128 + 2 * lane + 1] = h[3]; }
;             else {
;                 float s2 = 0.f;
; #pragma unroll
;                 for (int i = 0; i < 4; ++i) s2 += (h[i][0] * h[i][0] + h[i][1] * h[i][1]) + (h[i][2] * h[i][2] + h[i][3] * h[i][3]);
;                 const float rh = 1.0f / sqrtf(wave_sum(s2) * (1.0f / D) + RMS_EPS);
;                 v4u o0, o1; o0.x = pk2(h[0][0], h[0][1]); o0.y = pk2(h[0][2], h[0][3]); o0.z = pk2(h[1][0], h[1][1]); o0.w = pk2(h[1][2], h[1][3]);
;                 o1.x = pk2(h[2][0], h[2][1]); o1.y = pk2(h[2][2], h[2][3]); o1.z = pk2(h[3][0], h[3][1]); o1.w = pk2(h[3][2], h[3][3]);
;                 v4u* hp = (v4u*)(hout + (size_t)m * D); hp[lane] = o0; hp[64 + lane] = o1;
; #pragma unroll
;                 for (int i = 0; i < 4; ++i) h[i] = h[i] * rh * q4[i];
	v_and_b32_e32 v91, 0xffff0000, v68
	v_add_f32_e32 v2, v72, v73
	v_lshlrev_b32_e32 v94, 16, v69
	v_and_b32_e32 v95, 0xffff0000, v69
	v_add_f32_dpp v2, v2, v2 quad_perm:[1,0,3,2] row_mask:0xf bank_mask:0xf bound_ctrl:1
	v_lshlrev_b32_e32 v96, 16, v70
	v_and_b32_e32 v97, 0xffff0000, v70
	v_add_f32_dpp v2, v2, v2 quad_perm:[2,3,0,1] row_mask:0xf bank_mask:0xf bound_ctrl:1
	v_lshlrev_b32_e32 v118, 16, v71
	v_and_b32_e32 v119, 0xffff0000, v71
	v_add_f32_dpp v2, v2, v2 row_half_mirror row_mask:0xf bank_mask:0xf bound_ctrl:1
	v_lshlrev_b32_e32 v74, 16, v80
	v_and_b32_e32 v75, 0xffff0000, v80
	v_add_f32_dpp v2, v2, v2 row_mirror row_mask:0xf bank_mask:0xf bound_ctrl:1
	v_lshlrev_b32_e32 v80, 16, v81
	v_readlane_b32 s1, v2, 16
	v_readlane_b32 s9, v2, 48
	v_readlane_b32 s4, v2, 0
	v_readlane_b32 s5, v2, 32
	v_mov_b32_e32 v72, s1
	v_mov_b32_e32 v73, s9
	v_pk_add_f32 v[72:73], s[4:5], v[72:73]
	v_and_b32_e32 v81, 0xffff0000, v81
	v_add_f32_e32 v2, v72, v73
	v_fmamk_f32 v2, v2, 0x3a800000, v214
	v_mov_b32_e32 v73, v78
	v_mov_b32_e32 v78, v99
	v_lshlrev_b32_e32 v88, 16, v82
	v_and_b32_e32 v89, 0xffff0000, v82
	v_lshlrev_b32_e32 v82, 16, v83
	v_and_b32_e32 v83, 0xffff0000, v83
	v_mov_b32_e32 v85, v128
	s_mov_b64 s[4:5], -1
	v_rsq_f32_e32 v2, v2
	s_nop 0
	v_mul_f32_e32 v2, 0.5, v2
	v_pk_mul_f32 v[68:69], v[2:3], v[92:93] op_sel_hi:[0,1]
	v_pk_mul_f32 v[70:71], v[2:3], v[76:77] op_sel_hi:[0,1]
	v_pk_fma_f32 v[68:69], v[8:9], v[68:69], v[74:75]
	v_mov_b32_e32 v72, v98
	v_pk_mul_f32 v[74:75], v[2:3], v[78:79] op_sel_hi:[0,1]
	v_pk_fma_f32 v[70:71], v[10:11], v[70:71], v[80:81]
	v_pk_mul_f32 v[72:73], v[2:3], v[72:73] op_sel_hi:[0,1]
	v_pk_fma_f32 v[74:75], v[6:7], v[74:75], v[82:83]
	v_pk_mul_f32 v[76:77], v[2:3], v[120:121] op_sel_hi:[0,1]
	v_pk_mul_f32 v[78:79], v[2:3], v[124:125] op_sel_hi:[0,1]
	v_pk_mul_f32 v[80:81], v[84:85], v[2:3] op_sel_hi:[1,0]
	v_pk_mul_f32 v[82:83], v[86:87], v[2:3] op_sel_hi:[1,0]
	v_pk_fma_f32 v[72:73], v[4:5], v[72:73], v[88:89]
	v_pk_fma_f32 v[78:79], v[18:19], v[78:79], v[94:95]
	v_pk_fma_f32 v[76:77], v[16:17], v[76:77], v[90:91]
	v_pk_fma_f32 v[82:83], v[14:15], v[82:83], v[118:119]
	v_pk_fma_f32 v[80:81], v[12:13], v[80:81], v[96:97]
	s_and_b64 vcc, exec, s[2:3]
	s_cbranch_vccnz .LBB0_740
	v_pk_mul_f32 v[84:85], v[70:71], v[70:71]
	v_pk_mul_f32 v[86:87], v[68:69], v[68:69]
	v_mul_f32_e32 v2, v76, v76
	v_pk_mov_b32 v[88:89], v[86:87], v[84:85] op_sel:[1,0]
	v_mov_b32_e32 v87, v85
	v_pk_add_f32 v[84:85], v[88:89], v[86:87]
	v_pk_mul_f32 v[86:87], v[74:75], v[74:75]
	v_pk_mul_f32 v[88:89], v[72:73], v[72:73]
	v_pk_add_f32 v[84:85], v[84:85], v[84:85] op_sel_hi:[0,1]
	v_pk_mov_b32 v[90:91], v[88:89], v[86:87] op_sel:[1,0]
	v_mov_b32_e32 v89, v87
	v_pk_add_f32 v[86:87], v[90:91], v[88:89]
	v_pk_fma_f32 v[88:89], v[76:77], v[76:77], v[2:3] op_sel_hi:[1,1,0]
	v_mul_f32_e32 v2, v78, v78
	v_pk_add_f32 v[86:87], v[86:87], v[86:87] op_sel_hi:[0,1]
	v_pk_fma_f32 v[90:91], v[78:79], v[78:79], v[2:3] op_sel_hi:[1,1,0]
	v_mul_f32_e32 v88, v80, v80
	v_mul_f32_e32 v90, v81, v81
	v_mul_f32_e32 v84, v82, v82
	v_mul_f32_e32 v86, v83, v83
	v_pk_add_f32 v[88:89], v[88:89], v[90:91]
	v_pk_add_f32 v[84:85], v[84:85], v[86:87]
	v_cvt_pk_bf16_f32 v90, v80, v81
	v_cvt_pk_bf16_f32 v91, v82, v83
	s_nop 0
	v_pk_add_f32 v[84:85], v[88:89], v[84:85]
	v_cvt_pk_bf16_f32 v89, v78, v79
	s_nop 0
	v_add_f32_e32 v2, v84, v85
	s_nop 1
	v_add_f32_dpp v2, v2, v2 quad_perm:[1,0,3,2] row_mask:0xf bank_mask:0xf bound_ctrl:1
	s_nop 1
	v_add_f32_dpp v2, v2, v2 quad_perm:[2,3,0,1] row_mask:0xf bank_mask:0xf bound_ctrl:1
	s_nop 1
	v_add_f32_dpp v2, v2, v2 row_half_mirror row_mask:0xf bank_mask:0xf bound_ctrl:1
	s_nop 1
	v_add_f32_dpp v2, v2, v2 row_mirror row_mask:0xf bank_mask:0xf bound_ctrl:1
	s_nop 0
	v_readlane_b32 s1, v2, 16
	v_readlane_b32 s9, v2, 48
	v_readlane_b32 s4, v2, 0
	v_readlane_b32 s5, v2, 32
	v_mov_b32_e32 v84, s1
	v_mov_b32_e32 v85, s9
	v_pk_add_f32 v[84:85], s[4:5], v[84:85]
	s_brev_b32 s1, 64
	v_add_f32_e32 v2, v84, v85
	v_fmamk_f32 v2, v2, 0x3a800000, v214
	s_mov_b64 s[4:5], 0
	v_add_co_u32_e32 v92, vcc, s1, v116
	v_rsq_f32_e32 v2, v2
	s_nop 0
	v_cvt_pk_bf16_f32 v84, v68, v69
	v_cvt_pk_bf16_f32 v85, v70, v71
	v_cvt_pk_bf16_f32 v86, v72, v73
	v_cvt_pk_bf16_f32 v87, v74, v75
	v_cvt_pk_bf16_f32 v88, v76, v77
	s_nop 0
	v_addc_co_u32_e32 v93, vcc, 0, v117, vcc
	global_store_dwordx4 v[92:93], v[84:87], off offset:2048 sc1
	global_store_dwordx4 v[92:93], v[88:91], off offset:3072 sc1
	v_pk_mul_f32 v[92:93], v[76:77], v[2:3] op_sel_hi:[1,0]
	v_pk_mul_f32 v[84:85], v[68:69], v[2:3] op_sel_hi:[1,0]
	v_pk_mul_f32 v[86:87], v[70:71], v[2:3] op_sel_hi:[1,0]
	v_pk_mul_f32 v[88:89], v[72:73], v[2:3] op_sel_hi:[1,0]
	v_pk_mul_f32 v[86:87], v[26:27], v[86:87]
	v_pk_mul_f32 v[84:85], v[24:25], v[84:85]
	v_pk_mul_f32 v[88:89], v[20:21], v[88:89]
	v_pk_mul_f32 v[92:93], v[32:33], v[92:93]
	v_pk_mul_f32 v[90:91], v[74:75], v[2:3] op_sel_hi:[1,0]
	v_cvt_pk_bf16_f32 v84, v84, v85
	v_cvt_pk_bf16_f32 v85, v86, v87
	v_cvt_pk_bf16_f32 v86, v88, v89
	v_cvt_pk_bf16_f32 v88, v92, v93
	v_add_co_u32_e32 v92, vcc, 0xb000000, v114
	v_pk_mul_f32 v[90:91], v[22:23], v[90:91]
	v_pk_mul_f32 v[94:95], v[78:79], v[2:3] op_sel_hi:[1,0]
	v_pk_mul_f32 v[96:97], v[80:81], v[2:3] op_sel_hi:[1,0]
	v_pk_mul_f32 v[98:99], v[82:83], v[2:3] op_sel_hi:[1,0]
	v_cvt_pk_bf16_f32 v87, v90, v91
	v_addc_co_u32_e32 v93, vcc, 0, v115, vcc
	v_pk_mul_f32 v[94:95], v[34:35], v[94:95]
	v_pk_mul_f32 v[98:99], v[30:31], v[98:99]
	v_pk_mul_f32 v[96:97], v[28:29], v[96:97]
	v_cvt_pk_bf16_f32 v89, v94, v95
	v_cvt_pk_bf16_f32 v91, v98, v99
	s_nop 0
	v_cvt_pk_bf16_f32 v90, v96, v97
	flat_store_dwordx4 v[92:93], v[84:87] offset:2048 sc1
	flat_store_dwordx4 v[92:93], v[88:91] offset:3072 sc1
; __device__ __forceinline__ void thin_pass(const Ctx& C, const bf16* hin, bf16* hout, bf16* u, float* out, const bf16* y, const float* gpost, float cmul, const float* gpre, bool last) {
;     ...
;         for (int b = 0; b < RB; ++b) {
;             const int m = m0 + b; const v4u y0 = yr[b][0], y1 = yr[b][1], h0 = hr[b][0], h1 = hr[b][1];
;             f32x4 yv[4], h[4];
;             yv[0] = (f32x4){bf_lo(y0.x), bf_hi(y0.x), bf_lo(y0.y), bf_hi(y0.y)}; yv[1] = (f32x4){bf_lo(y0.z), bf_hi(y0.z), bf_lo(y0.w), bf_hi(y0.w)};
;             yv[2] = (f32x4){bf_lo(y1.x), bf_hi(y1.x), bf_lo(y1.y), bf_hi(y1.y)}; yv[3] = (f32x4){bf_lo(y1.z), bf_hi(y1.z), bf_lo(y1.w), bf_hi(y1.w)};
;             h[0] = (f32x4){bf_lo(h0.x), bf_hi(h0.x), bf_lo(h0.y), bf_hi(h0.y)}; h[1] = (f32x4){bf_lo(h0.z), bf_hi(h0.z), bf_lo(h0.w), bf_hi(h0.w)};
;             h[2] = (f32x4){bf_lo(h1.x), bf_hi(h1.x), bf_lo(h1.y), bf_hi(h1.y)}; h[3] = (f32x4){bf_lo(h1.z), bf_hi(h1.z), bf_lo(h1.w), bf_hi(h1.w)};
;             float ss = 0.f;
; #pragma unroll
;             for (int i = 0; i < 4; ++i) ss += (yv[i][0] * yv[i][0] + yv[i][1] * yv[i][1]) + (yv[i][2] * yv[i][2] + yv[i][3] * yv[i][3]);
;             const float ry = cmul / sqrtf(wave_sum(ss) * (1.0f / D) + RMS_EPS);
; #pragma unroll
;             for (int i = 0; i < 4; ++i) h[i] = h[i] + yv[i] * ry * g4[i];
;             if (last) { f32x4* op = (f32x4*)(out + (size_t)m * D); op[2 * lane] = h[0]; op[2 * lane + 1] = h[1]; op[128 + 2 * lane] = h[2]; op[128 + 2 * lane + 1] = h[3]; }
;             else {
;                 float s2 = 0.f;
; #pragma unroll
;                 for (int i = 0; i < 4; ++i) s2 += (h[i][0] * h[i][0] + h[i][1] * h[i][1]) + (h[i][2] * h[i][2] + h[i][3] * h[i][3]);
;                 const float rh = 1.0f / sqrtf(wave_sum(s2) * (1.0f / D) + RMS_EPS);
;                 v4u o0, o1; o0.x = pk2(h[0][0], h[0][1]); o0.y = pk2(h[0][2], h[0][3]); o0.z = pk2(h[1][0], h[1][1]); o0.w = pk2(h[1][2], h[1][3]);
;                 o1.x = pk2(h[2][0], h[2][1]); o1.y = pk2(h[2][2], h[2][3]); o1.z = pk2(h[3][0], h[3][1]); o1.w = pk2(h[3][2], h[3][3]);
;                 v4u* hp = (v4u*)(hout + (size_t)m * D); hp[lane] = o0; hp[64 + lane] = o1;
; #pragma unroll
;                 for (int i = 0; i < 4; ++i) h[i] = h[i] * rh * q4[i];
.LBB0_740:
	s_andn2_b64 vcc, exec, s[4:5]
	s_cbranch_vccnz .LBB0_742
	v_add_co_u32_e32 v84, vcc, 0xfffff000, v112
	s_nop 1
	v_addc_co_u32_e32 v85, vcc, -1, v113, vcc
	global_store_dwordx4 v[84:85], v[68:71], off offset:-2064 sc1
	global_store_dwordx4 v[84:85], v[72:75], off offset:-2048 sc1
	global_store_dwordx4 v[84:85], v[76:79], off offset:-16 sc1
	global_store_dwordx4 v[112:113], v[80:83], off offset:-4096 sc1
.LBB0_742:
	s_nop 0
	v_lshlrev_b32_e32 v76, 16, v60
	v_and_b32_e32 v77, 0xffff0000, v60
	v_mul_f32_e32 v2, v76, v76
	v_lshlrev_b32_e32 v60, 16, v61
	v_pk_fma_f32 v[78:79], v[76:77], v[76:77], v[2:3] op_sel_hi:[1,1,0]
	v_and_b32_e32 v61, 0xffff0000, v61
	v_mul_f32_e32 v2, v60, v60
	v_lshlrev_b32_e32 v83, 16, v63
	v_lshlrev_b32_e32 v82, 16, v62
	v_and_b32_e32 v63, 0xffff0000, v63
	v_and_b32_e32 v62, 0xffff0000, v62
	v_lshlrev_b32_e32 v86, 16, v56
	v_lshlrev_b32_e32 v68, 16, v58
	v_pk_fma_f32 v[80:81], v[60:61], v[60:61], v[2:3] op_sel_hi:[1,1,0]
	v_pk_mul_f32 v[84:85], v[62:63], v[62:63]
	v_and_b32_e32 v87, 0xffff0000, v56
	v_mul_f32_e32 v2, v86, v86
	v_lshlrev_b32_e32 v90, 16, v57
	v_pk_fma_f32 v[84:85], v[82:83], v[82:83], v[84:85]
	v_pk_fma_f32 v[88:89], v[86:87], v[86:87], v[2:3] op_sel_hi:[1,1,0]
	v_and_b32_e32 v91, 0xffff0000, v57
	v_mul_f32_e32 v2, v90, v90
	v_mov_b32_e32 v69, v79
	v_mov_b32_e32 v92, v68
	v_mov_b32_e32 v93, v81
	v_and_b32_e32 v94, 0xffff0000, v58
	v_lshlrev_b32_e32 v70, 16, v59
	v_and_b32_e32 v71, 0xffff0000, v59
	v_pk_add_f32 v[84:85], v[84:85], v[84:85] op_sel_hi:[0,1]
	v_pk_fma_f32 v[56:57], v[90:91], v[90:91], v[2:3] op_sel_hi:[1,1,0]
	v_pk_mul_f32 v[92:93], v[68:69], v[92:93]
	v_pk_add_f32 v[78:79], v[78:79], v[80:81]
	v_mul_f32_e32 v84, v94, v94
	v_mul_f32_e32 v88, v70, v70
	v_mul_f32_e32 v56, v71, v71
	v_mov_b32_e32 v93, v79
	v_pk_add_f32 v[78:79], v[92:93], v[84:85]
	v_pk_add_f32 v[56:57], v[88:89], v[56:57]
	v_lshlrev_b32_e32 v74, 16, v52
	v_pk_add_f32 v[56:57], v[78:79], v[56:57]
	v_and_b32_e32 v75, 0xffff0000, v52
	v_add_f32_e32 v2, v56, v57
	v_lshlrev_b32_e32 v78, 16, v53
	v_and_b32_e32 v79, 0xffff0000, v53
	v_add_f32_dpp v2, v2, v2 quad_perm:[1,0,3,2] row_mask:0xf bank_mask:0xf bound_ctrl:1
	v_lshlrev_b32_e32 v80, 16, v54
	v_and_b32_e32 v81, 0xffff0000, v54
	v_add_f32_dpp v2, v2, v2 quad_perm:[2,3,0,1] row_mask:0xf bank_mask:0xf bound_ctrl:1
	v_lshlrev_b32_e32 v84, 16, v55
	v_and_b32_e32 v85, 0xffff0000, v55
	v_add_f32_dpp v2, v2, v2 row_half_mirror row_mask:0xf bank_mask:0xf bound_ctrl:1
	v_lshlrev_b32_e32 v58, 16, v64
	v_and_b32_e32 v59, 0xffff0000, v64
	v_add_f32_dpp v2, v2, v2 row_mirror row_mask:0xf bank_mask:0xf bound_ctrl:1
	v_lshlrev_b32_e32 v64, 16, v65
	v_readlane_b32 s1, v2, 16
	v_readlane_b32 s9, v2, 48
	v_readlane_b32 s4, v2, 0
	v_readlane_b32 s5, v2, 32
	v_mov_b32_e32 v56, s1
	v_mov_b32_e32 v57, s9
	v_pk_add_f32 v[56:57], s[4:5], v[56:57]
	v_and_b32_e32 v65, 0xffff0000, v65
	v_add_f32_e32 v2, v56, v57
	v_fmamk_f32 v2, v2, 0x3a800000, v214
	v_mov_b32_e32 v57, v62
	v_mov_b32_e32 v62, v83
	v_lshlrev_b32_e32 v72, 16, v66
	v_and_b32_e32 v73, 0xffff0000, v66
	v_lshlrev_b32_e32 v66, 16, v67
	v_and_b32_e32 v67, 0xffff0000, v67
	v_mov_b32_e32 v69, v94
	s_mov_b64 s[4:5], -1
	v_rsq_f32_e32 v2, v2
	s_nop 0
	v_mul_f32_e32 v2, 0.5, v2
	v_pk_mul_f32 v[52:53], v[2:3], v[76:77] op_sel_hi:[0,1]
	v_pk_mul_f32 v[54:55], v[2:3], v[60:61] op_sel_hi:[0,1]
	v_pk_fma_f32 v[52:53], v[8:9], v[52:53], v[58:59]
	v_mov_b32_e32 v56, v82
	v_pk_mul_f32 v[58:59], v[2:3], v[62:63] op_sel_hi:[0,1]
	v_pk_fma_f32 v[54:55], v[10:11], v[54:55], v[64:65]
	v_pk_mul_f32 v[56:57], v[2:3], v[56:57] op_sel_hi:[0,1]
	v_pk_fma_f32 v[58:59], v[6:7], v[58:59], v[66:67]
	v_pk_mul_f32 v[60:61], v[2:3], v[86:87] op_sel_hi:[0,1]
	v_pk_mul_f32 v[62:63], v[2:3], v[90:91] op_sel_hi:[0,1]
	v_pk_mul_f32 v[64:65], v[68:69], v[2:3] op_sel_hi:[1,0]
	v_pk_mul_f32 v[66:67], v[70:71], v[2:3] op_sel_hi:[1,0]
	v_pk_fma_f32 v[56:57], v[4:5], v[56:57], v[72:73]
	v_pk_fma_f32 v[62:63], v[18:19], v[62:63], v[78:79]
	v_pk_fma_f32 v[60:61], v[16:17], v[60:61], v[74:75]
	v_pk_fma_f32 v[66:67], v[14:15], v[66:67], v[84:85]
	v_pk_fma_f32 v[64:65], v[12:13], v[64:65], v[80:81]
	s_and_b64 vcc, exec, s[2:3]
	s_cbranch_vccnz .LBB0_744
	v_pk_mul_f32 v[68:69], v[54:55], v[54:55]
	v_pk_mul_f32 v[70:71], v[52:53], v[52:53]
	v_mul_f32_e32 v2, v60, v60
	v_pk_mov_b32 v[72:73], v[70:71], v[68:69] op_sel:[1,0]
	v_mov_b32_e32 v71, v69
	v_pk_add_f32 v[68:69], v[72:73], v[70:71]
	v_pk_mul_f32 v[70:71], v[58:59], v[58:59]
	v_pk_mul_f32 v[72:73], v[56:57], v[56:57]
	v_pk_add_f32 v[68:69], v[68:69], v[68:69] op_sel_hi:[0,1]
	v_pk_mov_b32 v[74:75], v[72:73], v[70:71] op_sel:[1,0]
	v_mov_b32_e32 v73, v71
	v_pk_add_f32 v[70:71], v[74:75], v[72:73]
	v_pk_fma_f32 v[72:73], v[60:61], v[60:61], v[2:3] op_sel_hi:[1,1,0]
	v_mul_f32_e32 v2, v62, v62
	v_pk_add_f32 v[70:71], v[70:71], v[70:71] op_sel_hi:[0,1]
	v_pk_fma_f32 v[74:75], v[62:63], v[62:63], v[2:3] op_sel_hi:[1,1,0]
	v_mul_f32_e32 v72, v64, v64
	v_mul_f32_e32 v74, v65, v65
	v_mul_f32_e32 v68, v66, v66
	v_mul_f32_e32 v70, v67, v67
	v_pk_add_f32 v[72:73], v[72:73], v[74:75]
	v_pk_add_f32 v[68:69], v[68:69], v[70:71]
	v_cvt_pk_bf16_f32 v74, v64, v65
	v_cvt_pk_bf16_f32 v75, v66, v67
	s_nop 0
	v_pk_add_f32 v[68:69], v[72:73], v[68:69]
	v_cvt_pk_bf16_f32 v73, v62, v63
	s_nop 0
	v_add_f32_e32 v2, v68, v69
	s_nop 1
	v_add_f32_dpp v2, v2, v2 quad_perm:[1,0,3,2] row_mask:0xf bank_mask:0xf bound_ctrl:1
	s_nop 1
	v_add_f32_dpp v2, v2, v2 quad_perm:[2,3,0,1] row_mask:0xf bank_mask:0xf bound_ctrl:1
	s_nop 1
	v_add_f32_dpp v2, v2, v2 row_half_mirror row_mask:0xf bank_mask:0xf bound_ctrl:1
	s_nop 1
; __device__ __forceinline__ void thin_pass(const Ctx& C, const bf16* hin, bf16* hout, bf16* u, float* out, const bf16* y, const float* gpost, float cmul, const float* gpre, bool last) {
;     ...
;         for (int b = 0; b < RB; ++b) {
;             const int m = m0 + b; const v4u y0 = yr[b][0], y1 = yr[b][1], h0 = hr[b][0], h1 = hr[b][1];
;             f32x4 yv[4], h[4];
;             yv[0] = (f32x4){bf_lo(y0.x), bf_hi(y0.x), bf_lo(y0.y), bf_hi(y0.y)}; yv[1] = (f32x4){bf_lo(y0.z), bf_hi(y0.z), bf_lo(y0.w), bf_hi(y0.w)};
;             yv[2] = (f32x4){bf_lo(y1.x), bf_hi(y1.x), bf_lo(y1.y), bf_hi(y1.y)}; yv[3] = (f32x4){bf_lo(y1.z), bf_hi(y1.z), bf_lo(y1.w), bf_hi(y1.w)};
;             h[0] = (f32x4){bf_lo(h0.x), bf_hi(h0.x), bf_lo(h0.y), bf_hi(h0.y)}; h[1] = (f32x4){bf_lo(h0.z), bf_hi(h0.z), bf_lo(h0.w), bf_hi(h0.w)};
;             h[2] = (f32x4){bf_lo(h1.x), bf_hi(h1.x), bf_lo(h1.y), bf_hi(h1.y)}; h[3] = (f32x4){bf_lo(h1.z), bf_hi(h1.z), bf_lo(h1.w), bf_hi(h1.w)};
;             float ss = 0.f;
; #pragma unroll
;             for (int i = 0; i < 4; ++i) ss += (yv[i][0] * yv[i][0] + yv[i][1] * yv[i][1]) + (yv[i][2] * yv[i][2] + yv[i][3] * yv[i][3]);
;             const float ry = cmul / sqrtf(wave_sum(ss) * (1.0f / D) + RMS_EPS);
; #pragma unroll
;             for (int i = 0; i < 4; ++i) h[i] = h[i] + yv[i] * ry * g4[i];
;             if (last) { f32x4* op = (f32x4*)(out + (size_t)m * D); op[2 * lane] = h[0]; op[2 * lane + 1] = h[1]; op[128 + 2 * lane] = h[2]; op[128 + 2 * lane + 1] = h[3]; }
;             else {
;                 float s2 = 0.f;
; #pragma unroll
;                 for (int i = 0; i < 4; ++i) s2 += (h[i][0] * h[i][0] + h[i][1] * h[i][1]) + (h[i][2] * h[i][2] + h[i][3] * h[i][3]);
;                 const float rh = 1.0f / sqrtf(wave_sum(s2) * (1.0f / D) + RMS_EPS);
;                 v4u o0, o1; o0.x = pk2(h[0][0], h[0][1]); o0.y = pk2(h[0][2], h[0][3]); o0.z = pk2(h[1][0], h[1][1]); o0.w = pk2(h[1][2], h[1][3]);
;                 o1.x = pk2(h[2][0], h[2][1]); o1.y = pk2(h[2][2], h[2][3]); o1.z = pk2(h[3][0], h[3][1]); o1.w = pk2(h[3][2], h[3][3]);
;                 v4u* hp = (v4u*)(hout + (size_t)m * D); hp[lane] = o0; hp[64 + lane] = o1;
; #pragma unroll
;                 for (int i = 0; i < 4; ++i) h[i] = h[i] * rh * q4[i];
	v_add_f32_dpp v2, v2, v2 row_mirror row_mask:0xf bank_mask:0xf bound_ctrl:1
	s_nop 0
	v_readlane_b32 s1, v2, 16
	v_readlane_b32 s9, v2, 48
	v_readlane_b32 s4, v2, 0
	v_readlane_b32 s5, v2, 32
	v_mov_b32_e32 v68, s1
	v_mov_b32_e32 v69, s9
	v_pk_add_f32 v[68:69], s[4:5], v[68:69]
	s_nop 0
	v_add_f32_e32 v2, v68, v69
	v_fmamk_f32 v2, v2, 0x3a800000, v214
	s_mov_b64 s[4:5], 0
	v_add_co_u32_e32 v76, vcc, s93, v116
	v_rsq_f32_e32 v2, v2
	s_nop 0
	v_cvt_pk_bf16_f32 v68, v52, v53
	v_cvt_pk_bf16_f32 v69, v54, v55
	v_cvt_pk_bf16_f32 v70, v56, v57
	v_cvt_pk_bf16_f32 v71, v58, v59
	v_cvt_pk_bf16_f32 v72, v60, v61
	s_nop 0
	v_addc_co_u32_e32 v77, vcc, 0, v117, vcc
	global_store_dwordx4 v[76:77], v[68:71], off sc1
	global_store_dwordx4 v[76:77], v[72:75], off offset:1024 sc1
	v_pk_mul_f32 v[76:77], v[60:61], v[2:3] op_sel_hi:[1,0]
	v_pk_mul_f32 v[68:69], v[52:53], v[2:3] op_sel_hi:[1,0]
	v_pk_mul_f32 v[70:71], v[54:55], v[2:3] op_sel_hi:[1,0]
	v_pk_mul_f32 v[72:73], v[56:57], v[2:3] op_sel_hi:[1,0]
	v_pk_mul_f32 v[70:71], v[26:27], v[70:71]
	v_pk_mul_f32 v[68:69], v[24:25], v[68:69]
	v_pk_mul_f32 v[72:73], v[20:21], v[72:73]
	v_pk_mul_f32 v[76:77], v[32:33], v[76:77]
	v_pk_mul_f32 v[74:75], v[58:59], v[2:3] op_sel_hi:[1,0]
	v_cvt_pk_bf16_f32 v68, v68, v69
	v_cvt_pk_bf16_f32 v69, v70, v71
	v_cvt_pk_bf16_f32 v70, v72, v73
	v_cvt_pk_bf16_f32 v72, v76, v77
	v_add_co_u32_e32 v76, vcc, 0xb001000, v114
	v_pk_mul_f32 v[74:75], v[22:23], v[74:75]
	v_pk_mul_f32 v[78:79], v[62:63], v[2:3] op_sel_hi:[1,0]
	v_pk_mul_f32 v[80:81], v[64:65], v[2:3] op_sel_hi:[1,0]
	v_pk_mul_f32 v[82:83], v[66:67], v[2:3] op_sel_hi:[1,0]
	v_cvt_pk_bf16_f32 v71, v74, v75
	v_addc_co_u32_e32 v77, vcc, 0, v115, vcc
	v_pk_mul_f32 v[78:79], v[34:35], v[78:79]
	v_pk_mul_f32 v[82:83], v[30:31], v[82:83]
	v_pk_mul_f32 v[80:81], v[28:29], v[80:81]
	v_cvt_pk_bf16_f32 v73, v78, v79
	v_cvt_pk_bf16_f32 v75, v82, v83
	s_nop 0
	v_cvt_pk_bf16_f32 v74, v80, v81
	flat_store_dwordx4 v[76:77], v[68:71] sc1
	flat_store_dwordx4 v[76:77], v[72:75] offset:1024 sc1
.LBB0_744:
	s_andn2_b64 vcc, exec, s[4:5]
	s_cbranch_vccnz .LBB0_746
	global_store_dwordx4 v[112:113], v[52:55], off offset:-2064 sc1
	global_store_dwordx4 v[112:113], v[56:59], off offset:-2048 sc1
	global_store_dwordx4 v[112:113], v[60:63], off offset:-16 sc1
	global_store_dwordx4 v[112:113], v[64:67], off sc1
.LBB0_746:
	s_nop 0
	v_lshlrev_b32_e32 v60, 16, v44
	v_and_b32_e32 v61, 0xffff0000, v44
	v_mul_f32_e32 v2, v60, v60
	v_lshlrev_b32_e32 v44, 16, v45
	v_pk_fma_f32 v[62:63], v[60:61], v[60:61], v[2:3] op_sel_hi:[1,1,0]
	v_and_b32_e32 v45, 0xffff0000, v45
	v_mul_f32_e32 v2, v44, v44
	v_lshlrev_b32_e32 v67, 16, v47
	v_lshlrev_b32_e32 v66, 16, v46
	v_and_b32_e32 v47, 0xffff0000, v47
	v_and_b32_e32 v46, 0xffff0000, v46
	v_lshlrev_b32_e32 v70, 16, v40
	v_lshlrev_b32_e32 v52, 16, v42
	v_pk_fma_f32 v[64:65], v[44:45], v[44:45], v[2:3] op_sel_hi:[1,1,0]
	v_pk_mul_f32 v[68:69], v[46:47], v[46:47]
	v_and_b32_e32 v71, 0xffff0000, v40
	v_mul_f32_e32 v2, v70, v70
	v_lshlrev_b32_e32 v74, 16, v41
	v_pk_fma_f32 v[68:69], v[66:67], v[66:67], v[68:69]
	v_pk_fma_f32 v[72:73], v[70:71], v[70:71], v[2:3] op_sel_hi:[1,1,0]
	v_and_b32_e32 v75, 0xffff0000, v41
	v_mul_f32_e32 v2, v74, v74
	v_mov_b32_e32 v53, v63
	v_mov_b32_e32 v76, v52
	v_mov_b32_e32 v77, v65
	v_and_b32_e32 v78, 0xffff0000, v42
	v_lshlrev_b32_e32 v54, 16, v43
	v_and_b32_e32 v55, 0xffff0000, v43
	v_pk_add_f32 v[68:69], v[68:69], v[68:69] op_sel_hi:[0,1]
	v_pk_fma_f32 v[40:41], v[74:75], v[74:75], v[2:3] op_sel_hi:[1,1,0]
	v_pk_mul_f32 v[76:77], v[52:53], v[76:77]
	v_pk_add_f32 v[62:63], v[62:63], v[64:65]
	v_mul_f32_e32 v68, v78, v78
	v_mul_f32_e32 v72, v54, v54
	v_mul_f32_e32 v40, v55, v55
	v_mov_b32_e32 v77, v63
	v_pk_add_f32 v[62:63], v[76:77], v[68:69]
	v_pk_add_f32 v[40:41], v[72:73], v[40:41]
	v_lshlrev_b32_e32 v58, 16, v36
	v_pk_add_f32 v[40:41], v[62:63], v[40:41]
	v_and_b32_e32 v59, 0xffff0000, v36
	v_add_f32_e32 v2, v40, v41
	v_lshlrev_b32_e32 v62, 16, v37
	v_and_b32_e32 v63, 0xffff0000, v37
	v_add_f32_dpp v2, v2, v2 quad_perm:[1,0,3,2] row_mask:0xf bank_mask:0xf bound_ctrl:1
	v_lshlrev_b32_e32 v64, 16, v38
	v_and_b32_e32 v65, 0xffff0000, v38
	v_add_f32_dpp v2, v2, v2 quad_perm:[2,3,0,1] row_mask:0xf bank_mask:0xf bound_ctrl:1
	v_lshlrev_b32_e32 v68, 16, v39
	v_and_b32_e32 v69, 0xffff0000, v39
	v_add_f32_dpp v2, v2, v2 row_half_mirror row_mask:0xf bank_mask:0xf bound_ctrl:1
	v_lshlrev_b32_e32 v42, 16, v48
	v_and_b32_e32 v43, 0xffff0000, v48
	v_add_f32_dpp v2, v2, v2 row_mirror row_mask:0xf bank_mask:0xf bound_ctrl:1
	v_lshlrev_b32_e32 v48, 16, v49
	v_readlane_b32 s1, v2, 16
	v_readlane_b32 s9, v2, 48
	v_readlane_b32 s4, v2, 0
	v_readlane_b32 s5, v2, 32
	v_mov_b32_e32 v40, s1
	v_mov_b32_e32 v41, s9
	v_pk_add_f32 v[40:41], s[4:5], v[40:41]
	v_and_b32_e32 v49, 0xffff0000, v49
	v_add_f32_e32 v2, v40, v41
	v_fmamk_f32 v2, v2, 0x3a800000, v214
	v_mov_b32_e32 v41, v46
	v_mov_b32_e32 v46, v67
	v_lshlrev_b32_e32 v56, 16, v50
	v_and_b32_e32 v57, 0xffff0000, v50
	v_lshlrev_b32_e32 v50, 16, v51
	v_and_b32_e32 v51, 0xffff0000, v51
	v_mov_b32_e32 v53, v78
	v_rsq_f32_e32 v2, v2
	s_nop 0
	v_mul_f32_e32 v2, 0.5, v2
	v_pk_mul_f32 v[36:37], v[2:3], v[60:61] op_sel_hi:[0,1]
	v_pk_mul_f32 v[38:39], v[2:3], v[44:45] op_sel_hi:[0,1]
	v_pk_fma_f32 v[36:37], v[8:9], v[36:37], v[42:43]
	v_mov_b32_e32 v40, v66
	v_pk_mul_f32 v[42:43], v[2:3], v[46:47] op_sel_hi:[0,1]
	v_pk_fma_f32 v[38:39], v[10:11], v[38:39], v[48:49]
	v_pk_mul_f32 v[40:41], v[2:3], v[40:41] op_sel_hi:[0,1]
	v_pk_fma_f32 v[42:43], v[6:7], v[42:43], v[50:51]
	v_pk_mul_f32 v[44:45], v[2:3], v[70:71] op_sel_hi:[0,1]
	v_pk_mul_f32 v[46:47], v[2:3], v[74:75] op_sel_hi:[0,1]
	v_pk_mul_f32 v[48:49], v[52:53], v[2:3] op_sel_hi:[1,0]
	v_pk_mul_f32 v[50:51], v[54:55], v[2:3] op_sel_hi:[1,0]
	v_pk_fma_f32 v[40:41], v[4:5], v[40:41], v[56:57]
	v_pk_fma_f32 v[46:47], v[18:19], v[46:47], v[62:63]
	v_pk_fma_f32 v[44:45], v[16:17], v[44:45], v[58:59]
	v_pk_fma_f32 v[50:51], v[14:15], v[50:51], v[68:69]
	v_pk_fma_f32 v[48:49], v[12:13], v[48:49], v[64:65]
	s_and_b64 vcc, exec, s[2:3]
	s_mov_b64 s[2:3], -1
	s_cbranch_vccnz .LBB0_748
; __device__ __forceinline__ unsigned pk2(float lo, float hi) { unsigned r; asm("v_cvt_pk_bf16_f32 %0, %1, %2" : "=v"(r) : "v"(lo), "v"(hi)); return r; }
; __device__ __forceinline__ void thin_pass(const Ctx& C, const bf16* hin, bf16* hout, bf16* u, float* out, const bf16* y, const float* gpost, float cmul, const float* gpre, bool last) {
;     ...
;             if (last) { f32x4* op = (f32x4*)(out + (size_t)m * D); op[2 * lane] = h[0]; op[2 * lane + 1] = h[1]; op[128 + 2 * lane] = h[2]; op[128 + 2 * lane + 1] = h[3]; }
;             else {
;                 float s2 = 0.f;
; #pragma unroll
;                 for (int i = 0; i < 4; ++i) s2 += (h[i][0] * h[i][0] + h[i][1] * h[i][1]) + (h[i][2] * h[i][2] + h[i][3] * h[i][3]);
;                 const float rh = 1.0f / sqrtf(wave_sum(s2) * (1.0f / D) + RMS_EPS);
;                 v4u o0, o1; o0.x = pk2(h[0][0], h[0][1]); o0.y = pk2(h[0][2], h[0][3]); o0.z = pk2(h[1][0], h[1][1]); o0.w = pk2(h[1][2], h[1][3]);
;                 o1.x = pk2(h[2][0], h[2][1]); o1.y = pk2(h[2][2], h[2][3]); o1.z = pk2(h[3][0], h[3][1]); o1.w = pk2(h[3][2], h[3][3]);
;                 v4u* hp = (v4u*)(hout + (size_t)m * D); hp[lane] = o0; hp[64 + lane] = o1;
; #pragma unroll
;                 for (int i = 0; i < 4; ++i) h[i] = h[i] * rh * q4[i];
;                 o0.x = pk2(h[0][0], h[0][1]); o0.y = pk2(h[0][2], h[0][3]); o0.z = pk2(h[1][0], h[1][1]); o0.w = pk2(h[1][2], h[1][3]);
;                 o1.x = pk2(h[2][0], h[2][1]); o1.y = pk2(h[2][2], h[2][3]); o1.z = pk2(h[3][0], h[3][1]); o1.w = pk2(h[3][2], h[3][3]);
;                 v4u* up = (v4u*)(u + (size_t)m * D); up[lane] = o0; up[64 + lane] = o1;
	v_pk_mul_f32 v[52:53], v[38:39], v[38:39]
	v_pk_mul_f32 v[54:55], v[36:37], v[36:37]
	v_mul_f32_e32 v2, v44, v44
	v_pk_mov_b32 v[56:57], v[54:55], v[52:53] op_sel:[1,0]
	v_mov_b32_e32 v55, v53
	v_pk_add_f32 v[52:53], v[56:57], v[54:55]
	v_pk_mul_f32 v[54:55], v[42:43], v[42:43]
	v_pk_mul_f32 v[56:57], v[40:41], v[40:41]
	v_pk_add_f32 v[52:53], v[52:53], v[52:53] op_sel_hi:[0,1]
	v_pk_mov_b32 v[58:59], v[56:57], v[54:55] op_sel:[1,0]
	v_mov_b32_e32 v57, v55
	v_pk_add_f32 v[54:55], v[58:59], v[56:57]
	v_pk_fma_f32 v[56:57], v[44:45], v[44:45], v[2:3] op_sel_hi:[1,1,0]
	v_mul_f32_e32 v2, v46, v46
	v_pk_add_f32 v[54:55], v[54:55], v[54:55] op_sel_hi:[0,1]
	v_pk_fma_f32 v[58:59], v[46:47], v[46:47], v[2:3] op_sel_hi:[1,1,0]
	v_mul_f32_e32 v56, v48, v48
	v_mul_f32_e32 v58, v49, v49
	v_mul_f32_e32 v52, v50, v50
	v_mul_f32_e32 v54, v51, v51
	v_pk_add_f32 v[56:57], v[56:57], v[58:59]
	v_pk_add_f32 v[52:53], v[52:53], v[54:55]
	v_cvt_pk_bf16_f32 v58, v48, v49
	v_cvt_pk_bf16_f32 v59, v50, v51
	s_nop 0
	v_pk_add_f32 v[52:53], v[56:57], v[52:53]
	v_cvt_pk_bf16_f32 v57, v46, v47
	s_nop 0
	v_add_f32_e32 v2, v52, v53
	s_nop 1
	v_add_f32_dpp v2, v2, v2 quad_perm:[1,0,3,2] row_mask:0xf bank_mask:0xf bound_ctrl:1
	s_nop 1
	v_add_f32_dpp v2, v2, v2 quad_perm:[2,3,0,1] row_mask:0xf bank_mask:0xf bound_ctrl:1
	s_nop 1
	v_add_f32_dpp v2, v2, v2 row_half_mirror row_mask:0xf bank_mask:0xf bound_ctrl:1
	s_nop 1
	v_add_f32_dpp v2, v2, v2 row_mirror row_mask:0xf bank_mask:0xf bound_ctrl:1
	s_nop 0
	v_readlane_b32 s1, v2, 16
	v_readlane_b32 s4, v2, 48
	v_readlane_b32 s2, v2, 0
	v_readlane_b32 s3, v2, 32
	v_mov_b32_e32 v52, s1
	v_mov_b32_e32 v53, s4
	v_pk_add_f32 v[52:53], s[2:3], v[52:53]
	s_nop 0
	v_add_f32_e32 v2, v52, v53
	v_fmamk_f32 v2, v2, 0x3a800000, v214
	s_lshl_b64 s[2:3], s[22:23], 10
	s_lshl_b64 s[2:3], s[2:3], 1
	v_lshl_add_u64 v[60:61], v[106:107], 0, s[2:3]
	v_rsq_f32_e32 v2, v2
	s_nop 0
	v_cvt_pk_bf16_f32 v52, v36, v37
	v_cvt_pk_bf16_f32 v53, v38, v39
	v_cvt_pk_bf16_f32 v54, v40, v41
	v_cvt_pk_bf16_f32 v55, v42, v43
	v_cvt_pk_bf16_f32 v56, v44, v45
	global_store_dwordx4 v[60:61], v[52:55], off sc1
	global_store_dwordx4 v[60:61], v[56:59], off offset:1024 sc1
	v_pk_mul_f32 v[60:61], v[44:45], v[2:3] op_sel_hi:[1,0]
	v_pk_mul_f32 v[52:53], v[36:37], v[2:3] op_sel_hi:[1,0]
	v_pk_mul_f32 v[54:55], v[38:39], v[2:3] op_sel_hi:[1,0]
	v_pk_mul_f32 v[56:57], v[40:41], v[2:3] op_sel_hi:[1,0]
	v_pk_mul_f32 v[54:55], v[26:27], v[54:55]
	v_pk_mul_f32 v[52:53], v[24:25], v[52:53]
	v_pk_mul_f32 v[58:59], v[42:43], v[2:3] op_sel_hi:[1,0]
	v_pk_mul_f32 v[56:57], v[20:21], v[56:57]
	v_pk_mul_f32 v[60:61], v[32:33], v[60:61]
	v_pk_mul_f32 v[58:59], v[22:23], v[58:59]
	v_pk_mul_f32 v[62:63], v[46:47], v[2:3] op_sel_hi:[1,0]
	v_pk_mul_f32 v[64:65], v[48:49], v[2:3] op_sel_hi:[1,0]
	v_pk_mul_f32 v[66:67], v[50:51], v[2:3] op_sel_hi:[1,0]
	v_cvt_pk_bf16_f32 v52, v52, v53
	v_cvt_pk_bf16_f32 v53, v54, v55
	v_cvt_pk_bf16_f32 v54, v56, v57
	v_cvt_pk_bf16_f32 v55, v58, v59
	v_cvt_pk_bf16_f32 v56, v60, v61
	v_lshl_add_u64 v[60:61], v[108:109], 0, s[2:3]
	s_mov_b64 s[2:3], 0
	v_pk_mul_f32 v[62:63], v[34:35], v[62:63]
	v_pk_mul_f32 v[66:67], v[30:31], v[66:67]
	v_pk_mul_f32 v[64:65], v[28:29], v[64:65]
	v_cvt_pk_bf16_f32 v57, v62, v63
	v_cvt_pk_bf16_f32 v59, v66, v67
	s_nop 0
	v_cvt_pk_bf16_f32 v58, v64, v65
	flat_store_dwordx4 v[60:61], v[52:55] sc1
	flat_store_dwordx4 v[60:61], v[56:59] offset:1024 sc1
.LBB0_748:
	s_andn2_b64 vcc, exec, s[2:3]
	s_cbranch_vccnz .LBB0_733
	s_lshl_b64 s[2:3], s[22:23], 12
	v_lshl_add_u64 v[52:53], v[110:111], 0, s[2:3]
	global_store_dwordx4 v[52:53], v[36:39], off sc1
	global_store_dwordx4 v[52:53], v[40:43], off offset:16 sc1
	global_store_dwordx4 v[52:53], v[44:47], off offset:2048 sc1
	global_store_dwordx4 v[52:53], v[48:51], off offset:2064 sc1
	s_branch .LBB0_733

; #define GAS __attribute__((address_space(1)))
; __device__ __forceinline__ void fox_flog_tasks(const Ctx& C, const bf16* U, const bf16* WfT, float* flog) {
;     if (C.wave >= 4) return;
;     const int fr = C.lane & 15, fq = C.lane >> 4;
;     for (int task = C.vcu * 4 + C.wave; task < M / 16; task += C.G * 4) {
;         const GAS bf16x8_t* ap = (const GAS bf16x8_t*)(U + (size_t)(task * 16 + fr) * D + 8 * fq); const GAS bf16x8_t* bp = (const GAS bf16x8_t*)(WfT + (size_t)fr * D + 8 * fq);
;         f32x4 acc = (f32x4){0.f, 0.f, 0.f, 0.f};
; #pragma unroll
;         for (int kb = 0; kb < D / 32; kb += 16) {
;             bf16x8_t a[16], b[16];
; #pragma unroll
;             for (int j = 0; j < 16; ++j) { a[j] = ap[4 * (kb + j)]; b[j] = bp[4 * (kb + j)]; }
; #pragma unroll
;             for (int j = 0; j < 16; ++j) acc = __builtin_amdgcn_mfma_f32_16x16x32_bf16(a[j], b[j], acc, 0, 0, 0);
.LBB0_806:
	v_add_u32_e32 v4, s14, v2
	v_ashrrev_i32_e32 v5, 31, v4
	v_lshlrev_b64 v[4:5], 11, v[4:5]
	v_lshl_add_u64 v[98:99], v[92:93], 0, v[4:5]
	global_load_dwordx4 v[4:7], v[98:99], off
	global_load_dwordx4 v[8:11], v[94:95], off
	global_load_dwordx4 v[12:15], v[98:99], off offset:64
	global_load_dwordx4 v[16:19], v[94:95], off offset:64
	global_load_dwordx4 v[20:23], v[98:99], off offset:128
	global_load_dwordx4 v[24:27], v[94:95], off offset:128
	global_load_dwordx4 v[28:31], v[98:99], off offset:192
	global_load_dwordx4 v[32:35], v[94:95], off offset:192
	global_load_dwordx4 v[36:39], v[98:99], off offset:256
	global_load_dwordx4 v[40:43], v[94:95], off offset:256
	global_load_dwordx4 v[44:47], v[98:99], off offset:320
	global_load_dwordx4 v[48:51], v[94:95], off offset:320
	global_load_dwordx4 v[52:55], v[98:99], off offset:384
	global_load_dwordx4 v[56:59], v[94:95], off offset:384
	global_load_dwordx4 v[60:63], v[98:99], off offset:448
	global_load_dwordx4 v[64:67], v[94:95], off offset:448
	global_load_dwordx4 v[68:71], v[98:99], off offset:512
	global_load_dwordx4 v[72:75], v[94:95], off offset:512
	global_load_dwordx4 v[76:79], v[98:99], off offset:576
	global_load_dwordx4 v[80:83], v[94:95], off offset:576
	global_load_dwordx4 v[84:87], v[98:99], off offset:640
	global_load_dwordx4 v[88:91], v[94:95], off offset:640
	global_load_dwordx4 v[102:105], v[98:99], off offset:704
	global_load_dwordx4 v[106:109], v[94:95], off offset:704
	global_load_dwordx4 v[110:113], v[98:99], off offset:768
	global_load_dwordx4 v[114:117], v[94:95], off offset:768
	global_load_dwordx4 v[118:121], v[98:99], off offset:832
	global_load_dwordx4 v[122:125], v[94:95], off offset:832
	global_load_dwordx4 v[126:129], v[98:99], off offset:896
	global_load_dwordx4 v[130:133], v[94:95], off offset:896
	global_load_dwordx4 v[134:137], v[98:99], off offset:960
	global_load_dwordx4 v[138:141], v[94:95], off offset:960
	s_add_i32 s12, s12, s13
	s_waitcnt vmcnt(0)
	v_mfma_f32_16x16x32_bf16 v[4:7], v[4:7], v[8:11], 0
	s_waitcnt vmcnt(28)
	v_mfma_f32_16x16x32_bf16 v[4:7], v[12:15], v[16:19], v[4:7]
	s_waitcnt vmcnt(26)
	v_mfma_f32_16x16x32_bf16 v[4:7], v[20:23], v[24:27], v[4:7]
	s_waitcnt vmcnt(24)
	v_mfma_f32_16x16x32_bf16 v[4:7], v[28:31], v[32:35], v[4:7]
	s_waitcnt vmcnt(22)
	v_mfma_f32_16x16x32_bf16 v[4:7], v[36:39], v[40:43], v[4:7]
	s_waitcnt vmcnt(20)
	v_mfma_f32_16x16x32_bf16 v[4:7], v[44:47], v[48:51], v[4:7]
	s_waitcnt vmcnt(18)
	v_mfma_f32_16x16x32_bf16 v[4:7], v[52:55], v[56:59], v[4:7]
	s_waitcnt vmcnt(16)
	v_mfma_f32_16x16x32_bf16 v[4:7], v[60:63], v[64:67], v[4:7]
	s_waitcnt vmcnt(14)
	v_mfma_f32_16x16x32_bf16 v[4:7], v[68:71], v[72:75], v[4:7]
	s_waitcnt vmcnt(12)
	v_mfma_f32_16x16x32_bf16 v[4:7], v[76:79], v[80:83], v[4:7]
	s_waitcnt vmcnt(10)
	v_mfma_f32_16x16x32_bf16 v[4:7], v[84:87], v[88:91], v[4:7]
	s_waitcnt vmcnt(8)
	v_mfma_f32_16x16x32_bf16 v[4:7], v[102:105], v[106:109], v[4:7]
	s_waitcnt vmcnt(6)
	v_mfma_f32_16x16x32_bf16 v[4:7], v[110:113], v[114:117], v[4:7]
	s_waitcnt vmcnt(4)
	v_mfma_f32_16x16x32_bf16 v[4:7], v[118:121], v[122:125], v[4:7]
	s_waitcnt vmcnt(2)
	v_mfma_f32_16x16x32_bf16 v[4:7], v[126:129], v[130:133], v[4:7]
	s_waitcnt vmcnt(0)
; __device__ __forceinline__ void fox_flog_tasks(const Ctx& C, const bf16* U, const bf16* WfT, float* flog) {
;     ...
;         for (int kb = 0; kb < D / 32; kb += 16) {
;             bf16x8_t a[16], b[16];
; #pragma unroll
;             for (int j = 0; j < 16; ++j) { a[j] = ap[4 * (kb + j)]; b[j] = bp[4 * (kb + j)]; }
; #pragma unroll
;             for (int j = 0; j < 16; ++j) acc = __builtin_amdgcn_mfma_f32_16x16x32_bf16(a[j], b[j], acc, 0, 0, 0);
;         }
; #pragma unroll
;         for (int e = 0; e < 4; ++e) flog[(size_t)(task * 16 + 4 * fq + e) * 16 + fr] = acc[e];
	v_mfma_f32_16x16x32_bf16 v[4:7], v[134:137], v[138:141], v[4:7]
	global_load_dwordx4 v[8:11], v[98:99], off offset:1024
	global_load_dwordx4 v[28:31], v[94:95], off offset:1024
	global_load_dwordx4 v[12:15], v[98:99], off offset:1088
	global_load_dwordx4 v[36:39], v[94:95], off offset:1088
	global_load_dwordx4 v[16:19], v[98:99], off offset:1152
	global_load_dwordx4 v[44:47], v[94:95], off offset:1152
	global_load_dwordx4 v[20:23], v[98:99], off offset:1216
	global_load_dwordx4 v[52:55], v[94:95], off offset:1216
	global_load_dwordx4 v[24:27], v[98:99], off offset:1280
	global_load_dwordx4 v[60:63], v[94:95], off offset:1280
	global_load_dwordx4 v[32:35], v[98:99], off offset:1344
	global_load_dwordx4 v[64:67], v[94:95], off offset:1344
	global_load_dwordx4 v[40:43], v[98:99], off offset:1408
	global_load_dwordx4 v[68:71], v[94:95], off offset:1408
	global_load_dwordx4 v[48:51], v[98:99], off offset:1472
	global_load_dwordx4 v[72:75], v[94:95], off offset:1472
	global_load_dwordx4 v[56:59], v[98:99], off offset:1536
	global_load_dwordx4 v[76:79], v[94:95], off offset:1536
	global_load_dwordx4 v[80:83], v[98:99], off offset:1600
	global_load_dwordx4 v[84:87], v[94:95], off offset:1600
	global_load_dwordx4 v[88:91], v[98:99], off offset:1664
	global_load_dwordx4 v[102:105], v[94:95], off offset:1664
	global_load_dwordx4 v[106:109], v[98:99], off offset:1728
	global_load_dwordx4 v[110:113], v[94:95], off offset:1728
	global_load_dwordx4 v[114:117], v[98:99], off offset:1792
	global_load_dwordx4 v[118:121], v[94:95], off offset:1792
	global_load_dwordx4 v[122:125], v[98:99], off offset:1856
	global_load_dwordx4 v[126:129], v[94:95], off offset:1856
	global_load_dwordx4 v[130:133], v[98:99], off offset:1920
	global_load_dwordx4 v[134:137], v[94:95], off offset:1920
	global_load_dwordx4 v[138:141], v[98:99], off offset:1984
	global_load_dwordx4 v[142:145], v[94:95], off offset:1984
	s_waitcnt vmcnt(0)
	v_mfma_f32_16x16x32_bf16 v[4:7], v[8:11], v[28:31], v[4:7]
	v_add_u32_e32 v8, s14, v100
	v_ashrrev_i32_e32 v9, 31, v8
	v_lshlrev_b64 v[10:11], 6, v[8:9]
	s_waitcnt vmcnt(28)
	v_mfma_f32_16x16x32_bf16 v[4:7], v[12:15], v[36:39], v[4:7]
	v_lshl_add_u64 v[10:11], v[96:97], 0, v[10:11]
	s_add_i32 s14, s14, s15
	s_cmpk_lt_i32 s12, 0x400
	s_waitcnt vmcnt(26)
	v_mfma_f32_16x16x32_bf16 v[4:7], v[16:19], v[44:47], v[4:7]
	s_waitcnt vmcnt(24)
	v_mfma_f32_16x16x32_bf16 v[4:7], v[20:23], v[52:55], v[4:7]
	s_waitcnt vmcnt(22)
	v_mfma_f32_16x16x32_bf16 v[4:7], v[24:27], v[60:63], v[4:7]
	s_waitcnt vmcnt(20)
	v_mfma_f32_16x16x32_bf16 v[4:7], v[32:35], v[64:67], v[4:7]
	s_waitcnt vmcnt(18)
	v_mfma_f32_16x16x32_bf16 v[4:7], v[40:43], v[68:71], v[4:7]
	s_waitcnt vmcnt(16)
	v_mfma_f32_16x16x32_bf16 v[4:7], v[48:51], v[72:75], v[4:7]
	s_waitcnt vmcnt(14)
	v_mfma_f32_16x16x32_bf16 v[4:7], v[56:59], v[76:79], v[4:7]
	s_waitcnt vmcnt(12)
	v_mfma_f32_16x16x32_bf16 v[4:7], v[80:83], v[84:87], v[4:7]
	s_waitcnt vmcnt(10)
	v_mfma_f32_16x16x32_bf16 v[4:7], v[88:91], v[102:105], v[4:7]
	s_waitcnt vmcnt(8)
	v_mfma_f32_16x16x32_bf16 v[4:7], v[106:109], v[110:113], v[4:7]
	s_waitcnt vmcnt(6)
	v_mfma_f32_16x16x32_bf16 v[4:7], v[114:117], v[118:121], v[4:7]
	s_waitcnt vmcnt(4)
	v_mfma_f32_16x16x32_bf16 v[4:7], v[122:125], v[126:129], v[4:7]
	s_waitcnt vmcnt(2)
	v_mfma_f32_16x16x32_bf16 v[4:7], v[130:133], v[134:137], v[4:7]
	s_waitcnt vmcnt(0)
	v_mfma_f32_16x16x32_bf16 v[4:7], v[138:141], v[142:145], v[4:7]
	s_nop 7
	flat_store_dword v[10:11], v4 sc1
	v_add_u32_e32 v10, 1, v8
	v_ashrrev_i32_e32 v11, 31, v10
	v_lshlrev_b64 v[10:11], 6, v[10:11]
	v_lshl_add_u64 v[10:11], v[96:97], 0, v[10:11]
	v_add_u32_e32 v4, 2, v8
	flat_store_dword v[10:11], v5 sc1
	v_ashrrev_i32_e32 v5, 31, v4
	v_lshlrev_b64 v[4:5], 6, v[4:5]
	v_lshl_add_u64 v[4:5], v[96:97], 0, v[4:5]
	flat_store_dword v[4:5], v6 sc1
	v_add_u32_e32 v4, 3, v8
	v_ashrrev_i32_e32 v5, 31, v4
	v_lshlrev_b64 v[4:5], 6, v[4:5]
	v_lshl_add_u64 v[4:5], v[96:97], 0, v[4:5]
	flat_store_dword v[4:5], v7 sc1
	s_cbranch_scc1 .LBB0_806

; __device__ __forceinline__ unsigned xb_ld(unsigned* p)              { return __hip_atomic_load(p, __ATOMIC_RELAXED, __HIP_MEMORY_SCOPE_AGENT); }
; __device__ __forceinline__ unsigned xb_add(unsigned* p, unsigned v) { return __hip_atomic_fetch_add(p, v, __ATOMIC_RELAXED, __HIP_MEMORY_SCOPE_AGENT); }
; #define XB_SPIN(cond, bar) do { unsigned _sp = 0; while (cond) { __builtin_amdgcn_s_sleep(1); \
;     if ((++_sp & 255u) == 0u) { if (xb_ld(&(bar)[XB_TMO])) break; if (_sp > XB_SPIN_CAP) { atomicAdd(&(bar)[XB_TMO], 1u); break; } } } } while (0)
; __device__ __forceinline__ void xcd_barrier(const XcdBarrier& b) {
;     ...
;         const unsigned old = xb_add(&bar[XB_XSUB(b.x)], 1u);
;         const unsigned gen = old / nloc;
;         if (old + 1u == (gen + 1u) * nloc) {
;             __builtin_amdgcn_fence(__ATOMIC_RELEASE, "agent");
;             asm volatile("s_waitcnt vmcnt(0)" ::: "memory");
;             const unsigned og = xb_add(&bar[XB_TOP], 1u);
;             const unsigned tg = og / nx;
;             if (og + 1u == (tg + 1u) * nx) xb_add(&bar[XB_TOPGEN], 1u);
;             else XB_SPIN(xb_ld(&bar[XB_TOPGEN]) == tg, bar);
.LBB0_858:
	s_andn2_saveexec_b64 s[4:5], s[4:5]
	s_cbranch_execz .LBB0_874
	v_mov_b32_e32 v4, s40
	v_add_co_u32_e32 v4, vcc, 0x3000, v4
	v_mov_b32_e32 v5, s41
	s_waitcnt vmcnt(0)
	v_addc_co_u32_e32 v5, vcc, 0, v5, vcc
	flat_atomic_add v4, v[4:5], v1 offset:1024 sc0
	v_cvt_f32_u32_e32 v5, v2
	v_sub_u32_e32 v6, 0, v2
	s_mov_b64 s[8:9], -1
	v_rcp_iflag_f32_e32 v5, v5
	s_nop 0
	v_mul_f32_e32 v5, 0x4f7ffffe, v5
	v_cvt_u32_f32_e32 v5, v5
	v_mul_lo_u32 v6, v6, v5
	v_mul_hi_u32 v6, v5, v6
	v_add_u32_e32 v5, v5, v6
	s_waitcnt vmcnt(0) lgkmcnt(0)
	v_mul_hi_u32 v5, v4, v5
	v_mul_lo_u32 v6, v5, v2
	v_sub_u32_e32 v6, v4, v6
	v_cmp_ge_u32_e32 vcc, v6, v2
	v_add_u32_e32 v7, 1, v5
	s_nop 0
	v_cndmask_b32_e32 v5, v5, v7, vcc
	v_sub_u32_e32 v7, v6, v2
	v_cndmask_b32_e32 v6, v6, v7, vcc
	v_cmp_ge_u32_e32 vcc, v6, v2
	v_add_u32_e32 v6, 1, v5
	v_add_u32_e32 v7, 1, v4
	v_cndmask_b32_e32 v6, v5, v6, vcc
	v_mad_u64_u32 v[4:5], s[4:5], v2, v6, v[2:3]
	s_add_u32 s4, s40, 0x3500
	s_addc_u32 s5, s41, 0
	v_cmp_ne_u32_e32 vcc, v7, v4
	v_mov_b64_e32 v[4:5], s[4:5]
	s_and_saveexec_b64 s[6:7], vcc
	s_cbranch_execz .LBB0_871
	v_mov_b64_e32 v[4:5], s[4:5]
	flat_load_dword v2, v[4:5] sc1
	s_mov_b64 s[12:13], 0
	s_waitcnt vmcnt(0) lgkmcnt(0)
	v_cmp_eq_u32_e32 vcc, v2, v6
	s_and_saveexec_b64 s[10:11], vcc
	s_cbranch_execz .LBB0_870
	s_add_u32 s8, s40, 0x200
	s_addc_u32 s9, s41, 0
	s_mov_b32 s24, 1
	s_branch .LBB0_863

; __device__ __forceinline__ int crow(int r,int hi){return (r&3)+8*(r>>2)+4*hi;}
;     ...
;   float rli[16];
;   #pragma unroll
;   for(int r=0;r<16;++r)rli[r]=__builtin_amdgcn_rcpf(wsf[32+crow(r,hi)]);
;   bf16*Ow=O+(rowbase+q0+wid*QBLK)*DM+h*D;
;   { bf16*stg=(bf16*)(shm+LDS_OST)+wid*2048;
;     #pragma unroll
;     for(int r=0;r<16;++r){const int orow=crow(r,hi);
;       #pragma unroll
;       for(int d0=0;d0<2;++d0)stg[orow*64+d0*32+r32]=__float2bfloat16(o[d0][r]*rli[r]);}
;     asm volatile("s_waitcnt lgkmcnt(0)":::"memory");
;     #pragma unroll
;     for(int i=0;i<4;++i){const int row=i*8+(lane>>3),ch=lane&7; const u32x4 v=*(const u32x4*)(stg+row*64+ch*8); ATTN_STORE16(Ow+(long)row*DM+ch*8,v);} }
;   asm volatile("s_waitcnt lgkmcnt(0)\n\ts_barrier":::"memory");
.LBB0_930:
	s_or_b64 exec, exec, s[4:5]
	s_waitcnt lgkmcnt(0)
	ds_read_b128 v[36:39], v233 offset:49280
	ds_read_b128 v[40:43], v233 offset:49312
	s_lshl_b32 s4, s55, 12
	s_add_i32 s6, s4, 0
	v_lshlrev_b32_e32 v51, 1, v229
	s_waitcnt lgkmcnt(1)
	v_rcp_f32_e32 v2, v36
	v_rcp_f32_e32 v44, v37
	v_lshlrev_b32_e32 v52, 9, v230
	v_add3_u32 v51, s6, v51, v52
	v_mul_f32_e32 v20, v20, v2
	v_mul_f32_e32 v2, v4, v2
	v_cvt_pk_bf16_f32 v2, v2, s0
	v_rcp_f32_e32 v45, v38
	v_rcp_f32_e32 v46, v39
	s_waitcnt lgkmcnt(0)
	v_rcp_f32_e32 v47, v40
	ds_read_b128 v[36:39], v233 offset:49344
	v_rcp_f32_e32 v48, v41
	v_rcp_f32_e32 v49, v42
	v_rcp_f32_e32 v50, v43
	ds_read_b128 v[40:43], v233 offset:49376
	ds_write_b16 v51, v2 offset:51264
	v_mul_f32_e32 v2, v21, v44
	v_cvt_pk_bf16_f32 v2, v2, s0
	ds_write_b16 v51, v2 offset:51328
	v_mul_f32_e32 v2, v5, v44
	v_cvt_pk_bf16_f32 v2, v2, s0
	ds_write_b16 v51, v2 offset:51392
	v_mul_f32_e32 v2, v22, v45
	v_cvt_pk_bf16_f32 v2, v2, s0
	ds_write_b16 v51, v2 offset:51456
	v_mul_f32_e32 v2, v6, v45
	v_cvt_pk_bf16_f32 v2, v2, s0
	ds_write_b16 v51, v2 offset:51520
	v_mul_f32_e32 v2, v23, v46
	v_cvt_pk_bf16_f32 v2, v2, s0
	ds_write_b16 v51, v2 offset:51584
	v_mul_f32_e32 v2, v7, v46
	v_cvt_pk_bf16_f32 v2, v2, s0
	ds_write_b16 v51, v2 offset:51648
	v_mul_f32_e32 v2, v24, v47
	v_cvt_pk_bf16_f32 v2, v2, s0
	ds_write_b16 v51, v2 offset:52224
	v_mul_f32_e32 v2, v8, v47
	v_cvt_pk_bf16_f32 v2, v2, s0
	ds_write_b16 v51, v2 offset:52288
	v_mul_f32_e32 v2, v25, v48
	v_cvt_pk_bf16_f32 v2, v2, s0
	ds_write_b16 v51, v2 offset:52352
	v_mul_f32_e32 v2, v9, v48
	v_cvt_pk_bf16_f32 v2, v2, s0
	ds_write_b16 v51, v2 offset:52416
	v_mul_f32_e32 v2, v26, v49
	v_cvt_pk_bf16_f32 v2, v2, s0
	ds_write_b16 v51, v2 offset:52480
	v_mul_f32_e32 v2, v10, v49
	v_cvt_pk_bf16_f32 v2, v2, s0
	s_waitcnt lgkmcnt(13)
	v_rcp_f32_e32 v36, v36
	ds_write_b16 v51, v2 offset:52544
	v_mul_f32_e32 v2, v27, v50
	v_cvt_pk_bf16_f32 v2, v2, s0
	ds_write_b16 v51, v2 offset:52608
	v_mul_f32_e32 v2, v11, v50
	v_cvt_pk_bf16_f32 v2, v2, s0
	v_rcp_f32_e32 v37, v37
	ds_write_b16 v51, v2 offset:52672
	v_mul_f32_e32 v2, v28, v36
	v_cvt_pk_bf16_f32 v2, v2, s0
	ds_write_b16 v51, v2 offset:53248
	v_mul_f32_e32 v2, v12, v36
	v_cvt_pk_bf16_f32 v2, v2, s0
	v_rcp_f32_e32 v38, v38
	ds_write_b16 v51, v2 offset:53312
	v_mul_f32_e32 v2, v29, v37
	v_cvt_pk_bf16_f32 v2, v2, s0
	ds_write_b16 v51, v2 offset:53376
	v_mul_f32_e32 v2, v13, v37
	v_cvt_pk_bf16_f32 v2, v2, s0
	v_rcp_f32_e32 v39, v39
	ds_write_b16 v51, v2 offset:53440
	v_mul_f32_e32 v2, v30, v38
	v_cvt_pk_bf16_f32 v2, v2, s0
	ds_write_b16 v51, v2 offset:53504
	v_mul_f32_e32 v2, v14, v38
	v_cvt_pk_bf16_f32 v2, v2, s0
	s_waitcnt lgkmcnt(14)
	v_rcp_f32_e32 v40, v40
	ds_write_b16 v51, v2 offset:53568
	v_mul_f32_e32 v2, v31, v39
	v_cvt_pk_bf16_f32 v2, v2, s0
	ds_write_b16 v51, v2 offset:53632
	v_mul_f32_e32 v2, v15, v39
	v_cvt_pk_bf16_f32 v2, v2, s0
	v_rcp_f32_e32 v41, v41
	ds_write_b16 v51, v2 offset:53696
	v_mul_f32_e32 v2, v32, v40
	v_cvt_pk_bf16_f32 v2, v2, s0
	ds_write_b16 v51, v2 offset:54272
	v_mul_f32_e32 v2, v16, v40
	v_cvt_pk_bf16_f32 v2, v2, s0
	v_rcp_f32_e32 v42, v42
	ds_write_b16 v51, v2 offset:54336
	v_mul_f32_e32 v2, v33, v41
	v_cvt_pk_bf16_f32 v2, v2, s0
	ds_write_b16 v51, v2 offset:54400
	v_mul_f32_e32 v2, v17, v41
	v_cvt_pk_bf16_f32 v2, v2, s0
	v_rcp_f32_e32 v43, v43
	ds_write_b16 v51, v2 offset:54464
	v_mul_f32_e32 v2, v34, v42
	v_cvt_pk_bf16_f32 v2, v2, s0
	ds_write_b16 v51, v2 offset:54528
	v_mul_f32_e32 v2, v18, v42
	v_cvt_pk_bf16_f32 v2, v2, s0
	ds_write_b16 v51, v2 offset:54592
	v_mul_f32_e32 v2, v35, v43
	v_cvt_pk_bf16_f32 v2, v2, s0
	ds_write_b16 v51, v2 offset:54656
	v_mul_f32_e32 v2, v19, v43
	v_cvt_pk_bf16_f32 v2, v2, s0
	ds_write_b16 v51, v2 offset:54720
	v_lshlrev_b32_e32 v2, 1, v228
	v_cvt_pk_bf16_f32 v20, v20, s0
	v_and_b32_e32 v2, 0x70, v2
	ds_write_b16 v51, v20 offset:51200
	v_lshrrev_b32_e32 v12, 3, v227
	v_add_u32_e32 v13, s6, v2
	s_waitcnt lgkmcnt(0)
	v_lshl_add_u32 v4, v12, 7, v13
	s_lshl_b64 s[4:5], s[24:25], 1
	ds_read_b128 v[4:7], v4 offset:51200
	s_add_u32 s4, s53, s4
	s_addc_u32 s5, s54, s5
	v_lshl_add_u64 v[8:9], s[4:5], 0, v[2:3]
	v_lshlrev_b32_e32 v2, 11, v12
	v_lshl_add_u64 v[10:11], v[8:9], 0, v[2:3]
	v_or_b32_e32 v2, 8, v12
	s_waitcnt lgkmcnt(0)
	flat_store_dwordx4 v[10:11], v[4:7] sc1
	s_add_i32 s48, s48, 1
	s_cmp_eq_u32 s48, 4
	v_lshl_add_u32 v4, v2, 7, v13
	ds_read_b128 v[4:7], v4 offset:51200
	v_lshlrev_b32_e32 v2, 11, v2
	v_lshl_add_u64 v[10:11], v[8:9], 0, v[2:3]
	v_or_b32_e32 v2, 16, v12
	s_waitcnt lgkmcnt(0)
	flat_store_dwordx4 v[10:11], v[4:7] sc1
	s_nop 1
	v_lshl_add_u32 v4, v2, 7, v13
	ds_read_b128 v[4:7], v4 offset:51200
	v_lshlrev_b32_e32 v2, 11, v2
	v_lshl_add_u64 v[10:11], v[8:9], 0, v[2:3]
	v_or_b32_e32 v2, 24, v12
	s_waitcnt lgkmcnt(0)
	flat_store_dwordx4 v[10:11], v[4:7] sc1
	s_nop 1
	v_lshl_add_u32 v4, v2, 7, v13
	ds_read_b128 v[4:7], v4 offset:51200
	v_lshlrev_b32_e32 v2, 11, v2
	v_lshl_add_u64 v[8:9], v[8:9], 0, v[2:3]
	s_waitcnt lgkmcnt(0)
	flat_store_dwordx4 v[8:9], v[4:7] sc1
	s_waitcnt lgkmcnt(0)
	s_barrier
	s_cbranch_scc1 .LBB0_882

; __device__ __forceinline__ unsigned xb_ld(unsigned* p)              { return __hip_atomic_load(p, __ATOMIC_RELAXED, __HIP_MEMORY_SCOPE_AGENT); }
; __device__ __forceinline__ unsigned xb_add(unsigned* p, unsigned v) { return __hip_atomic_fetch_add(p, v, __ATOMIC_RELAXED, __HIP_MEMORY_SCOPE_AGENT); }
; #define XB_SPIN(cond, bar) do { unsigned _sp = 0; while (cond) { __builtin_amdgcn_s_sleep(1); \
;     if ((++_sp & 255u) == 0u) { if (xb_ld(&(bar)[XB_TMO])) break; if (_sp > XB_SPIN_CAP) { atomicAdd(&(bar)[XB_TMO], 1u); break; } } } } while (0)
; __device__ __forceinline__ void xcd_barrier(const XcdBarrier& b) {
;     ...
;         const unsigned old = xb_add(&bar[XB_XSUB(b.x)], 1u);
;         const unsigned gen = old / nloc;
;         if (old + 1u == (gen + 1u) * nloc) {
;             __builtin_amdgcn_fence(__ATOMIC_RELEASE, "agent");
;             asm volatile("s_waitcnt vmcnt(0)" ::: "memory");
;             const unsigned og = xb_add(&bar[XB_TOP], 1u);
;             const unsigned tg = og / nx;
;             if (og + 1u == (tg + 1u) * nx) xb_add(&bar[XB_TOPGEN], 1u);
;             else XB_SPIN(xb_ld(&bar[XB_TOPGEN]) == tg, bar);
.LBB0_1056:
	s_andn2_saveexec_b64 s[4:5], s[4:5]
	s_cbranch_execz .LBB0_1072
	v_mov_b32_e32 v4, s38
	v_add_co_u32_e32 v4, vcc, 0x3000, v4
	v_mov_b32_e32 v5, s39
	s_waitcnt vmcnt(0)
	v_addc_co_u32_e32 v5, vcc, 0, v5, vcc
	flat_atomic_add v4, v[4:5], v1 offset:1024 sc0
	v_cvt_f32_u32_e32 v5, v2
	v_sub_u32_e32 v6, 0, v2
	s_mov_b64 s[8:9], -1
	v_rcp_iflag_f32_e32 v5, v5
	s_nop 0
	v_mul_f32_e32 v5, 0x4f7ffffe, v5
	v_cvt_u32_f32_e32 v5, v5
	v_mul_lo_u32 v6, v6, v5
	v_mul_hi_u32 v6, v5, v6
	v_add_u32_e32 v5, v5, v6
	s_waitcnt vmcnt(0) lgkmcnt(0)
	v_mul_hi_u32 v5, v4, v5
	v_mul_lo_u32 v6, v5, v2
	v_sub_u32_e32 v6, v4, v6
	v_cmp_ge_u32_e32 vcc, v6, v2
	v_add_u32_e32 v7, 1, v5
	s_nop 0
	v_cndmask_b32_e32 v5, v5, v7, vcc
	v_sub_u32_e32 v7, v6, v2
	v_cndmask_b32_e32 v6, v6, v7, vcc
	v_cmp_ge_u32_e32 vcc, v6, v2
	v_add_u32_e32 v6, 1, v5
	v_add_u32_e32 v7, 1, v4
	v_cndmask_b32_e32 v6, v5, v6, vcc
	v_mad_u64_u32 v[4:5], s[4:5], v2, v6, v[2:3]
	s_add_u32 s4, s38, 0x3500
	s_addc_u32 s5, s39, 0
	v_cmp_ne_u32_e32 vcc, v7, v4
	v_mov_b64_e32 v[4:5], s[4:5]
	s_and_saveexec_b64 s[6:7], vcc
	s_cbranch_execz .LBB0_1069
	v_mov_b64_e32 v[4:5], s[4:5]
	flat_load_dword v2, v[4:5] sc1
	s_mov_b64 s[12:13], 0
	s_waitcnt vmcnt(0) lgkmcnt(0)
	v_cmp_eq_u32_e32 vcc, v2, v6
	s_and_saveexec_b64 s[10:11], vcc
	s_cbranch_execz .LBB0_1068
	s_add_u32 s8, s38, 0x200
	s_addc_u32 s9, s39, 0
	s_mov_b32 s24, 1
	s_branch .LBB0_1061

; __device__ __forceinline__ u32x4 pack8(const f32x4 a, const f32x4 b) { u32x4 w; w.x = cvt_pk_bf16(a[0], a[1]); w.y = cvt_pk_bf16(a[2], a[3]); w.z = cvt_pk_bf16(b[0], b[1]); w.w = cvt_pk_bf16(b[2], b[3]); return w; }
;     __device__ __forceinline__ void operator()(const f32x4 (&acc)[2][2][4][2], const Unit& u, int wr, int wc, int fr, int fq) const {
;         const int row0 = u.pm * BM + wr * 64 + fr, ct0 = wc * 32 + 8 * fq;
;         if (u.pn < 12) {
;             const int t = u.pn >> 2; const float sc = (t == 0) ? qscale : 1.0f;
;             bf16_t* base = QKV + (size_t)t * tstride + (u.pn & 3) * BM + ct0;
; #pragma unroll
;             for (int ai = 0; ai < 2; ++ai)
; #pragma unroll
;                 for (int m = 0; m < 4; ++m) { bf16_t* rowp = base + (size_t)(row0 + ai * HALF + m * 16) * 1024;
; #pragma unroll
;                     for (int bj = 0; bj < 2; ++bj) *(u32x4*)(rowp + bj * HALF) = pack8(acc[ai][bj][m][0] * sc, acc[ai][bj][m][1] * sc); }
.LBB0_1174:
	v_ashrrev_i32_e32 v151, 31, v150
	s_lshl_b32 s18, s18, 8
	v_lshlrev_b64 v[152:153], 11, v[150:151]
	s_ashr_i32 s19, s18, 31
	v_lshl_add_u64 v[152:153], s[10:11], 0, v[152:153]
	s_lshl_b64 s[18:19], s[18:19], 1
	v_readlane_b32 s20, v253, 57
	v_lshl_add_u64 v[152:153], v[152:153], 0, s[18:19]
	v_mov_b32_e32 v149, v3
	v_readlane_b32 s21, v253, 58
	v_lshl_add_u64 v[152:153], v[152:153], 0, v[148:149]
	v_pk_mul_f32 v[130:131], s[14:15], v[130:131]
	v_pk_mul_f32 v[128:129], s[20:21], v[128:129]
	v_pk_mul_f32 v[156:157], s[14:15], v[126:127]
	v_pk_mul_f32 v[126:127], s[20:21], v[124:125]
	v_cvt_pk_bf16_f32 v124, v128, v129
	v_cvt_pk_bf16_f32 v125, v130, v131
	v_pk_mul_f32 v[120:121], s[20:21], v[120:121]
	v_cvt_pk_bf16_f32 v126, v126, v127
	v_cvt_pk_bf16_f32 v127, v156, v157
	flat_store_dwordx4 v[152:153], v[124:127] sc1
	v_pk_mul_f32 v[122:123], s[14:15], v[122:123]
	v_pk_mul_f32 v[114:115], s[14:15], v[114:115]
	v_pk_mul_f32 v[124:125], s[14:15], v[118:119]
	v_pk_mul_f32 v[118:119], s[20:21], v[116:117]
	v_cvt_pk_bf16_f32 v116, v120, v121
	v_cvt_pk_bf16_f32 v117, v122, v123
	v_pk_mul_f32 v[112:113], s[20:21], v[112:113]
	v_cvt_pk_bf16_f32 v118, v118, v119
	v_cvt_pk_bf16_f32 v119, v124, v125
	flat_store_dwordx4 v[152:153], v[116:119] offset:256 sc1
	v_pk_mul_f32 v[104:105], s[20:21], v[104:105]
	v_pk_mul_f32 v[106:107], s[14:15], v[106:107]
	v_or_b32_e32 v116, 16, v150
	v_ashrrev_i32_e32 v117, 31, v116
	v_lshlrev_b64 v[116:117], 11, v[116:117]
	v_lshl_add_u64 v[116:117], s[10:11], 0, v[116:117]
	v_lshl_add_u64 v[116:117], v[116:117], 0, s[18:19]
	v_lshl_add_u64 v[116:117], v[116:117], 0, v[148:149]
	v_pk_mul_f32 v[118:119], s[14:15], v[110:111]
	v_pk_mul_f32 v[110:111], s[20:21], v[108:109]
	v_cvt_pk_bf16_f32 v108, v112, v113
	v_cvt_pk_bf16_f32 v109, v114, v115
	v_pk_mul_f32 v[98:99], s[14:15], v[98:99]
	v_cvt_pk_bf16_f32 v110, v110, v111
	v_cvt_pk_bf16_f32 v111, v118, v119
	flat_store_dwordx4 v[116:117], v[108:111] sc1
	v_pk_mul_f32 v[96:97], s[20:21], v[96:97]
	v_pk_mul_f32 v[88:89], s[20:21], v[88:89]
	v_pk_mul_f32 v[108:109], s[14:15], v[102:103]
	v_pk_mul_f32 v[102:103], s[20:21], v[100:101]
	v_cvt_pk_bf16_f32 v100, v104, v105
	v_cvt_pk_bf16_f32 v101, v106, v107
	v_pk_mul_f32 v[90:91], s[14:15], v[90:91]
	v_cvt_pk_bf16_f32 v102, v102, v103
	v_cvt_pk_bf16_f32 v103, v108, v109
	flat_store_dwordx4 v[116:117], v[100:103] offset:256 sc1
	v_pk_mul_f32 v[82:83], s[14:15], v[82:83]
	v_pk_mul_f32 v[80:81], s[20:21], v[80:81]
	v_or_b32_e32 v100, 32, v150
	v_ashrrev_i32_e32 v101, 31, v100
	v_lshlrev_b64 v[100:101], 11, v[100:101]
	v_lshl_add_u64 v[100:101], s[10:11], 0, v[100:101]
	v_lshl_add_u64 v[100:101], v[100:101], 0, s[18:19]
	v_lshl_add_u64 v[100:101], v[100:101], 0, v[148:149]
	v_pk_mul_f32 v[102:103], s[14:15], v[94:95]
	v_pk_mul_f32 v[94:95], s[20:21], v[92:93]
	v_cvt_pk_bf16_f32 v92, v96, v97
	v_cvt_pk_bf16_f32 v93, v98, v99
	v_pk_mul_f32 v[74:75], s[14:15], v[74:75]
	v_cvt_pk_bf16_f32 v94, v94, v95
	v_cvt_pk_bf16_f32 v95, v102, v103
	flat_store_dwordx4 v[100:101], v[92:95] sc1
	v_pk_mul_f32 v[72:73], s[20:21], v[72:73]
	v_pk_mul_f32 v[64:65], s[20:21], v[64:65]
	v_pk_mul_f32 v[92:93], s[14:15], v[86:87]
	v_pk_mul_f32 v[86:87], s[20:21], v[84:85]
	v_cvt_pk_bf16_f32 v84, v88, v89
	v_cvt_pk_bf16_f32 v85, v90, v91
	v_pk_mul_f32 v[66:67], s[14:15], v[66:67]
	v_cvt_pk_bf16_f32 v86, v86, v87
	v_cvt_pk_bf16_f32 v87, v92, v93
	flat_store_dwordx4 v[100:101], v[84:87] offset:256 sc1
	v_pk_mul_f32 v[58:59], s[14:15], v[58:59]
	v_pk_mul_f32 v[56:57], s[20:21], v[56:57]
	v_or_b32_e32 v84, 48, v150
	v_ashrrev_i32_e32 v85, 31, v84
	v_lshlrev_b64 v[84:85], 11, v[84:85]
	v_lshl_add_u64 v[84:85], s[10:11], 0, v[84:85]
	v_lshl_add_u64 v[84:85], v[84:85], 0, s[18:19]
	v_lshl_add_u64 v[84:85], v[84:85], 0, v[148:149]
	v_pk_mul_f32 v[86:87], s[14:15], v[78:79]
	v_pk_mul_f32 v[78:79], s[20:21], v[76:77]
	v_cvt_pk_bf16_f32 v76, v80, v81
	v_cvt_pk_bf16_f32 v77, v82, v83
; __device__ __forceinline__ u32x4 pack8(const f32x4 a, const f32x4 b) { u32x4 w; w.x = cvt_pk_bf16(a[0], a[1]); w.y = cvt_pk_bf16(a[2], a[3]); w.z = cvt_pk_bf16(b[0], b[1]); w.w = cvt_pk_bf16(b[2], b[3]); return w; }
;     __device__ __forceinline__ void operator()(const f32x4 (&acc)[2][2][4][2], const Unit& u, int wr, int wc, int fr, int fq) const {
;         const int row0 = u.pm * BM + wr * 64 + fr, ct0 = wc * 32 + 8 * fq;
;         if (u.pn < 12) {
;             const int t = u.pn >> 2; const float sc = (t == 0) ? qscale : 1.0f;
;             bf16_t* base = QKV + (size_t)t * tstride + (u.pn & 3) * BM + ct0;
; #pragma unroll
;             for (int ai = 0; ai < 2; ++ai)
; #pragma unroll
;                 for (int m = 0; m < 4; ++m) { bf16_t* rowp = base + (size_t)(row0 + ai * HALF + m * 16) * 1024;
; #pragma unroll
;                     for (int bj = 0; bj < 2; ++bj) *(u32x4*)(rowp + bj * HALF) = pack8(acc[ai][bj][m][0] * sc, acc[ai][bj][m][1] * sc); }
	s_mov_b64 s[18:19], 0x40000
	v_cvt_pk_bf16_f32 v78, v78, v79
	v_cvt_pk_bf16_f32 v79, v86, v87
	flat_store_dwordx4 v[84:85], v[76:79] sc1
	v_pk_mul_f32 v[52:53], s[20:21], v[52:53]
	v_pk_mul_f32 v[42:43], s[14:15], v[42:43]
	v_pk_mul_f32 v[76:77], s[14:15], v[70:71]
	v_pk_mul_f32 v[70:71], s[20:21], v[68:69]
	v_cvt_pk_bf16_f32 v68, v72, v73
	v_cvt_pk_bf16_f32 v69, v74, v75
	v_pk_mul_f32 v[40:41], s[20:21], v[40:41]
	v_cvt_pk_bf16_f32 v70, v70, v71
	v_cvt_pk_bf16_f32 v71, v76, v77
	flat_store_dwordx4 v[84:85], v[68:71] offset:256 sc1
	v_pk_mul_f32 v[36:37], s[20:21], v[36:37]
	v_pk_mul_f32 v[26:27], s[14:15], v[26:27]
	v_lshl_add_u64 v[68:69], v[152:153], 0, s[18:19]
	s_mov_b32 s18, 0x40000
	v_pk_mul_f32 v[70:71], s[14:15], v[62:63]
	v_pk_mul_f32 v[62:63], s[20:21], v[60:61]
	v_cvt_pk_bf16_f32 v60, v64, v65
	v_add_co_u32_e32 v64, vcc, s18, v152
	v_cvt_pk_bf16_f32 v61, v66, v67
	v_cvt_pk_bf16_f32 v62, v62, v63
	v_cvt_pk_bf16_f32 v63, v70, v71
	s_mov_b64 s[18:19], 0x48000
	s_nop 0
	v_addc_co_u32_e32 v65, vcc, 0, v153, vcc
	flat_store_dwordx4 v[64:65], v[60:63] sc1
	v_pk_mul_f32 v[24:25], s[20:21], v[24:25]
	v_pk_mul_f32 v[20:21], s[20:21], v[20:21]
	v_pk_mul_f32 v[60:61], s[14:15], v[50:51]
	v_pk_mul_f32 v[50:51], s[20:21], v[48:49]
	v_cvt_pk_bf16_f32 v48, v56, v57
	v_cvt_pk_bf16_f32 v49, v58, v59
	v_pk_mul_f32 v[10:11], s[14:15], v[10:11]
	v_cvt_pk_bf16_f32 v50, v50, v51
	v_cvt_pk_bf16_f32 v51, v60, v61
	flat_store_dwordx4 v[68:69], v[48:51] offset:256 sc1
	v_pk_mul_f32 v[8:9], s[20:21], v[8:9]
	s_nop 0
	v_lshl_add_u64 v[48:49], v[152:153], 0, s[18:19]
	v_pk_mul_f32 v[50:51], s[14:15], v[54:55]
	s_mov_b32 s18, 0x48000
	v_pk_mul_f32 v[54:55], s[14:15], v[46:47]
	v_pk_mul_f32 v[46:47], s[20:21], v[44:45]
	v_cvt_pk_bf16_f32 v44, v52, v53
	v_cvt_pk_bf16_f32 v45, v50, v51
	v_add_co_u32_e32 v50, vcc, s18, v152
	v_cvt_pk_bf16_f32 v46, v46, v47
	v_cvt_pk_bf16_f32 v47, v54, v55
	s_mov_b64 s[18:19], 0x50000
	s_nop 0
	v_addc_co_u32_e32 v51, vcc, 0, v153, vcc
	flat_store_dwordx4 v[50:51], v[44:47] sc1
	s_nop 1
	v_pk_mul_f32 v[44:45], s[14:15], v[34:35]
	v_pk_mul_f32 v[34:35], s[20:21], v[32:33]
	v_cvt_pk_bf16_f32 v32, v40, v41
	v_cvt_pk_bf16_f32 v33, v42, v43
	s_nop 0
	v_cvt_pk_bf16_f32 v34, v34, v35
	v_cvt_pk_bf16_f32 v35, v44, v45
	flat_store_dwordx4 v[48:49], v[32:35] offset:256 sc1
	s_nop 1
	v_lshl_add_u64 v[32:33], v[152:153], 0, s[18:19]
	v_pk_mul_f32 v[34:35], s[14:15], v[38:39]
	s_mov_b32 s18, 0x50000
	v_pk_mul_f32 v[38:39], s[14:15], v[30:31]
	v_pk_mul_f32 v[30:31], s[20:21], v[28:29]
	v_cvt_pk_bf16_f32 v28, v36, v37
	v_cvt_pk_bf16_f32 v29, v34, v35
	v_add_co_u32_e32 v34, vcc, s18, v152
	v_cvt_pk_bf16_f32 v30, v30, v31
	v_cvt_pk_bf16_f32 v31, v38, v39
	s_mov_b64 s[18:19], 0x58000
	s_nop 0
	v_addc_co_u32_e32 v35, vcc, 0, v153, vcc
	flat_store_dwordx4 v[34:35], v[28:31] sc1
	s_nop 1
	v_pk_mul_f32 v[28:29], s[14:15], v[18:19]
	v_pk_mul_f32 v[18:19], s[20:21], v[16:17]
	v_cvt_pk_bf16_f32 v16, v24, v25
	v_cvt_pk_bf16_f32 v17, v26, v27
	s_nop 0
	v_cvt_pk_bf16_f32 v18, v18, v19
	v_cvt_pk_bf16_f32 v19, v28, v29
	flat_store_dwordx4 v[32:33], v[16:19] offset:256 sc1
	s_nop 1
	v_lshl_add_u64 v[16:17], v[152:153], 0, s[18:19]
	v_pk_mul_f32 v[18:19], s[14:15], v[22:23]
	s_mov_b32 s18, 0x58000
	v_pk_mul_f32 v[22:23], s[14:15], v[14:15]
	v_pk_mul_f32 v[14:15], s[20:21], v[12:13]
	v_cvt_pk_bf16_f32 v12, v20, v21
	v_cvt_pk_bf16_f32 v13, v18, v19
	v_add_co_u32_e32 v18, vcc, s18, v152
	v_cvt_pk_bf16_f32 v14, v14, v15
	v_cvt_pk_bf16_f32 v15, v22, v23
	s_nop 1
	v_addc_co_u32_e32 v19, vcc, 0, v153, vcc
	flat_store_dwordx4 v[18:19], v[12:15] sc1
	s_nop 1
	v_pk_mul_f32 v[12:13], s[14:15], v[6:7]
	v_pk_mul_f32 v[6:7], s[20:21], v[4:5]
	v_cvt_pk_bf16_f32 v4, v8, v9
	v_cvt_pk_bf16_f32 v5, v10, v11
	s_nop 0
	v_cvt_pk_bf16_f32 v6, v6, v7
	v_cvt_pk_bf16_f32 v7, v12, v13
	flat_store_dwordx4 v[16:17], v[4:7] offset:256 sc1
	s_andn2_b64 vcc, exec, s[16:17]
	s_mov_b64 s[18:19], -1
	s_cbranch_vccnz .LBB0_1159

; #define GAS __attribute__((address_space(1)))
; __device__ __forceinline__ void cmp_tail_phase(const Ctx& C, const bf16* slabs, const float* b1f, const bf16* w2t, bf16* KC2) {
;     ...
;         for (int kk = 0; kk < 2; ++kk) {
;             const int k0 = 32 * (2 * kq + kk) + 8 * fq;
;             v4u pk[8];
; #pragma unroll
;             for (int kc = 0; kc < 8; ++kc) pk[kc] = *(const GAS v4u*)(slabs + ((size_t)kc * 8192 + row) * 256 + k0);
;             const GAS f32x4* bp = (const GAS f32x4*)(b1f + kv * 256 + k0); f32x4 s0 = bp[0], s1 = bp[1];
; #pragma unroll
;             for (int kc = 0; kc < 8; ++kc) { const v4u q = pk[kc]; s0 += (f32x4){bf_lo(q.x), bf_hi(q.x), bf_lo(q.y), bf_hi(q.y)}; s1 += (f32x4){bf_lo(q.z), bf_hi(q.z), bf_lo(q.w), bf_hi(q.w)}; }
.LBB0_1311:
	v_ashrrev_i32_e32 v33, 31, v32
	v_lshlrev_b64 v[4:5], 9, v[32:33]
	v_lshl_add_u64 v[12:13], v[28:29], 0, v[4:5]
	s_add_i32 s12, s8, s1
	v_add_co_u32_e32 v8, vcc, 0x400000, v12
	s_and_b32 s4, s12, 0xffffff00
	s_nop 0
	v_addc_co_u32_e32 v9, vcc, 0, v13, vcc
	s_ashr_i32 s5, s4, 31
	v_add_co_u32_e32 v14, vcc, 0x800000, v12
	global_load_dwordx4 v[4:7], v[12:13], off
	v_lshl_add_u64 v[10:11], s[4:5], 2, v[30:31]
	v_addc_co_u32_e32 v15, vcc, 0, v13, vcc
	global_load_dwordx4 v[40:43], v[10:11], off offset:16
	global_load_dwordx4 v[50:53], v[10:11], off
	global_load_dwordx4 v[54:57], v[8:9], off
	global_load_dwordx4 v[58:61], v[14:15], off
	v_add_co_u32_e32 v16, vcc, 0xc00000, v12
	s_ashr_i32 s4, s12, 8
	s_nop 0
	v_addc_co_u32_e32 v17, vcc, 0, v13, vcc
	global_load_dwordx4 v[62:65], v[16:17], off
	v_add_co_u32_e32 v18, vcc, 0x1000000, v12
	s_ashr_i32 s5, s4, 31
	s_nop 0
	v_addc_co_u32_e32 v19, vcc, 0, v13, vcc
	global_load_dwordx4 v[66:69], v[18:19], off
	v_add_co_u32_e32 v20, vcc, 0x1400000, v12
	s_lshl_b64 s[12:13], s[4:5], 15
	s_nop 0
	v_addc_co_u32_e32 v21, vcc, 0, v13, vcc
	global_load_dwordx4 v[70:73], v[20:21], off
	v_add_co_u32_e32 v22, vcc, 0x1800000, v12
	s_waitcnt vmcnt(0)
	v_lshlrev_b32_e32 v36, 16, v4
	v_addc_co_u32_e32 v23, vcc, 0, v13, vcc
	global_load_dwordx4 v[74:77], v[22:23], off
	v_add_co_u32_e32 v38, vcc, 0x1c00000, v12
	v_and_b32_e32 v37, 0xffff0000, v4
	s_nop 0
	v_addc_co_u32_e32 v39, vcc, 0, v13, vcc
	global_load_dwordx4 v[78:81], v[38:39], off
	v_lshlrev_b32_e32 v44, 16, v6
	v_and_b32_e32 v45, 0xffff0000, v6
	v_lshlrev_b32_e32 v6, 16, v7
	v_and_b32_e32 v7, 0xffff0000, v7
	s_waitcnt vmcnt(7)
	v_pk_add_f32 v[36:37], v[50:51], v[36:37]
	v_pk_add_f32 v[6:7], v[42:43], v[6:7]
	s_waitcnt vmcnt(6)
	v_lshlrev_b32_e32 v42, 16, v54
	v_and_b32_e32 v43, 0xffff0000, v54
	v_pk_add_f32 v[40:41], v[40:41], v[44:45]
	v_lshlrev_b32_e32 v50, 16, v56
	v_and_b32_e32 v51, 0xffff0000, v56
	v_pk_add_f32 v[36:37], v[36:37], v[42:43]
	s_waitcnt vmcnt(5)
	v_lshlrev_b32_e32 v42, 16, v58
	v_and_b32_e32 v43, 0xffff0000, v58
	v_pk_add_f32 v[40:41], v[40:41], v[50:51]
	v_lshlrev_b32_e32 v50, 16, v60
	v_and_b32_e32 v51, 0xffff0000, v60
	v_pk_add_f32 v[36:37], v[36:37], v[42:43]
	s_waitcnt vmcnt(4)
	v_lshlrev_b32_e32 v42, 16, v62
	v_and_b32_e32 v43, 0xffff0000, v62
	v_pk_add_f32 v[40:41], v[40:41], v[50:51]
	v_pk_add_f32 v[36:37], v[36:37], v[42:43]
	v_lshlrev_b32_e32 v42, 16, v64
	v_and_b32_e32 v43, 0xffff0000, v64
	v_pk_add_f32 v[40:41], v[40:41], v[42:43]
	s_waitcnt vmcnt(3)
	v_lshlrev_b32_e32 v42, 16, v66
	v_and_b32_e32 v43, 0xffff0000, v66
	v_pk_add_f32 v[36:37], v[36:37], v[42:43]
	v_lshlrev_b32_e32 v42, 16, v68
	v_and_b32_e32 v43, 0xffff0000, v68
	v_pk_add_f32 v[40:41], v[40:41], v[42:43]
	s_waitcnt vmcnt(2)
	v_lshlrev_b32_e32 v42, 16, v70
	v_and_b32_e32 v43, 0xffff0000, v70
	v_pk_add_f32 v[36:37], v[36:37], v[42:43]
	v_lshlrev_b32_e32 v42, 16, v72
	v_and_b32_e32 v43, 0xffff0000, v72
	v_pk_add_f32 v[40:41], v[40:41], v[42:43]
	v_lshlrev_b32_e32 v4, 16, v5
	v_and_b32_e32 v5, 0xffff0000, v5
	v_pk_add_f32 v[4:5], v[52:53], v[4:5]
	v_lshlrev_b32_e32 v44, 16, v55
	v_and_b32_e32 v45, 0xffff0000, v55
	v_lshlrev_b32_e32 v52, 16, v57
	v_and_b32_e32 v53, 0xffff0000, v57
	v_pk_add_f32 v[4:5], v[4:5], v[44:45]
	v_lshlrev_b32_e32 v44, 16, v59
	v_and_b32_e32 v45, 0xffff0000, v59
	v_pk_add_f32 v[6:7], v[6:7], v[52:53]
	v_lshlrev_b32_e32 v52, 16, v61
	v_and_b32_e32 v53, 0xffff0000, v61
	v_pk_add_f32 v[4:5], v[4:5], v[44:45]
	v_lshlrev_b32_e32 v44, 16, v63
	v_and_b32_e32 v45, 0xffff0000, v63
	v_pk_add_f32 v[6:7], v[6:7], v[52:53]
	v_pk_add_f32 v[4:5], v[4:5], v[44:45]
	v_lshlrev_b32_e32 v44, 16, v65
	v_and_b32_e32 v45, 0xffff0000, v65
	v_pk_add_f32 v[6:7], v[6:7], v[44:45]
	v_lshlrev_b32_e32 v44, 16, v67
	v_and_b32_e32 v45, 0xffff0000, v67
	v_pk_add_f32 v[4:5], v[4:5], v[44:45]
	v_lshlrev_b32_e32 v44, 16, v69
	v_and_b32_e32 v45, 0xffff0000, v69
	v_pk_add_f32 v[6:7], v[6:7], v[44:45]
	v_lshlrev_b32_e32 v44, 16, v71
	v_and_b32_e32 v45, 0xffff0000, v71
	v_pk_add_f32 v[4:5], v[4:5], v[44:45]
	v_lshlrev_b32_e32 v44, 16, v73
	v_and_b32_e32 v45, 0xffff0000, v73
	v_pk_add_f32 v[6:7], v[6:7], v[44:45]
	s_andn2_b64 vcc, exec, s[2:3]
	s_waitcnt vmcnt(1)
	v_lshlrev_b32_e32 v42, 16, v74
	v_and_b32_e32 v43, 0xffff0000, v74
	v_pk_add_f32 v[36:37], v[36:37], v[42:43]
	v_lshlrev_b32_e32 v42, 16, v76
	v_and_b32_e32 v43, 0xffff0000, v76
	v_pk_add_f32 v[40:41], v[40:41], v[42:43]
	s_waitcnt vmcnt(0)
; __device__ __forceinline__ u32x4 pack8(const f32x4 a, const f32x4 b) { u32x4 w; w.x = cvt_pk_bf16(a[0], a[1]); w.y = cvt_pk_bf16(a[2], a[3]); w.z = cvt_pk_bf16(b[0], b[1]); w.w = cvt_pk_bf16(b[2], b[3]); return w; }
; __device__ __forceinline__ float gelu_tanh(float x) { const float t = 0.7978845608028654f * (x + 0.044715f * x * x * x); return x * sigm(2.0f * t); }
; #define GAS __attribute__((address_space(1)))
; __device__ __forceinline__ void cmp_tail_phase(const Ctx& C, const bf16* slabs, const float* b1f, const bf16* w2t, bf16* KC2) {
;     ...
;         for (int kk = 0; kk < 2; ++kk) {
;             const int k0 = 32 * (2 * kq + kk) + 8 * fq;
;             v4u pk[8];
; #pragma unroll
;             for (int kc = 0; kc < 8; ++kc) pk[kc] = *(const GAS v4u*)(slabs + ((size_t)kc * 8192 + row) * 256 + k0);
;             const GAS f32x4* bp = (const GAS f32x4*)(b1f + kv * 256 + k0); f32x4 s0 = bp[0], s1 = bp[1];
; #pragma unroll
;             for (int kc = 0; kc < 8; ++kc) { const v4u q = pk[kc]; s0 += (f32x4){bf_lo(q.x), bf_hi(q.x), bf_lo(q.y), bf_hi(q.y)}; s1 += (f32x4){bf_lo(q.z), bf_hi(q.z), bf_lo(q.w), bf_hi(q.w)}; }
; #pragma unroll
;             for (int e = 0; e < 4; ++e) { s0[e] = pg8::gelu_tanh(s0[e]); s1[e] = pg8::gelu_tanh(s1[e]); }
;             const pg8::u32x4 bw = pg8::pack8(s0, s1); const bf16x8_t bfrag = __builtin_bit_cast(bf16x8_t, bw);
;             bf16x8_t afrag[4];
; #pragma unroll
;             for (int nt = 0; nt < 4; ++nt) afrag[nt] = *(const GAS bf16x8_t*)(w2t + ((size_t)kv * 64 + 16 * nt + fr) * 256 + k0);
; #pragma unroll
;             for (int nt = 0; nt < 4; ++nt) acc[nt] = __builtin_amdgcn_mfma_f32_16x16x32_bf16(afrag[nt], bfrag, acc[nt], 0, 0, 0);
	v_lshlrev_b32_e32 v42, 16, v78
	v_and_b32_e32 v43, 0xffff0000, v78
	v_pk_add_f32 v[36:37], v[36:37], v[42:43]
	v_lshlrev_b32_e32 v42, 16, v80
	v_and_b32_e32 v43, 0xffff0000, v80
	v_mul_f32_e32 v33, 0x3d372713, v36
	v_pk_add_f32 v[40:41], v[40:41], v[42:43]
	v_mul_f32_e32 v42, 0x3d372713, v37
	v_mul_f32_e32 v33, v36, v33
	v_mul_f32_e32 v42, v37, v42
	v_fma_f32 v33, v36, v33, v36
	v_fma_f32 v42, v37, v42, v37
	v_mul_f32_e32 v33, 0x3f4c422a, v33
	v_mul_f32_e32 v42, 0x3f4c422a, v42
	v_add_f32_e32 v33, v33, v33
	v_add_f32_e32 v42, v42, v42
	v_mul_f32_e32 v33, 0xbfb8aa3b, v33
	v_mul_f32_e32 v42, 0xbfb8aa3b, v42
	v_exp_f32_e32 v33, v33
	v_exp_f32_e32 v42, v42
	v_lshlrev_b32_e32 v44, 16, v75
	v_and_b32_e32 v45, 0xffff0000, v75
	v_add_f32_e32 v33, 1.0, v33
	v_add_f32_e32 v42, 1.0, v42
	v_mul_f32_e32 v43, 0x3d372713, v41
	v_pk_add_f32 v[4:5], v[4:5], v[44:45]
	v_lshlrev_b32_e32 v44, 16, v77
	v_and_b32_e32 v45, 0xffff0000, v77
	v_mul_f32_e32 v35, 0x3d372713, v40
	v_rcp_f32_e32 v33, v33
	v_rcp_f32_e32 v42, v42
	v_mul_f32_e32 v43, v41, v43
	v_pk_add_f32 v[6:7], v[6:7], v[44:45]
	v_lshlrev_b32_e32 v44, 16, v79
	v_and_b32_e32 v45, 0xffff0000, v79
	v_mul_f32_e32 v35, v40, v35
	v_fma_f32 v43, v41, v43, v41
	v_pk_add_f32 v[4:5], v[4:5], v[44:45]
	v_lshlrev_b32_e32 v44, 16, v81
	v_and_b32_e32 v45, 0xffff0000, v81
	v_fma_f32 v35, v40, v35, v40
	v_mul_f32_e32 v43, 0x3f4c422a, v43
	v_pk_add_f32 v[6:7], v[6:7], v[44:45]
	v_mul_f32_e32 v35, 0x3f4c422a, v35
	v_add_f32_e32 v43, v43, v43
	v_add_f32_e32 v35, v35, v35
	v_mul_f32_e32 v43, 0xbfb8aa3b, v43
	v_mul_f32_e32 v33, v36, v33
	v_mul_f32_e32 v36, v37, v42
	v_mul_f32_e32 v42, 0x3d372713, v6
	v_mul_f32_e32 v35, 0xbfb8aa3b, v35
	v_exp_f32_e32 v43, v43
	v_mul_f32_e32 v42, v6, v42
	v_exp_f32_e32 v35, v35
	v_fma_f32 v42, v6, v42, v6
	v_mul_f32_e32 v42, 0x3f4c422a, v42
	v_add_f32_e32 v42, v42, v42
	v_add_f32_e32 v37, 1.0, v43
	v_mul_f32_e32 v42, 0xbfb8aa3b, v42
	v_add_f32_e32 v35, 1.0, v35
	v_rcp_f32_e32 v37, v37
	v_exp_f32_e32 v42, v42
	v_rcp_f32_e32 v35, v35
	v_mul_f32_e32 v43, 0x3d372713, v7
	v_mul_f32_e32 v37, v41, v37
	v_add_f32_e32 v41, 1.0, v42
	v_mul_f32_e32 v42, 0x3d372713, v5
	v_mul_f32_e32 v35, v40, v35
	v_mul_f32_e32 v40, 0x3d372713, v4
	v_mul_f32_e32 v42, v5, v42
	v_mul_f32_e32 v40, v4, v40
	v_fma_f32 v42, v5, v42, v5
	v_fma_f32 v40, v4, v40, v4
	v_mul_f32_e32 v42, 0x3f4c422a, v42
	v_mul_f32_e32 v43, v7, v43
	v_mul_f32_e32 v40, 0x3f4c422a, v40
	v_add_f32_e32 v42, v42, v42
	v_fma_f32 v43, v7, v43, v7
	v_add_f32_e32 v40, v40, v40
	v_mul_f32_e32 v42, 0xbfb8aa3b, v42
	v_mul_f32_e32 v43, 0x3f4c422a, v43
	v_mul_f32_e32 v40, 0xbfb8aa3b, v40
	v_exp_f32_e32 v42, v42
	v_add_f32_e32 v43, v43, v43
	v_exp_f32_e32 v40, v40
	v_mul_f32_e32 v43, 0xbfb8aa3b, v43
	v_exp_f32_e32 v43, v43
	v_add_f32_e32 v42, 1.0, v42
	v_add_f32_e32 v40, 1.0, v40
	v_rcp_f32_e32 v42, v42
	v_rcp_f32_e32 v40, v40
	v_rcp_f32_e32 v41, v41
	v_add_f32_e32 v43, 1.0, v43
	v_rcp_f32_e32 v43, v43
	v_mul_f32_e32 v5, v5, v42
	v_mul_f32_e32 v40, v4, v40
	v_mul_f32_e32 v41, v6, v41
	v_cvt_pk_bf16_f32 v4, v33, v36
	v_cvt_pk_bf16_f32 v5, v40, v5
	v_cvt_pk_bf16_f32 v6, v35, v37
	v_mov_b32_e32 v37, s13
	v_or_b32_e32 v36, s12, v2
	v_mul_f32_e32 v7, v7, v43
	v_lshl_add_u64 v[42:43], v[24:25], 0, v[36:37]
	v_cvt_pk_bf16_f32 v7, v41, v7
	global_load_dwordx4 v[50:53], v[42:43], off
	v_or_b32_e32 v40, 0x2000, v36
	v_mov_b32_e32 v41, s13
	v_lshl_add_u64 v[44:45], v[24:25], 0, v[40:41]
	global_load_dwordx4 v[54:57], v[44:45], off
	v_or_b32_e32 v44, 0x4000, v36
	v_mov_b32_e32 v45, s13
	v_lshl_add_u64 v[58:59], v[24:25], 0, v[44:45]
	global_load_dwordx4 v[58:61], v[58:59], off
	s_nop 0
	global_load_dwordx4 v[62:65], v[12:13], off offset:64
	global_load_dwordx4 v[66:69], v[10:11], off offset:128
	global_load_dwordx4 v[70:73], v[10:11], off offset:144
	global_load_dwordx4 v[74:77], v[8:9], off offset:64
	global_load_dwordx4 v[78:81], v[14:15], off offset:64
	global_load_dwordx4 v[82:85], v[16:17], off offset:64
	global_load_dwordx4 v[86:89], v[18:19], off offset:64
	s_waitcnt vmcnt(9)
	v_mfma_f32_16x16x32_bf16 v[16:19], v[50:53], v[4:7], 0
	global_load_dwordx4 v[50:53], v[20:21], off offset:64
	global_load_dwordx4 v[90:93], v[22:23], off offset:64
	v_or_b32_e32 v36, 0x6000, v36
	v_lshl_add_u64 v[8:9], v[24:25], 0, v[36:37]
	s_waitcnt vmcnt(10)
	v_mfma_f32_16x16x32_bf16 v[12:15], v[54:57], v[4:7], 0
	global_load_dwordx4 v[20:23], v[8:9], off
	global_load_dwordx4 v[54:57], v[38:39], off offset:64
	s_waitcnt vmcnt(10)
	v_lshlrev_b32_e32 v38, 16, v62
	v_and_b32_e32 v39, 0xffff0000, v62
	v_mfma_f32_16x16x32_bf16 v[8:11], v[58:61], v[4:7], 0
	v_lshlrev_b32_e32 v58, 16, v63
	v_and_b32_e32 v59, 0xffff0000, v63
	s_waitcnt vmcnt(9)
	v_pk_add_f32 v[38:39], v[66:67], v[38:39]
	v_lshlrev_b32_e32 v60, 16, v64
	v_and_b32_e32 v61, 0xffff0000, v64
	v_lshlrev_b32_e32 v62, 16, v65
	v_and_b32_e32 v63, 0xffff0000, v65
	s_waitcnt vmcnt(7)
	v_lshlrev_b32_e32 v64, 16, v74
	v_and_b32_e32 v65, 0xffff0000, v74
	v_pk_add_f32 v[58:59], v[68:69], v[58:59]
	v_pk_add_f32 v[60:61], v[70:71], v[60:61]
	v_lshlrev_b32_e32 v66, 16, v75
	v_and_b32_e32 v67, 0xffff0000, v75
	v_pk_add_f32 v[38:39], v[38:39], v[64:65]
	v_lshlrev_b32_e32 v64, 16, v76
	v_and_b32_e32 v65, 0xffff0000, v76
	v_pk_add_f32 v[62:63], v[72:73], v[62:63]
	v_pk_add_f32 v[58:59], v[58:59], v[66:67]
	v_lshlrev_b32_e32 v66, 16, v77
	v_and_b32_e32 v67, 0xffff0000, v77
	v_pk_add_f32 v[60:61], v[60:61], v[64:65]
	s_waitcnt vmcnt(6)
; __device__ __forceinline__ u32x4 pack8(const f32x4 a, const f32x4 b) { u32x4 w; w.x = cvt_pk_bf16(a[0], a[1]); w.y = cvt_pk_bf16(a[2], a[3]); w.z = cvt_pk_bf16(b[0], b[1]); w.w = cvt_pk_bf16(b[2], b[3]); return w; }
; __device__ __forceinline__ float gelu_tanh(float x) { const float t = 0.7978845608028654f * (x + 0.044715f * x * x * x); return x * sigm(2.0f * t); }
; #define GAS __attribute__((address_space(1)))
; #define LAS __attribute__((address_space(3)))
; __device__ __forceinline__ void cmp_tail_phase(const Ctx& C, const bf16* slabs, const float* b1f, const bf16* w2t, bf16* KC2) {
;     ...
;         for (int kk = 0; kk < 2; ++kk) {
;             const int k0 = 32 * (2 * kq + kk) + 8 * fq;
;             v4u pk[8];
; #pragma unroll
;             for (int kc = 0; kc < 8; ++kc) pk[kc] = *(const GAS v4u*)(slabs + ((size_t)kc * 8192 + row) * 256 + k0);
;             const GAS f32x4* bp = (const GAS f32x4*)(b1f + kv * 256 + k0); f32x4 s0 = bp[0], s1 = bp[1];
; #pragma unroll
;             for (int kc = 0; kc < 8; ++kc) { const v4u q = pk[kc]; s0 += (f32x4){bf_lo(q.x), bf_hi(q.x), bf_lo(q.y), bf_hi(q.y)}; s1 += (f32x4){bf_lo(q.z), bf_hi(q.z), bf_lo(q.w), bf_hi(q.w)}; }
; #pragma unroll
;             for (int e = 0; e < 4; ++e) { s0[e] = pg8::gelu_tanh(s0[e]); s1[e] = pg8::gelu_tanh(s1[e]); }
;             const pg8::u32x4 bw = pg8::pack8(s0, s1); const bf16x8_t bfrag = __builtin_bit_cast(bf16x8_t, bw);
;             bf16x8_t afrag[4];
; #pragma unroll
;             for (int nt = 0; nt < 4; ++nt) afrag[nt] = *(const GAS bf16x8_t*)(w2t + ((size_t)kv * 64 + 16 * nt + fr) * 256 + k0);
; #pragma unroll
;             for (int nt = 0; nt < 4; ++nt) acc[nt] = __builtin_amdgcn_mfma_f32_16x16x32_bf16(afrag[nt], bfrag, acc[nt], 0, 0, 0);
;         }
;         LAS f32x4* rp = (LAS f32x4*)(red + (C.wave * 64 + C.lane) * 16);
; #pragma unroll
;         for (int nt = 0; nt < 4; ++nt) rp[nt] = acc[nt];
;         __syncthreads();
	v_lshlrev_b32_e32 v64, 16, v78
	v_and_b32_e32 v65, 0xffff0000, v78
	v_pk_add_f32 v[62:63], v[62:63], v[66:67]
	v_lshlrev_b32_e32 v66, 16, v79
	v_and_b32_e32 v67, 0xffff0000, v79
	v_pk_add_f32 v[38:39], v[38:39], v[64:65]
	v_lshlrev_b32_e32 v64, 16, v80
	v_and_b32_e32 v65, 0xffff0000, v80
	v_pk_add_f32 v[58:59], v[58:59], v[66:67]
	v_lshlrev_b32_e32 v66, 16, v81
	v_and_b32_e32 v67, 0xffff0000, v81
	v_pk_add_f32 v[60:61], v[60:61], v[64:65]
	s_waitcnt vmcnt(5)
	v_lshlrev_b32_e32 v64, 16, v82
	v_and_b32_e32 v65, 0xffff0000, v82
	v_pk_add_f32 v[62:63], v[62:63], v[66:67]
	v_lshlrev_b32_e32 v66, 16, v83
	v_and_b32_e32 v67, 0xffff0000, v83
	v_pk_add_f32 v[38:39], v[38:39], v[64:65]
	v_lshlrev_b32_e32 v64, 16, v84
	v_and_b32_e32 v65, 0xffff0000, v84
	v_pk_add_f32 v[58:59], v[58:59], v[66:67]
	v_lshlrev_b32_e32 v66, 16, v85
	v_and_b32_e32 v67, 0xffff0000, v85
	v_pk_add_f32 v[60:61], v[60:61], v[64:65]
	s_waitcnt vmcnt(4)
	v_lshlrev_b32_e32 v64, 16, v86
	v_and_b32_e32 v65, 0xffff0000, v86
	v_pk_add_f32 v[62:63], v[62:63], v[66:67]
	v_lshlrev_b32_e32 v66, 16, v87
	v_and_b32_e32 v67, 0xffff0000, v87
	v_pk_add_f32 v[38:39], v[38:39], v[64:65]
	v_lshlrev_b32_e32 v64, 16, v88
	v_and_b32_e32 v65, 0xffff0000, v88
	v_pk_add_f32 v[58:59], v[58:59], v[66:67]
	v_pk_add_f32 v[60:61], v[60:61], v[64:65]
	v_lshlrev_b32_e32 v66, 16, v89
	v_and_b32_e32 v67, 0xffff0000, v89
	v_pk_add_f32 v[62:63], v[62:63], v[66:67]
	s_waitcnt vmcnt(1)
	v_mfma_f32_16x16x32_bf16 v[4:7], v[20:23], v[4:7], 0
	v_lshlrev_b32_e32 v64, 16, v50
	v_and_b32_e32 v65, 0xffff0000, v50
	v_lshlrev_b32_e32 v50, 16, v51
	v_and_b32_e32 v51, 0xffff0000, v51
	v_pk_add_f32 v[50:51], v[58:59], v[50:51]
	v_lshlrev_b32_e32 v58, 16, v52
	v_and_b32_e32 v59, 0xffff0000, v52
	v_pk_add_f32 v[38:39], v[38:39], v[64:65]
	v_pk_add_f32 v[58:59], v[60:61], v[58:59]
	v_lshlrev_b32_e32 v60, 16, v90
	v_and_b32_e32 v61, 0xffff0000, v90
	v_pk_add_f32 v[38:39], v[38:39], v[60:61]
	v_lshlrev_b32_e32 v60, 16, v92
	v_and_b32_e32 v61, 0xffff0000, v92
	v_pk_add_f32 v[58:59], v[58:59], v[60:61]
	s_waitcnt vmcnt(0)
	v_lshlrev_b32_e32 v60, 16, v54
	v_and_b32_e32 v61, 0xffff0000, v54
	v_pk_add_f32 v[38:39], v[38:39], v[60:61]
	v_lshlrev_b32_e32 v52, 16, v53
	v_and_b32_e32 v53, 0xffff0000, v53
	v_mul_f32_e32 v33, 0x3d372713, v38
	v_mul_f32_e32 v49, 0x3d372713, v39
	v_pk_add_f32 v[52:53], v[62:63], v[52:53]
	v_lshlrev_b32_e32 v62, 16, v91
	v_and_b32_e32 v63, 0xffff0000, v91
	v_mul_f32_e32 v33, v38, v33
	v_mul_f32_e32 v49, v39, v49
	v_pk_add_f32 v[50:51], v[50:51], v[62:63]
	v_lshlrev_b32_e32 v54, 16, v55
	v_and_b32_e32 v55, 0xffff0000, v55
	v_fma_f32 v33, v38, v33, v38
	v_fma_f32 v49, v39, v49, v39
	v_lshlrev_b32_e32 v62, 16, v93
	v_and_b32_e32 v63, 0xffff0000, v93
	v_pk_add_f32 v[50:51], v[50:51], v[54:55]
	v_lshlrev_b32_e32 v54, 16, v56
	v_and_b32_e32 v55, 0xffff0000, v56
	v_mul_f32_e32 v33, 0x3f4c422a, v33
	v_mul_f32_e32 v49, 0x3f4c422a, v49
	v_pk_add_f32 v[52:53], v[52:53], v[62:63]
	v_lshlrev_b32_e32 v56, 16, v57
	v_add_f32_e32 v33, v33, v33
	v_and_b32_e32 v57, 0xffff0000, v57
	v_pk_add_f32 v[54:55], v[58:59], v[54:55]
	v_add_f32_e32 v49, v49, v49
	v_mul_f32_e32 v33, 0xbfb8aa3b, v33
	v_pk_add_f32 v[52:53], v[52:53], v[56:57]
	v_mul_f32_e32 v49, 0xbfb8aa3b, v49
	v_mul_f32_e32 v56, 0x3d372713, v55
	v_exp_f32_e32 v33, v33
	v_mul_f32_e32 v35, 0x3d372713, v54
	v_exp_f32_e32 v49, v49
	v_mul_f32_e32 v56, v55, v56
	v_mul_f32_e32 v35, v54, v35
	v_fma_f32 v56, v55, v56, v55
	v_fma_f32 v35, v54, v35, v54
	v_mul_f32_e32 v56, 0x3f4c422a, v56
	v_mul_f32_e32 v35, 0x3f4c422a, v35
	v_add_f32_e32 v56, v56, v56
	v_add_f32_e32 v33, 1.0, v33
	v_add_f32_e32 v35, v35, v35
	v_add_f32_e32 v49, 1.0, v49
	v_mul_f32_e32 v56, 0xbfb8aa3b, v56
	v_mul_f32_e32 v35, 0xbfb8aa3b, v35
	v_rcp_f32_e32 v33, v33
	v_rcp_f32_e32 v49, v49
	v_exp_f32_e32 v56, v56
	v_exp_f32_e32 v35, v35
	v_mul_f32_e32 v33, v38, v33
	v_mul_f32_e32 v38, v39, v49
	v_add_f32_e32 v39, 1.0, v56
	v_add_f32_e32 v35, 1.0, v35
	v_rcp_f32_e32 v39, v39
	v_rcp_f32_e32 v35, v35
	v_mul_f32_e32 v56, 0x3d372713, v53
	v_mul_f32_e32 v49, 0x3d372713, v50
	v_mul_f32_e32 v39, v55, v39
	v_mul_f32_e32 v55, 0x3d372713, v51
	v_mul_f32_e32 v35, v54, v35
	v_mul_f32_e32 v54, 0x3d372713, v52
	v_mul_f32_e32 v55, v51, v55
	v_mul_f32_e32 v56, v53, v56
	v_mul_f32_e32 v49, v50, v49
	v_mul_f32_e32 v54, v52, v54
	v_fma_f32 v55, v51, v55, v51
	v_fma_f32 v56, v53, v56, v53
	v_fma_f32 v49, v50, v49, v50
	v_fma_f32 v54, v52, v54, v52
	v_mul_f32_e32 v55, 0x3f4c422a, v55
	v_mul_f32_e32 v56, 0x3f4c422a, v56
	v_mul_f32_e32 v49, 0x3f4c422a, v49
	v_mul_f32_e32 v54, 0x3f4c422a, v54
	v_add_f32_e32 v55, v55, v55
	v_add_f32_e32 v56, v56, v56
	v_add_f32_e32 v49, v49, v49
	v_add_f32_e32 v54, v54, v54
	v_mul_f32_e32 v55, 0xbfb8aa3b, v55
	v_mul_f32_e32 v56, 0xbfb8aa3b, v56
	v_mul_f32_e32 v49, 0xbfb8aa3b, v49
	v_mul_f32_e32 v54, 0xbfb8aa3b, v54
	v_exp_f32_e32 v55, v55
	v_exp_f32_e32 v56, v56
	v_exp_f32_e32 v49, v49
	v_exp_f32_e32 v54, v54
	v_add_f32_e32 v55, 1.0, v55
	v_add_f32_e32 v56, 1.0, v56
	v_add_f32_e32 v49, 1.0, v49
	v_add_f32_e32 v54, 1.0, v54
	v_rcp_f32_e32 v55, v55
	v_rcp_f32_e32 v56, v56
	v_rcp_f32_e32 v49, v49
	v_rcp_f32_e32 v54, v54
	v_mul_f32_e32 v51, v51, v55
	v_mul_f32_e32 v53, v53, v56
	v_lshl_add_u64 v[20:21], v[26:27], 0, v[40:41]
	v_mul_f32_e32 v49, v50, v49
	v_mul_f32_e32 v54, v52, v54
	v_cvt_pk_bf16_f32 v50, v33, v38
	v_cvt_pk_bf16_f32 v51, v49, v51
	v_cvt_pk_bf16_f32 v52, v35, v39
	v_cvt_pk_bf16_f32 v53, v54, v53
	global_load_dwordx4 v[20:23], v[20:21], off
	v_lshl_add_u64 v[38:39], v[26:27], 0, v[44:45]
	v_lshl_add_u64 v[36:37], v[26:27], 0, v[36:37]
	global_load_dwordx4 v[54:57], v[42:43], off offset:64
	s_nop 0
	global_load_dwordx4 v[38:41], v[38:39], off
	s_waitcnt vmcnt(2)
	v_mfma_f32_16x16x32_bf16 v[12:15], v[20:23], v[50:53], v[12:15]
	global_load_dwordx4 v[20:23], v[36:37], off
	s_waitcnt vmcnt(2)
	v_mfma_f32_16x16x32_bf16 v[16:19], v[54:57], v[50:53], v[16:19]
	s_waitcnt vmcnt(1)
	v_mfma_f32_16x16x32_bf16 v[8:11], v[38:41], v[50:53], v[8:11]
	s_waitcnt vmcnt(0)
	v_mfma_f32_16x16x32_bf16 v[4:7], v[20:23], v[50:53], v[4:7]
	v_add_u32_e32 v20, s9, v46
	s_nop 2
	ds_write_b128 v20, v[16:19]
	ds_write_b128 v20, v[12:15] offset:16
	ds_write_b128 v20, v[8:11] offset:32
	s_nop 0
	ds_write_b128 v20, v[4:7] offset:48
	s_waitcnt lgkmcnt(0)
	s_barrier
; #define LAS __attribute__((address_space(3)))
; __device__ __forceinline__ unsigned pk2(float lo, float hi) { unsigned r; asm("v_cvt_pk_bf16_f32 %0, %1, %2" : "=v"(r) : "v"(lo), "v"(hi)); return r; }
; __device__ __forceinline__ void cmp_tail_phase(const Ctx& C, const bf16* slabs, const float* b1f, const bf16* w2t, bf16* KC2) {
;     ...
;         if (kq == 0) {
; #pragma unroll
;             for (int w = 1; w < 4; ++w) { const LAS f32x4* op = (const LAS f32x4*)(red + ((C.wave + w) * 64 + C.lane) * 16);
; #pragma unroll
;                 for (int nt = 0; nt < 4; ++nt) acc[nt] += op[nt]; }
;             const int m = row & 4095; const bool pad = (m & 127) == 127;
; #pragma unroll
;             for (int nt = 0; nt < 4; ++nt) { unsigned lo = pk2(acc[nt][0], acc[nt][1]), hi2 = pk2(acc[nt][2], acc[nt][3]); if (pad) { lo = 0u; hi2 = 0u; }
;                 *(unsigned long long*)(KC2 + (size_t)kv * KC2_STRIDE_E + (size_t)m * 64 + 16 * nt + 4 * fq) = (unsigned long long)lo | ((unsigned long long)hi2 << 32); }
;         }
;         __syncthreads();
	s_cbranch_vccnz .LBB0_1310
	ds_read_b128 v[20:23], v48 offset:4096
	ds_read_b128 v[36:39], v48 offset:4112
	ds_read_b128 v[40:43], v48 offset:4128
	ds_read_b128 v[50:53], v48 offset:4144
	s_lshl_b64 s[4:5], s[4:5], 19
	s_waitcnt lgkmcnt(3)
	v_pk_add_f32 v[18:19], v[18:19], v[22:23]
	v_pk_add_f32 v[16:17], v[16:17], v[20:21]
	s_waitcnt lgkmcnt(2)
	v_pk_add_f32 v[20:21], v[14:15], v[38:39]
	v_pk_add_f32 v[22:23], v[12:13], v[36:37]
	s_waitcnt lgkmcnt(1)
	v_pk_add_f32 v[36:37], v[10:11], v[42:43]
	ds_read_b128 v[10:13], v48 offset:8192
	v_pk_add_f32 v[38:39], v[8:9], v[40:41]
	s_waitcnt lgkmcnt(1)
	v_pk_add_f32 v[40:41], v[6:7], v[52:53]
	ds_read_b128 v[6:9], v48 offset:8208
	v_pk_add_f32 v[42:43], v[4:5], v[50:51]
	s_waitcnt lgkmcnt(1)
	v_pk_add_f32 v[18:19], v[18:19], v[12:13]
	ds_read_b128 v[12:15], v48 offset:8224
	v_pk_add_f32 v[16:17], v[16:17], v[10:11]
	s_waitcnt lgkmcnt(1)
	v_pk_add_f32 v[20:21], v[20:21], v[8:9]
	ds_read_b128 v[8:11], v48 offset:8240
	v_pk_add_f32 v[22:23], v[22:23], v[6:7]
	ds_read_b128 v[4:7], v48 offset:12288
	s_waitcnt lgkmcnt(2)
	v_pk_add_f32 v[36:37], v[36:37], v[14:15]
	v_pk_add_f32 v[38:39], v[38:39], v[12:13]
	s_waitcnt lgkmcnt(1)
	v_pk_add_f32 v[40:41], v[40:41], v[10:11]
	v_pk_add_f32 v[42:43], v[42:43], v[8:9]
	ds_read_b128 v[8:11], v48 offset:12304
	s_waitcnt lgkmcnt(1)
	v_pk_add_f32 v[18:19], v[18:19], v[6:7]
	ds_read_b128 v[12:15], v48 offset:12320
	v_pk_add_f32 v[16:17], v[16:17], v[4:5]
	ds_read_b128 v[4:7], v48 offset:12336
	s_waitcnt lgkmcnt(2)
	v_pk_add_f32 v[10:11], v[20:21], v[10:11]
	s_add_u32 s4, s6, s4
	v_and_b32_e32 v20, 0x3ffc0, v47
	s_addc_u32 s5, s7, s5
	v_lshlrev_b32_e32 v20, 1, v20
	v_mov_b32_e32 v21, v3
	v_pk_add_f32 v[8:9], v[22:23], v[8:9]
	v_and_b32_e32 v22, 0x7f, v32
	v_lshl_add_u64 v[20:21], s[4:5], 0, v[20:21]
	s_movk_i32 s4, 0x7f
	v_mov_b32_e32 v35, v3
	v_cmp_eq_u32_e32 vcc, s4, v22
	v_cvt_pk_bf16_f32 v8, v8, v9
	v_cvt_pk_bf16_f32 v9, v10, v11
	s_waitcnt lgkmcnt(0)
	v_pk_add_f32 v[4:5], v[42:43], v[4:5]
	v_lshl_add_u64 v[20:21], v[20:21], 0, v[34:35]
	v_cndmask_b32_e64 v8, v8, 0, vcc
	v_cndmask_b32_e64 v9, v9, 0, vcc
	v_pk_add_f32 v[14:15], v[36:37], v[14:15]
	v_pk_add_f32 v[12:13], v[38:39], v[12:13]
	v_pk_add_f32 v[6:7], v[40:41], v[6:7]
	v_cvt_pk_bf16_f32 v16, v16, v17
	v_cvt_pk_bf16_f32 v17, v18, v19
	flat_store_dwordx2 v[20:21], v[8:9] offset:32 sc1
	v_cvt_pk_bf16_f32 v8, v12, v13
	v_cvt_pk_bf16_f32 v9, v14, v15
	v_cvt_pk_bf16_f32 v4, v4, v5
	v_cvt_pk_bf16_f32 v5, v6, v7
	v_cndmask_b32_e64 v16, v16, 0, vcc
	v_cndmask_b32_e64 v17, v17, 0, vcc
	v_cndmask_b32_e64 v8, v8, 0, vcc
	v_cndmask_b32_e64 v9, v9, 0, vcc
	v_cndmask_b32_e64 v4, v4, 0, vcc
	v_cndmask_b32_e64 v5, v5, 0, vcc
	flat_store_dwordx2 v[20:21], v[16:17] sc1
	flat_store_dwordx2 v[20:21], v[8:9] offset:64 sc1
	flat_store_dwordx2 v[20:21], v[4:5] offset:96 sc1
	s_branch .LBB0_1310

; __device__ __forceinline__ void stash_acc(lds_fptr stash, const f32x16 (&ob)[2], float f, lds_fptr wsf, int lane, int r32, int hi, bool first) {
;     if (hi == 0) wsf[r32] = f;
;     asm volatile("s_waitcnt lgkmcnt(0)" ::: "memory");
; #pragma unroll
;     for (int g = 0; g < 4; ++g) { const f32x4_t fv = *(const __attribute__((address_space(3))) f32x4_t*)(wsf + 8 * g + 4 * hi);
; #pragma unroll
;         for (int e = 0; e < 4; ++e) { const int r = 4 * g + e;
; #pragma unroll
;             for (int d0 = 0; d0 < 2; ++d0) { const lds_fptr p = stash + (d0 * 16 + r) * 64 + lane; float v = ob[d0][r] * fv[e]; if (!first) v += *p; *p = v; } } }
;     asm volatile("s_waitcnt lgkmcnt(0)" ::: "memory");
; }
.LBB0_1368:
	s_or_b64 exec, exec, s[4:5]
	s_waitcnt lgkmcnt(0)
	ds_read_b128 v[4:7], v229 offset:49152
	ds_read2st64_b32 v[8:9], v228 offset0:200 offset1:201
	ds_read2st64_b32 v[10:11], v228 offset0:216 offset1:217
	s_lshl_b64 s[2:3], s[18:19], 1
	v_readlane_b32 s4, v252, 13
	s_add_u32 s2, s4, s2
	s_waitcnt lgkmcnt(1)
	v_fma_f32 v2, v34, v4, v8
	s_waitcnt lgkmcnt(0)
	v_fma_f32 v4, v18, v4, v10
	v_fmac_f32_e32 v9, v35, v5
	v_fmac_f32_e32 v11, v19, v5
	ds_write2st64_b32 v228, v2, v9 offset0:200 offset1:201
	ds_write2st64_b32 v228, v4, v11 offset0:216 offset1:217
	ds_read2st64_b32 v[4:5], v228 offset0:202 offset1:203
	ds_read2st64_b32 v[8:9], v228 offset0:218 offset1:219
	v_readlane_b32 s4, v252, 14
	s_addc_u32 s3, s4, s3
	s_add_u32 s2, s2, s12
	s_waitcnt lgkmcnt(1)
	v_fma_f32 v2, v36, v6, v4
	s_waitcnt lgkmcnt(0)
	v_fma_f32 v4, v20, v6, v8
	v_fmac_f32_e32 v5, v37, v7
	v_fmac_f32_e32 v9, v21, v7
	ds_write2st64_b32 v228, v2, v5 offset0:202 offset1:203
	ds_write2st64_b32 v228, v4, v9 offset0:218 offset1:219
	ds_read_b128 v[4:7], v229 offset:49184
	ds_read2st64_b32 v[8:9], v228 offset0:204 offset1:205
	ds_read2st64_b32 v[10:11], v228 offset0:220 offset1:221
	v_lshlrev_b32_e32 v36, 1, v212
	s_addc_u32 s3, s3, s13
	s_add_i32 s63, s63, 1
	s_waitcnt lgkmcnt(1)
	v_fma_f32 v2, v38, v4, v8
	s_waitcnt lgkmcnt(0)
	v_fma_f32 v4, v22, v4, v10
	v_fmac_f32_e32 v9, v39, v5
	v_fmac_f32_e32 v11, v23, v5
	ds_write2st64_b32 v228, v2, v9 offset0:204 offset1:205
	ds_write2st64_b32 v228, v4, v11 offset0:220 offset1:221
	ds_read2st64_b32 v[4:5], v228 offset0:206 offset1:207
	ds_read2st64_b32 v[8:9], v228 offset0:222 offset1:223
	s_cmp_eq_u32 s63, 4
	s_waitcnt lgkmcnt(1)
	v_fma_f32 v2, v40, v6, v4
	s_waitcnt lgkmcnt(0)
	v_fma_f32 v4, v24, v6, v8
	v_fmac_f32_e32 v5, v41, v7
	v_fmac_f32_e32 v9, v25, v7
	ds_write2st64_b32 v228, v2, v5 offset0:206 offset1:207
	ds_write2st64_b32 v228, v4, v9 offset0:222 offset1:223
	ds_read_b128 v[4:7], v229 offset:49216
	ds_read2st64_b32 v[8:9], v228 offset0:208 offset1:209
	ds_read2st64_b32 v[10:11], v228 offset0:224 offset1:225
	s_waitcnt lgkmcnt(1)
	v_fma_f32 v2, v42, v4, v8
	s_waitcnt lgkmcnt(0)
	v_fma_f32 v4, v26, v4, v10
	v_fmac_f32_e32 v9, v43, v5
	v_fmac_f32_e32 v11, v27, v5
	ds_write2st64_b32 v228, v2, v9 offset0:208 offset1:209
	ds_write2st64_b32 v228, v4, v11 offset0:224 offset1:225
	ds_read2st64_b32 v[4:5], v228 offset0:210 offset1:211
	ds_read2st64_b32 v[8:9], v228 offset0:226 offset1:227
	s_waitcnt lgkmcnt(1)
	v_fma_f32 v2, v44, v6, v4
	s_waitcnt lgkmcnt(0)
	v_fma_f32 v4, v28, v6, v8
	v_fmac_f32_e32 v5, v45, v7
	v_fmac_f32_e32 v9, v29, v7
	ds_write2st64_b32 v228, v2, v5 offset0:210 offset1:211
	ds_write2st64_b32 v228, v4, v9 offset0:226 offset1:227
	ds_read_b128 v[4:7], v229 offset:49248
	ds_read2st64_b32 v[8:9], v228 offset0:212 offset1:213
	ds_read2st64_b32 v[10:11], v228 offset0:228 offset1:229
	s_waitcnt lgkmcnt(1)
	v_fma_f32 v2, v46, v4, v8
	s_waitcnt lgkmcnt(0)
	v_fma_f32 v4, v30, v4, v10
	v_fmac_f32_e32 v9, v47, v5
	v_fmac_f32_e32 v11, v31, v5
	ds_write2st64_b32 v228, v2, v9 offset0:212 offset1:213
	ds_write2st64_b32 v228, v4, v11 offset0:228 offset1:229
	ds_read2st64_b32 v[4:5], v228 offset0:214 offset1:215
	ds_read2st64_b32 v[8:9], v228 offset0:230 offset1:231
	s_waitcnt lgkmcnt(1)
	v_fma_f32 v2, v48, v6, v4
	s_waitcnt lgkmcnt(0)
	v_fma_f32 v4, v32, v6, v8
	v_fmac_f32_e32 v5, v49, v7
	v_fmac_f32_e32 v9, v33, v7
	ds_write2st64_b32 v228, v2, v5 offset0:214 offset1:215
	ds_write2st64_b32 v228, v4, v9 offset0:230 offset1:231
	s_waitcnt lgkmcnt(0)
; __device__ __forceinline__ int crow(int r,int hi){return (r&3)+8*(r>>2)+4*hi;}
; __device__ __forceinline__ void nsa_unit(int b, int g, int qc, const bf16* Q, const bf16* KV, const bf16* KC2, size_t kvstride, size_t kc2stride, const float* gates, const float* lutg, bf16* O, char* shm) {
;     ...
;     { f32x16 ot[2];
; #pragma unroll
;       for (int d0 = 0; d0 < 2; ++d0)
; #pragma unroll
;           for (int r = 0; r < 16; ++r) ot[d0][r] = stash[(d0 * 16 + r) * 64 + lane];
;       asm volatile("s_waitcnt lgkmcnt(0)" ::: "memory");
;       bf16* stg = (bf16*)(shm + L_OST) + wid * 4096;
; #pragma unroll
;       for (int r = 0; r < 16; ++r) { const int orow = crow(r, hi);
; #pragma unroll
;           for (int d0 = 0; d0 < 2; ++d0) stg[orow * 64 + d0 * 32 + r32] = __float2bfloat16(ot[d0][r]); }
;       asm volatile("s_waitcnt lgkmcnt(0)" ::: "memory");
; #pragma unroll
;       for (int i = 0; i < 4; ++i) { const int row = i * 8 + (lane >> 3), ch = lane & 7; const u32x4 v = *(const u32x4*)(stg + row * 64 + ch * 8); *(u32x4*)(Ow + (size_t)row * 1024 + ch * 8) = v; } }
;     asm volatile("s_waitcnt lgkmcnt(0)\n\ts_barrier" ::: "memory");
	ds_read2st64_b32 v[4:5], v228 offset0:200 offset1:201
	ds_read2st64_b32 v[6:7], v228 offset0:202 offset1:203
	ds_read2st64_b32 v[8:9], v228 offset0:204 offset1:205
	ds_read2st64_b32 v[10:11], v228 offset0:206 offset1:207
	ds_read2st64_b32 v[12:13], v228 offset0:208 offset1:209
	ds_read2st64_b32 v[14:15], v228 offset0:210 offset1:211
	ds_read2st64_b32 v[16:17], v228 offset0:212 offset1:213
	ds_read2st64_b32 v[18:19], v228 offset0:214 offset1:215
	ds_read2st64_b32 v[20:21], v228 offset0:216 offset1:217
	ds_read2st64_b32 v[22:23], v228 offset0:218 offset1:219
	ds_read2st64_b32 v[24:25], v228 offset0:220 offset1:221
	ds_read2st64_b32 v[26:27], v228 offset0:222 offset1:223
	ds_read2st64_b32 v[28:29], v228 offset0:224 offset1:225
	ds_read2st64_b32 v[30:31], v228 offset0:226 offset1:227
	ds_read2st64_b32 v[32:33], v228 offset0:228 offset1:229
	ds_read2st64_b32 v[34:35], v228 offset0:230 offset1:231
	v_lshlrev_b32_e32 v2, 9, v213
	v_add3_u32 v2, s17, v2, v36
	s_waitcnt lgkmcnt(14)
	v_cvt_pk_bf16_f32 v4, v4, s0
	s_waitcnt lgkmcnt(0)
	ds_write_b16 v2, v4 offset:51200
	s_waitcnt lgkmcnt(8)
	v_cvt_pk_bf16_f32 v4, v20, s0
	ds_write_b16 v2, v4 offset:51264
	v_cvt_pk_bf16_f32 v4, v5, s0
	ds_write_b16 v2, v4 offset:51328
	v_cvt_pk_bf16_f32 v4, v21, s0
	ds_write_b16 v2, v4 offset:51392
	v_cvt_pk_bf16_f32 v4, v6, s0
	ds_write_b16 v2, v4 offset:51456
	s_waitcnt lgkmcnt(11)
	v_cvt_pk_bf16_f32 v4, v22, s0
	ds_write_b16 v2, v4 offset:51520
	v_cvt_pk_bf16_f32 v4, v7, s0
	ds_write_b16 v2, v4 offset:51584
	v_cvt_pk_bf16_f32 v4, v23, s0
	ds_write_b16 v2, v4 offset:51648
	v_cvt_pk_bf16_f32 v4, v8, s0
	ds_write_b16 v2, v4 offset:52224
	s_waitcnt lgkmcnt(14)
	v_cvt_pk_bf16_f32 v4, v24, s0
	ds_write_b16 v2, v4 offset:52288
	v_cvt_pk_bf16_f32 v4, v9, s0
	ds_write_b16 v2, v4 offset:52352
	v_cvt_pk_bf16_f32 v4, v25, s0
	ds_write_b16 v2, v4 offset:52416
	v_cvt_pk_bf16_f32 v4, v10, s0
	ds_write_b16 v2, v4 offset:52480
	s_waitcnt lgkmcnt(14)
	v_cvt_pk_bf16_f32 v4, v26, s0
	ds_write_b16 v2, v4 offset:52544
	v_cvt_pk_bf16_f32 v4, v11, s0
	ds_write_b16 v2, v4 offset:52608
	v_cvt_pk_bf16_f32 v4, v27, s0
	ds_write_b16 v2, v4 offset:52672
	v_cvt_pk_bf16_f32 v4, v12, s0
	ds_write_b16 v2, v4 offset:53248
	v_cvt_pk_bf16_f32 v4, v28, s0
	ds_write_b16 v2, v4 offset:53312
	v_cvt_pk_bf16_f32 v4, v13, s0
	ds_write_b16 v2, v4 offset:53376
	v_cvt_pk_bf16_f32 v4, v29, s0
	ds_write_b16 v2, v4 offset:53440
	v_cvt_pk_bf16_f32 v4, v14, s0
	ds_write_b16 v2, v4 offset:53504
	v_cvt_pk_bf16_f32 v4, v30, s0
	ds_write_b16 v2, v4 offset:53568
	v_cvt_pk_bf16_f32 v4, v15, s0
	ds_write_b16 v2, v4 offset:53632
	v_cvt_pk_bf16_f32 v4, v31, s0
	ds_write_b16 v2, v4 offset:53696
	v_cvt_pk_bf16_f32 v4, v16, s0
	ds_write_b16 v2, v4 offset:54272
	v_cvt_pk_bf16_f32 v4, v32, s0
	ds_write_b16 v2, v4 offset:54336
	v_cvt_pk_bf16_f32 v4, v17, s0
	ds_write_b16 v2, v4 offset:54400
	v_cvt_pk_bf16_f32 v4, v33, s0
	ds_write_b16 v2, v4 offset:54464
	v_cvt_pk_bf16_f32 v4, v18, s0
	ds_write_b16 v2, v4 offset:54528
	s_waitcnt lgkmcnt(14)
	v_cvt_pk_bf16_f32 v4, v34, s0
	ds_write_b16 v2, v4 offset:54592
	v_cvt_pk_bf16_f32 v4, v19, s0
	ds_write_b16 v2, v4 offset:54656
	v_cvt_pk_bf16_f32 v4, v35, s0
	ds_write_b16 v2, v4 offset:54720
	v_lshlrev_b32_e32 v2, 1, v226
	v_and_b32_e32 v2, 0x70, v2
	v_lshrrev_b32_e32 v12, 3, v211
	v_add_u32_e32 v13, s17, v2
	s_waitcnt lgkmcnt(0)
	v_lshl_add_u64 v[8:9], s[2:3], 0, v[2:3]
	v_lshl_add_u32 v2, v12, 7, v13
	ds_read_b128 v[4:7], v2 offset:51200
	v_lshlrev_b32_e32 v2, 11, v12
	v_lshl_add_u64 v[10:11], v[8:9], 0, v[2:3]
	v_or_b32_e32 v2, 8, v12
	s_waitcnt lgkmcnt(0)
	flat_store_dwordx4 v[10:11], v[4:7] sc1
	s_nop 1
	v_lshl_add_u32 v4, v2, 7, v13
	ds_read_b128 v[4:7], v4 offset:51200
	v_lshlrev_b32_e32 v2, 11, v2
	v_lshl_add_u64 v[10:11], v[8:9], 0, v[2:3]
	v_or_b32_e32 v2, 16, v12
	s_waitcnt lgkmcnt(0)
	flat_store_dwordx4 v[10:11], v[4:7] sc1
	s_nop 1
	v_lshl_add_u32 v4, v2, 7, v13
	ds_read_b128 v[4:7], v4 offset:51200
	v_lshlrev_b32_e32 v2, 11, v2
	v_lshl_add_u64 v[10:11], v[8:9], 0, v[2:3]
	v_or_b32_e32 v2, 24, v12
	s_waitcnt lgkmcnt(0)
	flat_store_dwordx4 v[10:11], v[4:7] sc1
	s_nop 1
	v_lshl_add_u32 v4, v2, 7, v13
	ds_read_b128 v[4:7], v4 offset:51200
	v_lshlrev_b32_e32 v2, 11, v2
	v_lshl_add_u64 v[8:9], v[8:9], 0, v[2:3]
	s_waitcnt lgkmcnt(0)
	flat_store_dwordx4 v[8:9], v[4:7] sc1
	s_waitcnt lgkmcnt(0)
	s_barrier
	s_cbranch_scc1 .LBB0_1366

; __device__ __forceinline__ void thin_pass(const Ctx& C, const bf16* hin, bf16* hout, bf16* u, float* out, const bf16* y, const float* gpost, float cmul, const float* gpre, bool last) {
;     ...
;         for (int b = 0; b < RB; ++b) { const v4u* yp = (const v4u*)(y + (size_t)(m0 + b) * D); const v4u* hp = (const v4u*)(hin + (size_t)(m0 + b) * D);
;             yr[b][0] = yp[lane]; yr[b][1] = yp[64 + lane]; hr[b][0] = hp[lane]; hr[b][1] = hp[64 + lane]; }
; #pragma unroll
;         for (int b = 0; b < RB; ++b) {
;             const int m = m0 + b; const v4u y0 = yr[b][0], y1 = yr[b][1], h0 = hr[b][0], h1 = hr[b][1];
;             f32x4 yv[4], h[4];
;             yv[0] = (f32x4){bf_lo(y0.x), bf_hi(y0.x), bf_lo(y0.y), bf_hi(y0.y)}; yv[1] = (f32x4){bf_lo(y0.z), bf_hi(y0.z), bf_lo(y0.w), bf_hi(y0.w)};
;             yv[2] = (f32x4){bf_lo(y1.x), bf_hi(y1.x), bf_lo(y1.y), bf_hi(y1.y)}; yv[3] = (f32x4){bf_lo(y1.z), bf_hi(y1.z), bf_lo(y1.w), bf_hi(y1.w)};
;             h[0] = (f32x4){bf_lo(h0.x), bf_hi(h0.x), bf_lo(h0.y), bf_hi(h0.y)}; h[1] = (f32x4){bf_lo(h0.z), bf_hi(h0.z), bf_lo(h0.w), bf_hi(h0.w)};
;             h[2] = (f32x4){bf_lo(h1.x), bf_hi(h1.x), bf_lo(h1.y), bf_hi(h1.y)}; h[3] = (f32x4){bf_lo(h1.z), bf_hi(h1.z), bf_lo(h1.w), bf_hi(h1.w)};
;             float ss = 0.f;
; #pragma unroll
;             for (int i = 0; i < 4; ++i) ss += (yv[i][0] * yv[i][0] + yv[i][1] * yv[i][1]) + (yv[i][2] * yv[i][2] + yv[i][3] * yv[i][3]);
;             const float ry = cmul / sqrtf(wave_sum(ss) * (1.0f / D) + RMS_EPS);
; #pragma unroll
;             for (int i = 0; i < 4; ++i) h[i] = h[i] + yv[i] * ry * g4[i];
;             if (last) { f32x4* op = (f32x4*)(out + (size_t)m * D); op[2 * lane] = h[0]; op[2 * lane + 1] = h[1]; op[128 + 2 * lane] = h[2]; op[128 + 2 * lane + 1] = h[3]; }
;             else {
;                 float s2 = 0.f;
; #pragma unroll
;                 for (int i = 0; i < 4; ++i) s2 += (h[i][0] * h[i][0] + h[i][1] * h[i][1]) + (h[i][2] * h[i][2] + h[i][3] * h[i][3]);
;                 const float rh = 1.0f / sqrtf(wave_sum(s2) * (1.0f / D) + RMS_EPS);
.LBB0_1757:
	v_lshl_add_u64 v[102:103], s[8:9], 0, v[92:93]
	v_add_co_u32_e32 v36, vcc, 0xd000000, v102
	v_lshl_add_u64 v[38:39], s[14:15], 0, v[92:93]
	s_nop 0
	v_addc_co_u32_e32 v37, vcc, 0, v103, vcc
	flat_load_dwordx4 v[84:87], v[36:37]
	flat_load_dwordx4 v[88:91], v[36:37] offset:1024
	v_add_co_u32_e32 v40, vcc, 0x2000000, v38
	s_add_i32 s2, s6, 3
	s_nop 0
	v_addc_co_u32_e32 v41, vcc, 0, v39, vcc
	global_load_dwordx4 v[104:107], v[40:41], off
	global_load_dwordx4 v[108:111], v[40:41], off offset:1024
	flat_load_dwordx4 v[72:75], v[36:37] offset:2048
	flat_load_dwordx4 v[68:71], v[36:37] offset:3072
	global_load_dwordx4 v[80:83], v[40:41], off offset:2048
	global_load_dwordx4 v[76:79], v[40:41], off offset:3072
	s_ashr_i32 s3, s2, 31
	v_add_co_u32_e32 v36, vcc, s91, v102
	s_lshl_b64 s[16:17], s[2:3], 11
	s_nop 0
	v_addc_co_u32_e32 v37, vcc, 0, v103, vcc
	flat_load_dwordx4 v[56:59], v[36:37]
	flat_load_dwordx4 v[52:55], v[36:37] offset:1024
	v_add_co_u32_e32 v36, vcc, s93, v38
	v_lshl_add_u64 v[44:45], v[96:97], 0, s[16:17]
	s_nop 0
	v_addc_co_u32_e32 v37, vcc, 0, v39, vcc
	global_load_dwordx4 v[64:67], v[36:37], off
	global_load_dwordx4 v[60:63], v[36:37], off offset:1024
	v_lshl_add_u64 v[36:37], v[94:95], 0, s[16:17]
	flat_load_dwordx4 v[40:43], v[36:37]
	s_nop 0
	flat_load_dwordx4 v[36:39], v[36:37] offset:1024
	s_nop 0
	global_load_dwordx4 v[48:51], v[44:45], off
	s_nop 0
	global_load_dwordx4 v[44:47], v[44:45], off offset:1024
	s_add_i32 s6, s6, s4
	s_add_u32 s8, s8, s10
	s_addc_u32 s9, s9, s11
	s_waitcnt vmcnt(0) lgkmcnt(0)
	v_lshlrev_b32_e32 v129, 16, v87
	v_lshlrev_b32_e32 v128, 16, v86
	v_lshlrev_b32_e32 v114, 16, v106
	v_and_b32_e32 v115, 0xffff0000, v106
	v_lshlrev_b32_e32 v106, 16, v84
	v_lshlrev_b32_e32 v118, 16, v107
	v_and_b32_e32 v119, 0xffff0000, v107
	v_and_b32_e32 v107, 0xffff0000, v84
	v_mul_f32_e32 v2, v106, v106
	v_lshlrev_b32_e32 v84, 16, v85
	v_lshlrev_b32_e32 v120, 16, v108
	v_and_b32_e32 v121, 0xffff0000, v108
	v_lshlrev_b32_e32 v122, 16, v109
	v_and_b32_e32 v123, 0xffff0000, v109
	v_pk_fma_f32 v[108:109], v[106:107], v[106:107], v[2:3] op_sel_hi:[1,1,0]
	v_and_b32_e32 v85, 0xffff0000, v85
	v_mul_f32_e32 v2, v84, v84
	v_and_b32_e32 v87, 0xffff0000, v87
	v_and_b32_e32 v86, 0xffff0000, v86
	v_lshlrev_b32_e32 v132, 16, v88
	v_lshlrev_b32_e32 v116, 16, v90
	v_lshlrev_b32_e32 v124, 16, v110
	v_and_b32_e32 v125, 0xffff0000, v110
	v_lshlrev_b32_e32 v126, 16, v111
	v_and_b32_e32 v127, 0xffff0000, v111
	v_pk_fma_f32 v[110:111], v[84:85], v[84:85], v[2:3] op_sel_hi:[1,1,0]
	v_pk_mul_f32 v[130:131], v[86:87], v[86:87]
	v_and_b32_e32 v133, 0xffff0000, v88
	v_mul_f32_e32 v2, v132, v132
	v_lshlrev_b32_e32 v88, 16, v89
	v_pk_fma_f32 v[130:131], v[128:129], v[128:129], v[130:131]
	v_pk_fma_f32 v[134:135], v[132:133], v[132:133], v[2:3] op_sel_hi:[1,1,0]
	v_and_b32_e32 v89, 0xffff0000, v89
	v_mul_f32_e32 v2, v88, v88
	v_mov_b32_e32 v117, v109
	v_mov_b32_e32 v138, v116
	v_mov_b32_e32 v139, v111
	v_and_b32_e32 v140, 0xffff0000, v90
	v_lshlrev_b32_e32 v90, 16, v91
	v_and_b32_e32 v91, 0xffff0000, v91
	v_pk_add_f32 v[130:131], v[130:131], v[130:131] op_sel_hi:[0,1]
	v_pk_fma_f32 v[136:137], v[88:89], v[88:89], v[2:3] op_sel_hi:[1,1,0]
	v_pk_mul_f32 v[138:139], v[116:117], v[138:139]
	v_pk_add_f32 v[108:109], v[108:109], v[110:111]
	v_mul_f32_e32 v130, v140, v140
	v_mul_f32_e32 v134, v90, v90
	v_mul_f32_e32 v136, v91, v91
	v_mov_b32_e32 v139, v109
	v_pk_add_f32 v[108:109], v[138:139], v[130:131]
	v_pk_add_f32 v[110:111], v[134:135], v[136:137]
	v_lshlrev_b32_e32 v112, 16, v104
	v_pk_add_f32 v[108:109], v[108:109], v[110:111]
	v_and_b32_e32 v113, 0xffff0000, v104
	v_add_f32_e32 v2, v108, v109
	v_lshlrev_b32_e32 v104, 16, v105
	v_and_b32_e32 v105, 0xffff0000, v105
	v_add_f32_dpp v2, v2, v2 quad_perm:[1,0,3,2] row_mask:0xf bank_mask:0xf bound_ctrl:1
	s_nop 1
	v_add_f32_dpp v2, v2, v2 quad_perm:[2,3,0,1] row_mask:0xf bank_mask:0xf bound_ctrl:1
	s_nop 1
	v_add_f32_dpp v2, v2, v2 row_half_mirror row_mask:0xf bank_mask:0xf bound_ctrl:1
	s_nop 1
	v_add_f32_dpp v2, v2, v2 row_mirror row_mask:0xf bank_mask:0xf bound_ctrl:1
	s_nop 0
	v_readlane_b32 s5, v2, 16
	v_readlane_b32 s7, v2, 48
	v_readlane_b32 s2, v2, 0
	v_readlane_b32 s3, v2, 32
	v_mov_b32_e32 v108, s5
	v_mov_b32_e32 v109, s7
	v_pk_add_f32 v[108:109], s[2:3], v[108:109]
	s_nop 0
	v_add_f32_e32 v2, v108, v109
	v_fmamk_f32 v2, v2, 0x3a800000, v214
	v_rsq_f32_e32 v2, v2
	s_nop 0
	v_pk_mul_f32 v[84:85], v[2:3], v[84:85] op_sel_hi:[0,1]
	v_pk_fma_f32 v[104:105], v[10:11], v[84:85], v[104:105]
	v_mov_b32_e32 v84, v128
	v_mov_b32_e32 v85, v86
	v_mov_b32_e32 v86, v129
	v_pk_mul_f32 v[106:107], v[2:3], v[106:107] op_sel_hi:[0,1]
	v_pk_mul_f32 v[84:85], v[2:3], v[84:85] op_sel_hi:[0,1]
	v_pk_mul_f32 v[86:87], v[2:3], v[86:87] op_sel_hi:[0,1]
	v_pk_fma_f32 v[106:107], v[8:9], v[106:107], v[112:113]
	v_pk_fma_f32 v[108:109], v[6:7], v[86:87], v[118:119]
	v_pk_fma_f32 v[112:113], v[4:5], v[84:85], v[114:115]
	v_pk_mul_f32 v[84:85], v[2:3], v[132:133] op_sel_hi:[0,1]
	v_pk_mul_f32 v[86:87], v[2:3], v[88:89] op_sel_hi:[0,1]
	v_mov_b32_e32 v117, v140
	v_pk_fma_f32 v[110:111], v[18:19], v[86:87], v[122:123]
	v_pk_fma_f32 v[114:115], v[16:17], v[84:85], v[120:121]
	v_pk_mul_f32 v[84:85], v[90:91], v[2:3] op_sel_hi:[1,0]
	v_pk_mul_f32 v[86:87], v[116:117], v[2:3] op_sel_hi:[1,0]
	v_pk_fma_f32 v[118:119], v[14:15], v[84:85], v[126:127]
	v_pk_fma_f32 v[116:117], v[12:13], v[86:87], v[124:125]
	v_pk_mul_f32 v[84:85], v[104:105], v[104:105]
	v_pk_mul_f32 v[86:87], v[106:107], v[106:107]
	v_mul_f32_e32 v2, v114, v114
	v_pk_mov_b32 v[88:89], v[86:87], v[84:85] op_sel:[1,0]
	v_mov_b32_e32 v87, v85
; __device__ __forceinline__ void thin_pass(const Ctx& C, const bf16* hin, bf16* hout, bf16* u, float* out, const bf16* y, const float* gpost, float cmul, const float* gpre, bool last) {
;     ...
;         for (int b = 0; b < RB; ++b) {
;             const int m = m0 + b; const v4u y0 = yr[b][0], y1 = yr[b][1], h0 = hr[b][0], h1 = hr[b][1];
;             f32x4 yv[4], h[4];
;             yv[0] = (f32x4){bf_lo(y0.x), bf_hi(y0.x), bf_lo(y0.y), bf_hi(y0.y)}; yv[1] = (f32x4){bf_lo(y0.z), bf_hi(y0.z), bf_lo(y0.w), bf_hi(y0.w)};
;             yv[2] = (f32x4){bf_lo(y1.x), bf_hi(y1.x), bf_lo(y1.y), bf_hi(y1.y)}; yv[3] = (f32x4){bf_lo(y1.z), bf_hi(y1.z), bf_lo(y1.w), bf_hi(y1.w)};
;             h[0] = (f32x4){bf_lo(h0.x), bf_hi(h0.x), bf_lo(h0.y), bf_hi(h0.y)}; h[1] = (f32x4){bf_lo(h0.z), bf_hi(h0.z), bf_lo(h0.w), bf_hi(h0.w)};
;             h[2] = (f32x4){bf_lo(h1.x), bf_hi(h1.x), bf_lo(h1.y), bf_hi(h1.y)}; h[3] = (f32x4){bf_lo(h1.z), bf_hi(h1.z), bf_lo(h1.w), bf_hi(h1.w)};
;             float ss = 0.f;
; #pragma unroll
;             for (int i = 0; i < 4; ++i) ss += (yv[i][0] * yv[i][0] + yv[i][1] * yv[i][1]) + (yv[i][2] * yv[i][2] + yv[i][3] * yv[i][3]);
;             const float ry = cmul / sqrtf(wave_sum(ss) * (1.0f / D) + RMS_EPS);
; #pragma unroll
;             for (int i = 0; i < 4; ++i) h[i] = h[i] + yv[i] * ry * g4[i];
;             if (last) { f32x4* op = (f32x4*)(out + (size_t)m * D); op[2 * lane] = h[0]; op[2 * lane + 1] = h[1]; op[128 + 2 * lane] = h[2]; op[128 + 2 * lane + 1] = h[3]; }
;             else {
;                 float s2 = 0.f;
; #pragma unroll
;                 for (int i = 0; i < 4; ++i) s2 += (h[i][0] * h[i][0] + h[i][1] * h[i][1]) + (h[i][2] * h[i][2] + h[i][3] * h[i][3]);
;                 const float rh = 1.0f / sqrtf(wave_sum(s2) * (1.0f / D) + RMS_EPS);
;                 v4u o0, o1; o0.x = pk2(h[0][0], h[0][1]); o0.y = pk2(h[0][2], h[0][3]); o0.z = pk2(h[1][0], h[1][1]); o0.w = pk2(h[1][2], h[1][3]);
;                 o1.x = pk2(h[2][0], h[2][1]); o1.y = pk2(h[2][2], h[2][3]); o1.z = pk2(h[3][0], h[3][1]); o1.w = pk2(h[3][2], h[3][3]);
;                 v4u* hp = (v4u*)(hout + (size_t)m * D); hp[lane] = o0; hp[64 + lane] = o1;
; #pragma unroll
;                 for (int i = 0; i < 4; ++i) h[i] = h[i] * rh * q4[i];
	v_pk_add_f32 v[84:85], v[88:89], v[86:87]
	v_pk_mul_f32 v[86:87], v[108:109], v[108:109]
	v_pk_mul_f32 v[88:89], v[112:113], v[112:113]
	v_pk_add_f32 v[84:85], v[84:85], v[84:85] op_sel_hi:[0,1]
	v_pk_mov_b32 v[90:91], v[88:89], v[86:87] op_sel:[1,0]
	v_mov_b32_e32 v89, v87
	v_pk_add_f32 v[86:87], v[90:91], v[88:89]
	v_pk_fma_f32 v[88:89], v[114:115], v[114:115], v[2:3] op_sel_hi:[1,1,0]
	v_mul_f32_e32 v2, v110, v110
	v_pk_add_f32 v[86:87], v[86:87], v[86:87] op_sel_hi:[0,1]
	v_pk_fma_f32 v[90:91], v[110:111], v[110:111], v[2:3] op_sel_hi:[1,1,0]
	v_mul_f32_e32 v88, v116, v116
	v_mul_f32_e32 v90, v117, v117
	v_mul_f32_e32 v84, v118, v118
	v_mul_f32_e32 v86, v119, v119
	v_pk_add_f32 v[88:89], v[88:89], v[90:91]
	v_pk_add_f32 v[84:85], v[84:85], v[86:87]
	v_cvt_pk_bf16_f32 v90, v116, v117
	v_cvt_pk_bf16_f32 v91, v118, v119
	v_lshl_add_u64 v[120:121], s[12:13], 0, v[92:93]
	v_pk_add_f32 v[84:85], v[88:89], v[84:85]
	v_cvt_pk_bf16_f32 v89, v110, v111
	v_and_b32_e32 v128, 0xffff0000, v70
	v_add_f32_e32 v2, v84, v85
	s_add_u32 s12, s12, s10
	s_addc_u32 s13, s13, s11
	v_add_f32_dpp v2, v2, v2 quad_perm:[1,0,3,2] row_mask:0xf bank_mask:0xf bound_ctrl:1
	s_add_u32 s14, s14, s10
	s_addc_u32 s15, s15, s11
	v_add_f32_dpp v2, v2, v2 quad_perm:[2,3,0,1] row_mask:0xf bank_mask:0xf bound_ctrl:1
	s_cmp_lt_i32 s6, s1
	s_nop 0
	v_add_f32_dpp v2, v2, v2 row_half_mirror row_mask:0xf bank_mask:0xf bound_ctrl:1
	s_nop 1
	v_add_f32_dpp v2, v2, v2 row_mirror row_mask:0xf bank_mask:0xf bound_ctrl:1
	s_nop 0
	v_readlane_b32 s5, v2, 16
	v_readlane_b32 s7, v2, 48
	v_readlane_b32 s2, v2, 0
	v_readlane_b32 s3, v2, 32
	v_mov_b32_e32 v84, s5
	v_mov_b32_e32 v85, s7
	v_pk_add_f32 v[84:85], s[2:3], v[84:85]
	s_nop 0
	v_add_f32_e32 v2, v84, v85
	v_fmamk_f32 v2, v2, 0x3a800000, v214
	s_mov_b32 s2, 0xb000000
	v_rsq_f32_e32 v2, v2
	s_nop 0
	v_cvt_pk_bf16_f32 v84, v106, v107
	v_cvt_pk_bf16_f32 v85, v104, v105
	v_cvt_pk_bf16_f32 v86, v112, v113
	v_cvt_pk_bf16_f32 v87, v108, v109
	v_cvt_pk_bf16_f32 v88, v114, v115
	flat_store_dwordx4 v[120:121], v[84:87] sc1
	flat_store_dwordx4 v[120:121], v[88:91] offset:1024 sc1
	s_nop 0
	v_pk_mul_f32 v[84:85], v[106:107], v[2:3] op_sel_hi:[1,0]
	v_pk_mul_f32 v[86:87], v[104:105], v[2:3] op_sel_hi:[1,0]
	v_pk_mul_f32 v[90:91], v[108:109], v[2:3] op_sel_hi:[1,0]
	v_pk_mul_f32 v[108:109], v[116:117], v[2:3] op_sel_hi:[1,0]
	v_pk_mul_f32 v[86:87], v[26:27], v[86:87]
	v_pk_mul_f32 v[84:85], v[24:25], v[84:85]
	v_pk_mul_f32 v[88:89], v[112:113], v[2:3] op_sel_hi:[1,0]
	v_pk_mul_f32 v[90:91], v[22:23], v[90:91]
	v_pk_mul_f32 v[104:105], v[114:115], v[2:3] op_sel_hi:[1,0]
	v_pk_mul_f32 v[108:109], v[28:29], v[108:109]
	v_pk_mul_f32 v[88:89], v[20:21], v[88:89]
	v_pk_mul_f32 v[106:107], v[110:111], v[2:3] op_sel_hi:[1,0]
	v_pk_mul_f32 v[104:105], v[32:33], v[104:105]
	v_pk_mul_f32 v[110:111], v[118:119], v[2:3] op_sel_hi:[1,0]
	v_cvt_pk_bf16_f32 v84, v84, v85
	v_cvt_pk_bf16_f32 v85, v86, v87
	v_cvt_pk_bf16_f32 v87, v90, v91
	v_cvt_pk_bf16_f32 v90, v108, v109
	v_lshlrev_b32_e32 v108, 16, v72
	v_pk_mul_f32 v[110:111], v[30:31], v[110:111]
	v_cvt_pk_bf16_f32 v86, v88, v89
	v_cvt_pk_bf16_f32 v88, v104, v105
	v_add_co_u32_e32 v104, vcc, s2, v102
	v_and_b32_e32 v109, 0xffff0000, v72
	v_mul_f32_e32 v2, v108, v108
	v_lshlrev_b32_e32 v72, 16, v73
	v_cvt_pk_bf16_f32 v91, v110, v111
	v_addc_co_u32_e32 v105, vcc, 0, v103, vcc
	v_pk_fma_f32 v[110:111], v[108:109], v[108:109], v[2:3] op_sel_hi:[1,1,0]
	v_and_b32_e32 v73, 0xffff0000, v73
	v_mul_f32_e32 v2, v72, v72
	v_lshlrev_b32_e32 v115, 16, v75
	v_lshlrev_b32_e32 v114, 16, v74
	v_and_b32_e32 v75, 0xffff0000, v75
	v_and_b32_e32 v74, 0xffff0000, v74
	v_lshlrev_b32_e32 v118, 16, v68
	v_pk_mul_f32 v[106:107], v[34:35], v[106:107]
	v_pk_fma_f32 v[112:113], v[72:73], v[72:73], v[2:3] op_sel_hi:[1,1,0]
	v_cvt_pk_bf16_f32 v89, v106, v107
	flat_store_dwordx4 v[104:105], v[84:87] sc1
	flat_store_dwordx4 v[104:105], v[88:91] offset:1024 sc1
	v_pk_mul_f32 v[116:117], v[74:75], v[74:75]
	v_lshlrev_b32_e32 v84, 16, v70
	v_and_b32_e32 v119, 0xffff0000, v68
	v_mul_f32_e32 v2, v118, v118
	v_lshlrev_b32_e32 v68, 16, v69
	v_pk_fma_f32 v[116:117], v[114:115], v[114:115], v[116:117]
	v_pk_fma_f32 v[122:123], v[118:119], v[118:119], v[2:3] op_sel_hi:[1,1,0]
	v_and_b32_e32 v69, 0xffff0000, v69
	v_mul_f32_e32 v2, v68, v68
	v_mov_b32_e32 v85, v111
	v_mov_b32_e32 v126, v84
	v_mov_b32_e32 v127, v113
	v_lshlrev_b32_e32 v70, 16, v71
	v_and_b32_e32 v71, 0xffff0000, v71
	v_pk_add_f32 v[116:117], v[116:117], v[116:117] op_sel_hi:[0,1]
	v_pk_fma_f32 v[124:125], v[68:69], v[68:69], v[2:3] op_sel_hi:[1,1,0]
	v_pk_mul_f32 v[126:127], v[84:85], v[126:127]
	v_pk_add_f32 v[110:111], v[110:111], v[112:113]
	v_mul_f32_e32 v116, v128, v128
	v_mul_f32_e32 v122, v70, v70
	v_mul_f32_e32 v124, v71, v71
	v_mov_b32_e32 v127, v111
	v_pk_add_f32 v[110:111], v[126:127], v[116:117]
	v_pk_add_f32 v[112:113], v[122:123], v[124:125]
	v_lshlrev_b32_e32 v86, 16, v80
	v_pk_add_f32 v[110:111], v[110:111], v[112:113]
	v_and_b32_e32 v87, 0xffff0000, v80
	v_add_f32_e32 v2, v110, v111
	v_lshlrev_b32_e32 v80, 16, v81
	v_and_b32_e32 v81, 0xffff0000, v81
	v_add_f32_dpp v2, v2, v2 quad_perm:[1,0,3,2] row_mask:0xf bank_mask:0xf bound_ctrl:1
	v_lshlrev_b32_e32 v90, 16, v76
	v_and_b32_e32 v91, 0xffff0000, v76
	v_add_f32_dpp v2, v2, v2 quad_perm:[2,3,0,1] row_mask:0xf bank_mask:0xf bound_ctrl:1
	v_lshlrev_b32_e32 v76, 16, v77
	v_and_b32_e32 v77, 0xffff0000, v77
	v_add_f32_dpp v2, v2, v2 row_half_mirror row_mask:0xf bank_mask:0xf bound_ctrl:1
	v_lshlrev_b32_e32 v88, 16, v82
	v_and_b32_e32 v89, 0xffff0000, v82
	v_add_f32_dpp v2, v2, v2 row_mirror row_mask:0xf bank_mask:0xf bound_ctrl:1
; __device__ __forceinline__ void thin_pass(const Ctx& C, const bf16* hin, bf16* hout, bf16* u, float* out, const bf16* y, const float* gpost, float cmul, const float* gpre, bool last) {
;     ...
;         for (int b = 0; b < RB; ++b) {
;             const int m = m0 + b; const v4u y0 = yr[b][0], y1 = yr[b][1], h0 = hr[b][0], h1 = hr[b][1];
;             f32x4 yv[4], h[4];
;             yv[0] = (f32x4){bf_lo(y0.x), bf_hi(y0.x), bf_lo(y0.y), bf_hi(y0.y)}; yv[1] = (f32x4){bf_lo(y0.z), bf_hi(y0.z), bf_lo(y0.w), bf_hi(y0.w)};
;             yv[2] = (f32x4){bf_lo(y1.x), bf_hi(y1.x), bf_lo(y1.y), bf_hi(y1.y)}; yv[3] = (f32x4){bf_lo(y1.z), bf_hi(y1.z), bf_lo(y1.w), bf_hi(y1.w)};
;             h[0] = (f32x4){bf_lo(h0.x), bf_hi(h0.x), bf_lo(h0.y), bf_hi(h0.y)}; h[1] = (f32x4){bf_lo(h0.z), bf_hi(h0.z), bf_lo(h0.w), bf_hi(h0.w)};
;             h[2] = (f32x4){bf_lo(h1.x), bf_hi(h1.x), bf_lo(h1.y), bf_hi(h1.y)}; h[3] = (f32x4){bf_lo(h1.z), bf_hi(h1.z), bf_lo(h1.w), bf_hi(h1.w)};
;             float ss = 0.f;
; #pragma unroll
;             for (int i = 0; i < 4; ++i) ss += (yv[i][0] * yv[i][0] + yv[i][1] * yv[i][1]) + (yv[i][2] * yv[i][2] + yv[i][3] * yv[i][3]);
;             const float ry = cmul / sqrtf(wave_sum(ss) * (1.0f / D) + RMS_EPS);
; #pragma unroll
;             for (int i = 0; i < 4; ++i) h[i] = h[i] + yv[i] * ry * g4[i];
;             if (last) { f32x4* op = (f32x4*)(out + (size_t)m * D); op[2 * lane] = h[0]; op[2 * lane + 1] = h[1]; op[128 + 2 * lane] = h[2]; op[128 + 2 * lane + 1] = h[3]; }
;             else {
;                 float s2 = 0.f;
; #pragma unroll
;                 for (int i = 0; i < 4; ++i) s2 += (h[i][0] * h[i][0] + h[i][1] * h[i][1]) + (h[i][2] * h[i][2] + h[i][3] * h[i][3]);
;                 const float rh = 1.0f / sqrtf(wave_sum(s2) * (1.0f / D) + RMS_EPS);
;                 v4u o0, o1; o0.x = pk2(h[0][0], h[0][1]); o0.y = pk2(h[0][2], h[0][3]); o0.z = pk2(h[1][0], h[1][1]); o0.w = pk2(h[1][2], h[1][3]);
;                 o1.x = pk2(h[2][0], h[2][1]); o1.y = pk2(h[2][2], h[2][3]); o1.z = pk2(h[3][0], h[3][1]); o1.w = pk2(h[3][2], h[3][3]);
;                 v4u* hp = (v4u*)(hout + (size_t)m * D); hp[lane] = o0; hp[64 + lane] = o1;
; #pragma unroll
;                 for (int i = 0; i < 4; ++i) h[i] = h[i] * rh * q4[i];
	v_lshlrev_b32_e32 v106, 16, v78
	v_readlane_b32 s5, v2, 16
	v_readlane_b32 s7, v2, 48
	v_readlane_b32 s2, v2, 0
	v_readlane_b32 s3, v2, 32
	v_mov_b32_e32 v110, s5
	v_mov_b32_e32 v111, s7
	v_pk_add_f32 v[110:111], s[2:3], v[110:111]
	v_and_b32_e32 v107, 0xffff0000, v78
	v_add_f32_e32 v2, v110, v111
	v_fmamk_f32 v2, v2, 0x3a800000, v214
	v_lshlrev_b32_e32 v78, 16, v79
	v_and_b32_e32 v79, 0xffff0000, v79
	v_lshlrev_b32_e32 v82, 16, v83
	v_and_b32_e32 v83, 0xffff0000, v83
	v_rsq_f32_e32 v2, v2
	s_nop 0
	v_pk_mul_f32 v[72:73], v[2:3], v[72:73] op_sel_hi:[0,1]
	v_pk_mul_f32 v[108:109], v[2:3], v[108:109] op_sel_hi:[0,1]
	v_pk_fma_f32 v[80:81], v[10:11], v[72:73], v[80:81]
	v_mov_b32_e32 v72, v114
	v_mov_b32_e32 v73, v74
	v_pk_mul_f32 v[68:69], v[2:3], v[68:69] op_sel_hi:[0,1]
	v_mov_b32_e32 v85, v128
	v_pk_fma_f32 v[86:87], v[8:9], v[108:109], v[86:87]
	v_pk_mul_f32 v[72:73], v[2:3], v[72:73] op_sel_hi:[0,1]
	v_mov_b32_e32 v74, v115
	v_pk_fma_f32 v[76:77], v[18:19], v[68:69], v[76:77]
	v_pk_mul_f32 v[68:69], v[70:71], v[2:3] op_sel_hi:[1,0]
	v_pk_mul_f32 v[70:71], v[84:85], v[2:3] op_sel_hi:[1,0]
	v_pk_mul_f32 v[74:75], v[2:3], v[74:75] op_sel_hi:[0,1]
	v_pk_fma_f32 v[88:89], v[4:5], v[72:73], v[88:89]
	v_pk_mul_f32 v[72:73], v[2:3], v[118:119] op_sel_hi:[0,1]
	v_pk_fma_f32 v[84:85], v[12:13], v[70:71], v[106:107]
	v_pk_fma_f32 v[78:79], v[14:15], v[68:69], v[78:79]
	v_pk_mul_f32 v[68:69], v[80:81], v[80:81]
	v_pk_mul_f32 v[70:71], v[86:87], v[86:87]
	v_pk_fma_f32 v[82:83], v[6:7], v[74:75], v[82:83]
	v_pk_fma_f32 v[90:91], v[16:17], v[72:73], v[90:91]
	v_pk_mov_b32 v[72:73], v[70:71], v[68:69] op_sel:[1,0]
	v_mov_b32_e32 v71, v69
	v_pk_add_f32 v[68:69], v[72:73], v[70:71]
	v_pk_mul_f32 v[70:71], v[82:83], v[82:83]
	v_pk_mul_f32 v[72:73], v[88:89], v[88:89]
	v_mul_f32_e32 v2, v90, v90
	v_pk_mov_b32 v[74:75], v[72:73], v[70:71] op_sel:[1,0]
	v_mov_b32_e32 v73, v71
	v_pk_add_f32 v[70:71], v[74:75], v[72:73]
	v_pk_fma_f32 v[72:73], v[90:91], v[90:91], v[2:3] op_sel_hi:[1,1,0]
	v_mul_f32_e32 v2, v76, v76
	v_pk_add_f32 v[68:69], v[68:69], v[68:69] op_sel_hi:[0,1]
	v_pk_add_f32 v[70:71], v[70:71], v[70:71] op_sel_hi:[0,1]
	v_pk_fma_f32 v[74:75], v[76:77], v[76:77], v[2:3] op_sel_hi:[1,1,0]
	v_mul_f32_e32 v72, v84, v84
	v_mul_f32_e32 v74, v85, v85
	v_mul_f32_e32 v68, v78, v78
	v_mul_f32_e32 v70, v79, v79
	v_pk_add_f32 v[72:73], v[72:73], v[74:75]
	v_pk_add_f32 v[68:69], v[68:69], v[70:71]
	v_cvt_pk_bf16_f32 v74, v84, v85
	v_cvt_pk_bf16_f32 v75, v78, v79
	v_and_b32_e32 v108, 0xffff0000, v54
	v_pk_add_f32 v[68:69], v[72:73], v[68:69]
	v_cvt_pk_bf16_f32 v73, v76, v77
	s_nop 0
	v_add_f32_e32 v2, v68, v69
	s_nop 1
	v_add_f32_dpp v2, v2, v2 quad_perm:[1,0,3,2] row_mask:0xf bank_mask:0xf bound_ctrl:1
	s_nop 1
	v_add_f32_dpp v2, v2, v2 quad_perm:[2,3,0,1] row_mask:0xf bank_mask:0xf bound_ctrl:1
	s_nop 1
	v_add_f32_dpp v2, v2, v2 row_half_mirror row_mask:0xf bank_mask:0xf bound_ctrl:1
	s_nop 1
	v_add_f32_dpp v2, v2, v2 row_mirror row_mask:0xf bank_mask:0xf bound_ctrl:1
	s_nop 0
	v_readlane_b32 s5, v2, 16
	v_readlane_b32 s7, v2, 48
	v_readlane_b32 s2, v2, 0
	v_readlane_b32 s3, v2, 32
	v_mov_b32_e32 v68, s5
	v_mov_b32_e32 v69, s7
	v_pk_add_f32 v[68:69], s[2:3], v[68:69]
	s_nop 0
	v_add_f32_e32 v2, v68, v69
	v_fmamk_f32 v2, v2, 0x3a800000, v214
	v_rsq_f32_e32 v2, v2
	s_nop 0
	v_cvt_pk_bf16_f32 v68, v86, v87
	v_cvt_pk_bf16_f32 v69, v80, v81
	v_cvt_pk_bf16_f32 v70, v88, v89
	v_cvt_pk_bf16_f32 v71, v82, v83
	v_cvt_pk_bf16_f32 v72, v90, v91
	flat_store_dwordx4 v[120:121], v[68:71] offset:2048 sc1
	flat_store_dwordx4 v[120:121], v[72:75] offset:3072 sc1
	v_pk_mul_f32 v[78:79], v[78:79], v[2:3] op_sel_hi:[1,0]
	v_pk_mul_f32 v[68:69], v[86:87], v[2:3] op_sel_hi:[1,0]
	v_pk_mul_f32 v[70:71], v[80:81], v[2:3] op_sel_hi:[1,0]
	v_pk_mul_f32 v[74:75], v[82:83], v[2:3] op_sel_hi:[1,0]
	v_pk_mul_f32 v[70:71], v[26:27], v[70:71]
	v_pk_mul_f32 v[68:69], v[24:25], v[68:69]
	v_pk_mul_f32 v[74:75], v[22:23], v[74:75]
	v_pk_mul_f32 v[78:79], v[30:31], v[78:79]
	v_pk_mul_f32 v[72:73], v[88:89], v[2:3] op_sel_hi:[1,0]
	v_pk_mul_f32 v[80:81], v[90:91], v[2:3] op_sel_hi:[1,0]
	v_cvt_pk_bf16_f32 v68, v68, v69
	v_cvt_pk_bf16_f32 v69, v70, v71
	v_cvt_pk_bf16_f32 v71, v74, v75
	v_cvt_pk_bf16_f32 v75, v78, v79
	v_lshlrev_b32_e32 v78, 16, v56
	v_pk_mul_f32 v[72:73], v[20:21], v[72:73]
	v_pk_mul_f32 v[76:77], v[76:77], v[2:3] op_sel_hi:[1,0]
	v_pk_mul_f32 v[80:81], v[32:33], v[80:81]
	v_pk_mul_f32 v[82:83], v[84:85], v[2:3] op_sel_hi:[1,0]
	v_and_b32_e32 v79, 0xffff0000, v56
	v_mul_f32_e32 v2, v78, v78
	v_lshlrev_b32_e32 v56, 16, v57
	v_pk_mul_f32 v[82:83], v[28:29], v[82:83]
	v_cvt_pk_bf16_f32 v70, v72, v73
	v_cvt_pk_bf16_f32 v72, v80, v81
	v_pk_fma_f32 v[80:81], v[78:79], v[78:79], v[2:3] op_sel_hi:[1,1,0]
	v_and_b32_e32 v57, 0xffff0000, v57
	v_mul_f32_e32 v2, v56, v56
	v_lshlrev_b32_e32 v85, 16, v59
	v_lshlrev_b32_e32 v84, 16, v58
	v_and_b32_e32 v59, 0xffff0000, v59
	v_and_b32_e32 v58, 0xffff0000, v58
	v_lshlrev_b32_e32 v88, 16, v52
	v_pk_mul_f32 v[76:77], v[34:35], v[76:77]
	v_cvt_pk_bf16_f32 v74, v82, v83
	v_pk_fma_f32 v[82:83], v[56:57], v[56:57], v[2:3] op_sel_hi:[1,1,0]
	v_cvt_pk_bf16_f32 v73, v76, v77
	flat_store_dwordx4 v[104:105], v[68:71] offset:2048 sc1
	flat_store_dwordx4 v[104:105], v[72:75] offset:3072 sc1
	v_pk_mul_f32 v[86:87], v[58:59], v[58:59]
	v_lshlrev_b32_e32 v68, 16, v54
	v_and_b32_e32 v89, 0xffff0000, v52
	v_mul_f32_e32 v2, v88, v88
	v_lshlrev_b32_e32 v52, 16, v53
	v_pk_fma_f32 v[86:87], v[84:85], v[84:85], v[86:87]
	v_pk_fma_f32 v[90:91], v[88:89], v[88:89], v[2:3] op_sel_hi:[1,1,0]
	v_and_b32_e32 v53, 0xffff0000, v53
	v_mul_f32_e32 v2, v52, v52
	v_mov_b32_e32 v69, v81
; __device__ __forceinline__ void thin_pass(const Ctx& C, const bf16* hin, bf16* hout, bf16* u, float* out, const bf16* y, const float* gpost, float cmul, const float* gpre, bool last) {
;     ...
;         for (int b = 0; b < RB; ++b) {
;             const int m = m0 + b; const v4u y0 = yr[b][0], y1 = yr[b][1], h0 = hr[b][0], h1 = hr[b][1];
;             f32x4 yv[4], h[4];
;             yv[0] = (f32x4){bf_lo(y0.x), bf_hi(y0.x), bf_lo(y0.y), bf_hi(y0.y)}; yv[1] = (f32x4){bf_lo(y0.z), bf_hi(y0.z), bf_lo(y0.w), bf_hi(y0.w)};
;             yv[2] = (f32x4){bf_lo(y1.x), bf_hi(y1.x), bf_lo(y1.y), bf_hi(y1.y)}; yv[3] = (f32x4){bf_lo(y1.z), bf_hi(y1.z), bf_lo(y1.w), bf_hi(y1.w)};
;             h[0] = (f32x4){bf_lo(h0.x), bf_hi(h0.x), bf_lo(h0.y), bf_hi(h0.y)}; h[1] = (f32x4){bf_lo(h0.z), bf_hi(h0.z), bf_lo(h0.w), bf_hi(h0.w)};
;             h[2] = (f32x4){bf_lo(h1.x), bf_hi(h1.x), bf_lo(h1.y), bf_hi(h1.y)}; h[3] = (f32x4){bf_lo(h1.z), bf_hi(h1.z), bf_lo(h1.w), bf_hi(h1.w)};
;             float ss = 0.f;
; #pragma unroll
;             for (int i = 0; i < 4; ++i) ss += (yv[i][0] * yv[i][0] + yv[i][1] * yv[i][1]) + (yv[i][2] * yv[i][2] + yv[i][3] * yv[i][3]);
;             const float ry = cmul / sqrtf(wave_sum(ss) * (1.0f / D) + RMS_EPS);
; #pragma unroll
;             for (int i = 0; i < 4; ++i) h[i] = h[i] + yv[i] * ry * g4[i];
;             if (last) { f32x4* op = (f32x4*)(out + (size_t)m * D); op[2 * lane] = h[0]; op[2 * lane + 1] = h[1]; op[128 + 2 * lane] = h[2]; op[128 + 2 * lane + 1] = h[3]; }
;             else {
;                 float s2 = 0.f;
; #pragma unroll
;                 for (int i = 0; i < 4; ++i) s2 += (h[i][0] * h[i][0] + h[i][1] * h[i][1]) + (h[i][2] * h[i][2] + h[i][3] * h[i][3]);
;                 const float rh = 1.0f / sqrtf(wave_sum(s2) * (1.0f / D) + RMS_EPS);
;                 v4u o0, o1; o0.x = pk2(h[0][0], h[0][1]); o0.y = pk2(h[0][2], h[0][3]); o0.z = pk2(h[1][0], h[1][1]); o0.w = pk2(h[1][2], h[1][3]);
;                 o1.x = pk2(h[2][0], h[2][1]); o1.y = pk2(h[2][2], h[2][3]); o1.z = pk2(h[3][0], h[3][1]); o1.w = pk2(h[3][2], h[3][3]);
;                 v4u* hp = (v4u*)(hout + (size_t)m * D); hp[lane] = o0; hp[64 + lane] = o1;
; #pragma unroll
;                 for (int i = 0; i < 4; ++i) h[i] = h[i] * rh * q4[i];
	v_mov_b32_e32 v106, v68
	v_mov_b32_e32 v107, v83
	v_lshlrev_b32_e32 v54, 16, v55
	v_and_b32_e32 v55, 0xffff0000, v55
	v_pk_add_f32 v[86:87], v[86:87], v[86:87] op_sel_hi:[0,1]
	v_pk_fma_f32 v[104:105], v[52:53], v[52:53], v[2:3] op_sel_hi:[1,1,0]
	v_pk_mul_f32 v[106:107], v[68:69], v[106:107]
	v_pk_add_f32 v[80:81], v[80:81], v[82:83]
	v_mul_f32_e32 v86, v108, v108
	v_mul_f32_e32 v90, v54, v54
	v_mul_f32_e32 v104, v55, v55
	v_mov_b32_e32 v107, v81
	v_pk_add_f32 v[80:81], v[106:107], v[86:87]
	v_pk_add_f32 v[82:83], v[90:91], v[104:105]
	v_lshlrev_b32_e32 v70, 16, v64
	v_pk_add_f32 v[80:81], v[80:81], v[82:83]
	v_and_b32_e32 v71, 0xffff0000, v64
	v_add_f32_e32 v2, v80, v81
	v_lshlrev_b32_e32 v64, 16, v65
	v_and_b32_e32 v65, 0xffff0000, v65
	v_add_f32_dpp v2, v2, v2 quad_perm:[1,0,3,2] row_mask:0xf bank_mask:0xf bound_ctrl:1
	v_lshlrev_b32_e32 v74, 16, v60
	v_and_b32_e32 v75, 0xffff0000, v60
	v_add_f32_dpp v2, v2, v2 quad_perm:[2,3,0,1] row_mask:0xf bank_mask:0xf bound_ctrl:1
	v_lshlrev_b32_e32 v60, 16, v61
	v_and_b32_e32 v61, 0xffff0000, v61
	v_add_f32_dpp v2, v2, v2 row_half_mirror row_mask:0xf bank_mask:0xf bound_ctrl:1
	v_lshlrev_b32_e32 v72, 16, v66
	v_and_b32_e32 v73, 0xffff0000, v66
	v_add_f32_dpp v2, v2, v2 row_mirror row_mask:0xf bank_mask:0xf bound_ctrl:1
	v_lshlrev_b32_e32 v76, 16, v62
	v_readlane_b32 s5, v2, 16
	v_readlane_b32 s7, v2, 48
	v_readlane_b32 s2, v2, 0
	v_readlane_b32 s3, v2, 32
	v_mov_b32_e32 v80, s5
	v_mov_b32_e32 v81, s7
	v_pk_add_f32 v[80:81], s[2:3], v[80:81]
	v_and_b32_e32 v77, 0xffff0000, v62
	v_add_f32_e32 v2, v80, v81
	v_fmamk_f32 v2, v2, 0x3a800000, v214
	v_lshlrev_b32_e32 v62, 16, v63
	v_and_b32_e32 v63, 0xffff0000, v63
	v_lshlrev_b32_e32 v66, 16, v67
	v_and_b32_e32 v67, 0xffff0000, v67
	v_rsq_f32_e32 v2, v2
	s_nop 0
	v_pk_mul_f32 v[56:57], v[2:3], v[56:57] op_sel_hi:[0,1]
	v_pk_mul_f32 v[78:79], v[2:3], v[78:79] op_sel_hi:[0,1]
	v_pk_fma_f32 v[64:65], v[10:11], v[56:57], v[64:65]
	v_mov_b32_e32 v56, v84
	v_mov_b32_e32 v57, v58
	v_pk_mul_f32 v[52:53], v[2:3], v[52:53] op_sel_hi:[0,1]
	v_mov_b32_e32 v69, v108
	v_pk_fma_f32 v[70:71], v[8:9], v[78:79], v[70:71]
	v_pk_mul_f32 v[56:57], v[2:3], v[56:57] op_sel_hi:[0,1]
	v_mov_b32_e32 v58, v85
	v_pk_fma_f32 v[60:61], v[18:19], v[52:53], v[60:61]
	v_pk_mul_f32 v[52:53], v[54:55], v[2:3] op_sel_hi:[1,0]
	v_pk_mul_f32 v[54:55], v[68:69], v[2:3] op_sel_hi:[1,0]
	v_pk_mul_f32 v[58:59], v[2:3], v[58:59] op_sel_hi:[0,1]
	v_pk_fma_f32 v[72:73], v[4:5], v[56:57], v[72:73]
	v_pk_mul_f32 v[56:57], v[2:3], v[88:89] op_sel_hi:[0,1]
	v_pk_fma_f32 v[68:69], v[12:13], v[54:55], v[76:77]
	v_pk_fma_f32 v[62:63], v[14:15], v[52:53], v[62:63]
	v_pk_mul_f32 v[52:53], v[64:65], v[64:65]
	v_pk_mul_f32 v[54:55], v[70:71], v[70:71]
	v_pk_fma_f32 v[66:67], v[6:7], v[58:59], v[66:67]
	v_pk_fma_f32 v[74:75], v[16:17], v[56:57], v[74:75]
	v_pk_mov_b32 v[56:57], v[54:55], v[52:53] op_sel:[1,0]
	v_mov_b32_e32 v55, v53
	v_pk_add_f32 v[52:53], v[56:57], v[54:55]
	v_pk_mul_f32 v[54:55], v[66:67], v[66:67]
	v_pk_mul_f32 v[56:57], v[72:73], v[72:73]
	v_mul_f32_e32 v2, v74, v74
	v_pk_mov_b32 v[58:59], v[56:57], v[54:55] op_sel:[1,0]
	v_mov_b32_e32 v57, v55
	v_pk_add_f32 v[54:55], v[58:59], v[56:57]
	v_pk_fma_f32 v[56:57], v[74:75], v[74:75], v[2:3] op_sel_hi:[1,1,0]
	v_mul_f32_e32 v2, v60, v60
	v_pk_add_f32 v[52:53], v[52:53], v[52:53] op_sel_hi:[0,1]
	v_pk_add_f32 v[54:55], v[54:55], v[54:55] op_sel_hi:[0,1]
	v_pk_fma_f32 v[58:59], v[60:61], v[60:61], v[2:3] op_sel_hi:[1,1,0]
	v_mul_f32_e32 v56, v68, v68
	v_mul_f32_e32 v58, v69, v69
	v_mul_f32_e32 v52, v62, v62
	v_mul_f32_e32 v54, v63, v63
	v_pk_add_f32 v[56:57], v[56:57], v[58:59]
	v_pk_add_f32 v[52:53], v[52:53], v[54:55]
	v_cvt_pk_bf16_f32 v58, v68, v69
	v_cvt_pk_bf16_f32 v59, v62, v63
	v_and_b32_e32 v80, 0xffff0000, v38
	v_pk_add_f32 v[52:53], v[56:57], v[52:53]
	v_cvt_pk_bf16_f32 v57, v60, v61
	s_nop 0
	v_add_f32_e32 v2, v52, v53
	s_nop 1
	v_add_f32_dpp v2, v2, v2 quad_perm:[1,0,3,2] row_mask:0xf bank_mask:0xf bound_ctrl:1
	s_nop 1
	v_add_f32_dpp v2, v2, v2 quad_perm:[2,3,0,1] row_mask:0xf bank_mask:0xf bound_ctrl:1
	s_nop 1
	v_add_f32_dpp v2, v2, v2 row_half_mirror row_mask:0xf bank_mask:0xf bound_ctrl:1
	s_nop 1
	v_add_f32_dpp v2, v2, v2 row_mirror row_mask:0xf bank_mask:0xf bound_ctrl:1
	s_nop 0
	v_readlane_b32 s5, v2, 16
	v_readlane_b32 s7, v2, 48
	v_readlane_b32 s2, v2, 0
	v_readlane_b32 s3, v2, 32
	v_mov_b32_e32 v52, s5
	v_mov_b32_e32 v53, s7
	v_pk_add_f32 v[52:53], s[2:3], v[52:53]
	s_nop 0
	v_add_f32_e32 v2, v52, v53
	v_fmamk_f32 v2, v2, 0x3a800000, v214
	s_mov_b32 s2, 0xb001000
	v_add_co_u32_e32 v76, vcc, s84, v120
	v_rsq_f32_e32 v2, v2
	s_nop 0
	v_cvt_pk_bf16_f32 v52, v70, v71
	v_cvt_pk_bf16_f32 v53, v64, v65
	v_cvt_pk_bf16_f32 v54, v72, v73
	v_cvt_pk_bf16_f32 v55, v66, v67
	s_nop 0
	v_addc_co_u32_e32 v77, vcc, 0, v121, vcc
	v_cvt_pk_bf16_f32 v56, v74, v75
	flat_store_dwordx4 v[76:77], v[52:55] sc1
	flat_store_dwordx4 v[76:77], v[56:59] offset:1024 sc1
	v_pk_mul_f32 v[62:63], v[62:63], v[2:3] op_sel_hi:[1,0]
	v_pk_mul_f32 v[52:53], v[70:71], v[2:3] op_sel_hi:[1,0]
	v_pk_mul_f32 v[54:55], v[64:65], v[2:3] op_sel_hi:[1,0]
	v_pk_mul_f32 v[58:59], v[66:67], v[2:3] op_sel_hi:[1,0]
	v_pk_mul_f32 v[54:55], v[26:27], v[54:55]
	v_pk_mul_f32 v[52:53], v[24:25], v[52:53]
	v_pk_mul_f32 v[56:57], v[72:73], v[2:3] op_sel_hi:[1,0]
	v_pk_mul_f32 v[58:59], v[22:23], v[58:59]
	v_pk_mul_f32 v[60:61], v[60:61], v[2:3] op_sel_hi:[1,0]
	v_pk_mul_f32 v[62:63], v[30:31], v[62:63]
	v_pk_mul_f32 v[56:57], v[20:21], v[56:57]
	v_pk_mul_f32 v[64:65], v[74:75], v[2:3] op_sel_hi:[1,0]
	v_pk_mul_f32 v[60:61], v[34:35], v[60:61]
	v_cvt_pk_bf16_f32 v52, v52, v53
; __device__ __forceinline__ void thin_pass(const Ctx& C, const bf16* hin, bf16* hout, bf16* u, float* out, const bf16* y, const float* gpost, float cmul, const float* gpre, bool last) {
;     ...
;         for (int b = 0; b < RB; ++b) {
;             const int m = m0 + b; const v4u y0 = yr[b][0], y1 = yr[b][1], h0 = hr[b][0], h1 = hr[b][1];
;             f32x4 yv[4], h[4];
;             yv[0] = (f32x4){bf_lo(y0.x), bf_hi(y0.x), bf_lo(y0.y), bf_hi(y0.y)}; yv[1] = (f32x4){bf_lo(y0.z), bf_hi(y0.z), bf_lo(y0.w), bf_hi(y0.w)};
;             yv[2] = (f32x4){bf_lo(y1.x), bf_hi(y1.x), bf_lo(y1.y), bf_hi(y1.y)}; yv[3] = (f32x4){bf_lo(y1.z), bf_hi(y1.z), bf_lo(y1.w), bf_hi(y1.w)};
;             h[0] = (f32x4){bf_lo(h0.x), bf_hi(h0.x), bf_lo(h0.y), bf_hi(h0.y)}; h[1] = (f32x4){bf_lo(h0.z), bf_hi(h0.z), bf_lo(h0.w), bf_hi(h0.w)};
;             h[2] = (f32x4){bf_lo(h1.x), bf_hi(h1.x), bf_lo(h1.y), bf_hi(h1.y)}; h[3] = (f32x4){bf_lo(h1.z), bf_hi(h1.z), bf_lo(h1.w), bf_hi(h1.w)};
;             float ss = 0.f;
; #pragma unroll
;             for (int i = 0; i < 4; ++i) ss += (yv[i][0] * yv[i][0] + yv[i][1] * yv[i][1]) + (yv[i][2] * yv[i][2] + yv[i][3] * yv[i][3]);
;             const float ry = cmul / sqrtf(wave_sum(ss) * (1.0f / D) + RMS_EPS);
; #pragma unroll
;             for (int i = 0; i < 4; ++i) h[i] = h[i] + yv[i] * ry * g4[i];
;             if (last) { f32x4* op = (f32x4*)(out + (size_t)m * D); op[2 * lane] = h[0]; op[2 * lane + 1] = h[1]; op[128 + 2 * lane] = h[2]; op[128 + 2 * lane + 1] = h[3]; }
;             else {
;                 float s2 = 0.f;
; #pragma unroll
;                 for (int i = 0; i < 4; ++i) s2 += (h[i][0] * h[i][0] + h[i][1] * h[i][1]) + (h[i][2] * h[i][2] + h[i][3] * h[i][3]);
;                 const float rh = 1.0f / sqrtf(wave_sum(s2) * (1.0f / D) + RMS_EPS);
;                 v4u o0, o1; o0.x = pk2(h[0][0], h[0][1]); o0.y = pk2(h[0][2], h[0][3]); o0.z = pk2(h[1][0], h[1][1]); o0.w = pk2(h[1][2], h[1][3]);
;                 o1.x = pk2(h[2][0], h[2][1]); o1.y = pk2(h[2][2], h[2][3]); o1.z = pk2(h[3][0], h[3][1]); o1.w = pk2(h[3][2], h[3][3]);
;                 v4u* hp = (v4u*)(hout + (size_t)m * D); hp[lane] = o0; hp[64 + lane] = o1;
; #pragma unroll
;                 for (int i = 0; i < 4; ++i) h[i] = h[i] * rh * q4[i];
	v_cvt_pk_bf16_f32 v53, v54, v55
	v_cvt_pk_bf16_f32 v55, v58, v59
	v_cvt_pk_bf16_f32 v59, v62, v63
	v_lshlrev_b32_e32 v62, 16, v40
	v_pk_mul_f32 v[64:65], v[32:33], v[64:65]
	v_pk_mul_f32 v[66:67], v[68:69], v[2:3] op_sel_hi:[1,0]
	v_cvt_pk_bf16_f32 v54, v56, v57
	v_cvt_pk_bf16_f32 v57, v60, v61
	v_add_co_u32_e32 v60, vcc, s2, v102
	v_and_b32_e32 v63, 0xffff0000, v40
	v_mul_f32_e32 v2, v62, v62
	v_lshlrev_b32_e32 v40, 16, v41
	v_pk_mul_f32 v[66:67], v[28:29], v[66:67]
	v_cvt_pk_bf16_f32 v56, v64, v65
	v_addc_co_u32_e32 v61, vcc, 0, v103, vcc
	v_pk_fma_f32 v[64:65], v[62:63], v[62:63], v[2:3] op_sel_hi:[1,1,0]
	v_and_b32_e32 v41, 0xffff0000, v41
	v_mul_f32_e32 v2, v40, v40
	v_lshlrev_b32_e32 v69, 16, v43
	v_lshlrev_b32_e32 v68, 16, v42
	v_and_b32_e32 v43, 0xffff0000, v43
	v_and_b32_e32 v42, 0xffff0000, v42
	v_lshlrev_b32_e32 v72, 16, v36
	v_cvt_pk_bf16_f32 v58, v66, v67
	flat_store_dwordx4 v[60:61], v[52:55] sc1
	flat_store_dwordx4 v[60:61], v[56:59] offset:1024 sc1
	v_pk_fma_f32 v[66:67], v[40:41], v[40:41], v[2:3] op_sel_hi:[1,1,0]
	v_lshlrev_b32_e32 v52, 16, v38
	v_pk_mul_f32 v[70:71], v[42:43], v[42:43]
	v_and_b32_e32 v73, 0xffff0000, v36
	v_mul_f32_e32 v2, v72, v72
	v_lshlrev_b32_e32 v36, 16, v37
	v_pk_fma_f32 v[70:71], v[68:69], v[68:69], v[70:71]
	v_pk_fma_f32 v[74:75], v[72:73], v[72:73], v[2:3] op_sel_hi:[1,1,0]
	v_and_b32_e32 v37, 0xffff0000, v37
	v_mul_f32_e32 v2, v36, v36
	v_mov_b32_e32 v53, v65
	v_mov_b32_e32 v78, v52
	v_mov_b32_e32 v79, v67
	v_lshlrev_b32_e32 v38, 16, v39
	v_and_b32_e32 v39, 0xffff0000, v39
	v_pk_add_f32 v[70:71], v[70:71], v[70:71] op_sel_hi:[0,1]
	v_pk_fma_f32 v[76:77], v[36:37], v[36:37], v[2:3] op_sel_hi:[1,1,0]
	v_pk_mul_f32 v[78:79], v[52:53], v[78:79]
	v_pk_add_f32 v[64:65], v[64:65], v[66:67]
	v_mul_f32_e32 v70, v80, v80
	v_mul_f32_e32 v74, v38, v38
	v_mul_f32_e32 v76, v39, v39
	v_mov_b32_e32 v79, v65
	v_pk_add_f32 v[64:65], v[78:79], v[70:71]
	v_pk_add_f32 v[66:67], v[74:75], v[76:77]
	v_lshlrev_b32_e32 v54, 16, v48
	v_pk_add_f32 v[64:65], v[64:65], v[66:67]
	v_and_b32_e32 v55, 0xffff0000, v48
	v_add_f32_e32 v2, v64, v65
	v_lshlrev_b32_e32 v48, 16, v49
	v_and_b32_e32 v49, 0xffff0000, v49
	v_add_f32_dpp v2, v2, v2 quad_perm:[1,0,3,2] row_mask:0xf bank_mask:0xf bound_ctrl:1
	v_lshlrev_b32_e32 v58, 16, v44
	v_and_b32_e32 v59, 0xffff0000, v44
	v_add_f32_dpp v2, v2, v2 quad_perm:[2,3,0,1] row_mask:0xf bank_mask:0xf bound_ctrl:1
	v_lshlrev_b32_e32 v44, 16, v45
	v_and_b32_e32 v45, 0xffff0000, v45
	v_add_f32_dpp v2, v2, v2 row_half_mirror row_mask:0xf bank_mask:0xf bound_ctrl:1
	v_lshlrev_b32_e32 v56, 16, v50
	v_and_b32_e32 v57, 0xffff0000, v50
	v_add_f32_dpp v2, v2, v2 row_mirror row_mask:0xf bank_mask:0xf bound_ctrl:1
	v_lshlrev_b32_e32 v50, 16, v51
	v_readlane_b32 s5, v2, 16
	v_readlane_b32 s7, v2, 48
	v_readlane_b32 s2, v2, 0
	v_readlane_b32 s3, v2, 32
	v_mov_b32_e32 v64, s5
	v_mov_b32_e32 v65, s7
	v_pk_add_f32 v[64:65], s[2:3], v[64:65]
	v_and_b32_e32 v51, 0xffff0000, v51
	v_add_f32_e32 v2, v64, v65
	v_fmamk_f32 v2, v2, 0x3a800000, v214
	v_lshlrev_b32_e32 v60, 16, v46
	v_and_b32_e32 v61, 0xffff0000, v46
	v_lshlrev_b32_e32 v46, 16, v47
	v_and_b32_e32 v47, 0xffff0000, v47
	v_rsq_f32_e32 v2, v2
	s_nop 0
	v_pk_mul_f32 v[40:41], v[2:3], v[40:41] op_sel_hi:[0,1]
	v_pk_mul_f32 v[62:63], v[2:3], v[62:63] op_sel_hi:[0,1]
	v_pk_fma_f32 v[48:49], v[10:11], v[40:41], v[48:49]
	v_mov_b32_e32 v40, v69
	v_mov_b32_e32 v41, v43
	v_pk_mul_f32 v[36:37], v[2:3], v[36:37] op_sel_hi:[0,1]
	v_mov_b32_e32 v53, v80
	v_pk_fma_f32 v[54:55], v[8:9], v[62:63], v[54:55]
	v_pk_mul_f32 v[40:41], v[2:3], v[40:41] op_sel_hi:[0,1]
	v_mov_b32_e32 v69, v42
	v_pk_fma_f32 v[44:45], v[18:19], v[36:37], v[44:45]
	v_pk_mul_f32 v[36:37], v[38:39], v[2:3] op_sel_hi:[1,0]
; __device__ __forceinline__ void thin_pass(const Ctx& C, const bf16* hin, bf16* hout, bf16* u, float* out, const bf16* y, const float* gpost, float cmul, const float* gpre, bool last) {
;     ...
;         for (int b = 0; b < RB; ++b) {
;             const int m = m0 + b; const v4u y0 = yr[b][0], y1 = yr[b][1], h0 = hr[b][0], h1 = hr[b][1];
;             f32x4 yv[4], h[4];
;             yv[0] = (f32x4){bf_lo(y0.x), bf_hi(y0.x), bf_lo(y0.y), bf_hi(y0.y)}; yv[1] = (f32x4){bf_lo(y0.z), bf_hi(y0.z), bf_lo(y0.w), bf_hi(y0.w)};
;             yv[2] = (f32x4){bf_lo(y1.x), bf_hi(y1.x), bf_lo(y1.y), bf_hi(y1.y)}; yv[3] = (f32x4){bf_lo(y1.z), bf_hi(y1.z), bf_lo(y1.w), bf_hi(y1.w)};
;             h[0] = (f32x4){bf_lo(h0.x), bf_hi(h0.x), bf_lo(h0.y), bf_hi(h0.y)}; h[1] = (f32x4){bf_lo(h0.z), bf_hi(h0.z), bf_lo(h0.w), bf_hi(h0.w)};
;             h[2] = (f32x4){bf_lo(h1.x), bf_hi(h1.x), bf_lo(h1.y), bf_hi(h1.y)}; h[3] = (f32x4){bf_lo(h1.z), bf_hi(h1.z), bf_lo(h1.w), bf_hi(h1.w)};
;             float ss = 0.f;
; #pragma unroll
;             for (int i = 0; i < 4; ++i) ss += (yv[i][0] * yv[i][0] + yv[i][1] * yv[i][1]) + (yv[i][2] * yv[i][2] + yv[i][3] * yv[i][3]);
;             const float ry = cmul / sqrtf(wave_sum(ss) * (1.0f / D) + RMS_EPS);
; #pragma unroll
;             for (int i = 0; i < 4; ++i) h[i] = h[i] + yv[i] * ry * g4[i];
;             if (last) { f32x4* op = (f32x4*)(out + (size_t)m * D); op[2 * lane] = h[0]; op[2 * lane + 1] = h[1]; op[128 + 2 * lane] = h[2]; op[128 + 2 * lane + 1] = h[3]; }
;             else {
;                 float s2 = 0.f;
; #pragma unroll
;                 for (int i = 0; i < 4; ++i) s2 += (h[i][0] * h[i][0] + h[i][1] * h[i][1]) + (h[i][2] * h[i][2] + h[i][3] * h[i][3]);
;                 const float rh = 1.0f / sqrtf(wave_sum(s2) * (1.0f / D) + RMS_EPS);
;                 v4u o0, o1; o0.x = pk2(h[0][0], h[0][1]); o0.y = pk2(h[0][2], h[0][3]); o0.z = pk2(h[1][0], h[1][1]); o0.w = pk2(h[1][2], h[1][3]);
;                 o1.x = pk2(h[2][0], h[2][1]); o1.y = pk2(h[2][2], h[2][3]); o1.z = pk2(h[3][0], h[3][1]); o1.w = pk2(h[3][2], h[3][3]);
;                 v4u* hp = (v4u*)(hout + (size_t)m * D); hp[lane] = o0; hp[64 + lane] = o1;
; #pragma unroll
;                 for (int i = 0; i < 4; ++i) h[i] = h[i] * rh * q4[i];
	v_pk_mul_f32 v[38:39], v[52:53], v[2:3] op_sel_hi:[1,0]
	v_pk_mul_f32 v[42:43], v[2:3], v[68:69] op_sel_hi:[0,1]
	v_pk_fma_f32 v[50:51], v[6:7], v[40:41], v[50:51]
	v_pk_mul_f32 v[40:41], v[2:3], v[72:73] op_sel_hi:[0,1]
	v_pk_fma_f32 v[52:53], v[12:13], v[38:39], v[60:61]
	v_pk_fma_f32 v[46:47], v[14:15], v[36:37], v[46:47]
	v_pk_mul_f32 v[36:37], v[48:49], v[48:49]
	v_pk_mul_f32 v[38:39], v[54:55], v[54:55]
	v_pk_fma_f32 v[56:57], v[4:5], v[42:43], v[56:57]
	v_pk_fma_f32 v[58:59], v[16:17], v[40:41], v[58:59]
	v_pk_mov_b32 v[40:41], v[38:39], v[36:37] op_sel:[1,0]
	v_mov_b32_e32 v39, v37
	v_pk_add_f32 v[36:37], v[40:41], v[38:39]
	v_pk_mul_f32 v[38:39], v[50:51], v[50:51]
	v_pk_mul_f32 v[40:41], v[56:57], v[56:57]
	v_mul_f32_e32 v2, v58, v58
	v_pk_mov_b32 v[42:43], v[40:41], v[38:39] op_sel:[1,0]
	v_mov_b32_e32 v41, v39
	v_pk_add_f32 v[38:39], v[42:43], v[40:41]
	v_pk_fma_f32 v[40:41], v[58:59], v[58:59], v[2:3] op_sel_hi:[1,1,0]
	v_mul_f32_e32 v2, v44, v44
	v_pk_add_f32 v[36:37], v[36:37], v[36:37] op_sel_hi:[0,1]
	v_pk_add_f32 v[38:39], v[38:39], v[38:39] op_sel_hi:[0,1]
	v_pk_fma_f32 v[42:43], v[44:45], v[44:45], v[2:3] op_sel_hi:[1,1,0]
	v_mul_f32_e32 v40, v52, v52
	v_mul_f32_e32 v42, v53, v53
	v_mul_f32_e32 v36, v46, v46
	v_mul_f32_e32 v38, v47, v47
	v_pk_add_f32 v[40:41], v[40:41], v[42:43]
	v_pk_add_f32 v[36:37], v[36:37], v[38:39]
	v_lshl_add_u64 v[60:61], v[98:99], 0, s[16:17]
	v_pk_add_f32 v[36:37], v[40:41], v[36:37]
	v_cvt_pk_bf16_f32 v41, v44, v45
	v_cvt_pk_bf16_f32 v42, v52, v53
	v_cvt_pk_bf16_f32 v43, v46, v47
	s_nop 0
	v_add_f32_e32 v2, v36, v37
	s_nop 1
	v_add_f32_dpp v2, v2, v2 quad_perm:[1,0,3,2] row_mask:0xf bank_mask:0xf bound_ctrl:1
	s_nop 1
	v_add_f32_dpp v2, v2, v2 quad_perm:[2,3,0,1] row_mask:0xf bank_mask:0xf bound_ctrl:1
	s_nop 1
	v_add_f32_dpp v2, v2, v2 row_half_mirror row_mask:0xf bank_mask:0xf bound_ctrl:1
	s_nop 1
	v_add_f32_dpp v2, v2, v2 row_mirror row_mask:0xf bank_mask:0xf bound_ctrl:1
	s_nop 0
	v_readlane_b32 s5, v2, 16
	v_readlane_b32 s7, v2, 48
	v_readlane_b32 s2, v2, 0
	v_readlane_b32 s3, v2, 32
	v_mov_b32_e32 v36, s5
	v_mov_b32_e32 v37, s7
	v_pk_add_f32 v[36:37], s[2:3], v[36:37]
	s_nop 0
	v_add_f32_e32 v2, v36, v37
	v_fmamk_f32 v2, v2, 0x3a800000, v214
	v_rsq_f32_e32 v2, v2
	s_nop 0
	v_cvt_pk_bf16_f32 v36, v54, v55
	v_cvt_pk_bf16_f32 v37, v48, v49
	v_cvt_pk_bf16_f32 v38, v56, v57
	v_cvt_pk_bf16_f32 v39, v50, v51
	v_cvt_pk_bf16_f32 v40, v58, v59
	flat_store_dwordx4 v[60:61], v[36:39] sc1
	flat_store_dwordx4 v[60:61], v[40:43] offset:1024 sc1
	v_pk_mul_f32 v[44:45], v[44:45], v[2:3] op_sel_hi:[1,0]
	v_pk_mul_f32 v[36:37], v[54:55], v[2:3] op_sel_hi:[1,0]
	v_pk_mul_f32 v[38:39], v[48:49], v[2:3] op_sel_hi:[1,0]
	v_pk_mul_f32 v[40:41], v[56:57], v[2:3] op_sel_hi:[1,0]
	v_pk_mul_f32 v[38:39], v[26:27], v[38:39]
	v_pk_mul_f32 v[36:37], v[24:25], v[36:37]
	v_pk_mul_f32 v[42:43], v[50:51], v[2:3] op_sel_hi:[1,0]
	v_pk_mul_f32 v[40:41], v[20:21], v[40:41]
	v_pk_mul_f32 v[44:45], v[34:35], v[44:45]
	v_pk_mul_f32 v[42:43], v[22:23], v[42:43]
	v_pk_mul_f32 v[48:49], v[58:59], v[2:3] op_sel_hi:[1,0]
	v_pk_mul_f32 v[50:51], v[52:53], v[2:3] op_sel_hi:[1,0]
	v_pk_mul_f32 v[46:47], v[46:47], v[2:3] op_sel_hi:[1,0]
	v_cvt_pk_bf16_f32 v36, v36, v37
	v_cvt_pk_bf16_f32 v37, v38, v39
	v_cvt_pk_bf16_f32 v38, v40, v41
	v_cvt_pk_bf16_f32 v39, v42, v43
	v_cvt_pk_bf16_f32 v41, v44, v45
	v_lshl_add_u64 v[44:45], v[100:101], 0, s[16:17]
	v_pk_mul_f32 v[48:49], v[32:33], v[48:49]
	v_pk_mul_f32 v[46:47], v[30:31], v[46:47]
	v_pk_mul_f32 v[50:51], v[28:29], v[50:51]
	v_cvt_pk_bf16_f32 v40, v48, v49
	v_cvt_pk_bf16_f32 v43, v46, v47
	s_nop 0
	v_cvt_pk_bf16_f32 v42, v50, v51
	flat_store_dwordx4 v[44:45], v[36:39] sc1
	flat_store_dwordx4 v[44:45], v[40:43] offset:1024 sc1
	s_cbranch_scc1 .LBB0_1757

; __device__ __forceinline__ unsigned xb_ld(unsigned* p)              { return __hip_atomic_load(p, __ATOMIC_RELAXED, __HIP_MEMORY_SCOPE_AGENT); }
; __device__ __forceinline__ unsigned xb_add(unsigned* p, unsigned v) { return __hip_atomic_fetch_add(p, v, __ATOMIC_RELAXED, __HIP_MEMORY_SCOPE_AGENT); }
; #define XB_SPIN(cond, bar) do { unsigned _sp = 0; while (cond) { __builtin_amdgcn_s_sleep(1); \
;     if ((++_sp & 255u) == 0u) { if (xb_ld(&(bar)[XB_TMO])) break; if (_sp > XB_SPIN_CAP) { atomicAdd(&(bar)[XB_TMO], 1u); break; } } } } while (0)
; __device__ __forceinline__ void xcd_barrier(const XcdBarrier& b) {
;     ...
;         const unsigned old = xb_add(&bar[XB_XSUB(b.x)], 1u);
;         const unsigned gen = old / nloc;
;         if (old + 1u == (gen + 1u) * nloc) {
;             __builtin_amdgcn_fence(__ATOMIC_RELEASE, "agent");
;             asm volatile("s_waitcnt vmcnt(0)" ::: "memory");
;             const unsigned og = xb_add(&bar[XB_TOP], 1u);
;             const unsigned tg = og / nx;
;             if (og + 1u == (tg + 1u) * nx) xb_add(&bar[XB_TOPGEN], 1u);
;             else XB_SPIN(xb_ld(&bar[XB_TOPGEN]) == tg, bar);
.LBB0_1787:
	s_andn2_saveexec_b64 s[2:3], s[2:3]
	s_cbranch_execz .LBB0_1803
	v_mov_b32_e32 v4, s34
	v_add_co_u32_e32 v4, vcc, 0x3000, v4
	v_mov_b32_e32 v5, s35
	s_waitcnt vmcnt(0)
	v_addc_co_u32_e32 v5, vcc, 0, v5, vcc
	flat_atomic_add v4, v[4:5], v1 offset:1024 sc0
	v_cvt_f32_u32_e32 v5, v2
	v_sub_u32_e32 v6, 0, v2
	s_mov_b64 s[6:7], -1
	v_rcp_iflag_f32_e32 v5, v5
	s_nop 0
	v_mul_f32_e32 v5, 0x4f7ffffe, v5
	v_cvt_u32_f32_e32 v5, v5
	v_mul_lo_u32 v6, v6, v5
	v_mul_hi_u32 v6, v5, v6
	v_add_u32_e32 v5, v5, v6
	s_waitcnt vmcnt(0) lgkmcnt(0)
	v_mul_hi_u32 v5, v4, v5
	v_mul_lo_u32 v6, v5, v2
	v_sub_u32_e32 v6, v4, v6
	v_cmp_ge_u32_e32 vcc, v6, v2
	v_add_u32_e32 v7, 1, v5
	s_nop 0
	v_cndmask_b32_e32 v5, v5, v7, vcc
	v_sub_u32_e32 v7, v6, v2
	v_cndmask_b32_e32 v6, v6, v7, vcc
	v_cmp_ge_u32_e32 vcc, v6, v2
	v_add_u32_e32 v6, 1, v5
	v_add_u32_e32 v7, 1, v4
	v_cndmask_b32_e32 v6, v5, v6, vcc
	v_mad_u64_u32 v[4:5], s[2:3], v2, v6, v[2:3]
	s_add_u32 s2, s34, 0x3500
	s_addc_u32 s3, s35, 0
	v_cmp_ne_u32_e32 vcc, v7, v4
	v_mov_b64_e32 v[4:5], s[2:3]
	s_and_saveexec_b64 s[4:5], vcc
	s_cbranch_execz .LBB0_1800
	v_mov_b64_e32 v[4:5], s[2:3]
	flat_load_dword v2, v[4:5] sc1
	s_mov_b64 s[10:11], 0
	s_waitcnt vmcnt(0) lgkmcnt(0)
	v_cmp_eq_u32_e32 vcc, v2, v6
	s_and_saveexec_b64 s[8:9], vcc
	s_cbranch_execz .LBB0_1799
	s_add_u32 s6, s34, 0x200
	s_addc_u32 s7, s35, 0
	s_mov_b32 s1, 1
	s_branch .LBB0_1792
